# GEMM K-loops: LDS-DMA issue without the M0 save/restore and hazard s_nop (the M0 write moved one SALU instruction earlier)
# baseline (speedup 1.0000x reference)
; #define PG8_STAGE(bufoff, gbase, voff) do { _Pragma("unroll") for (int _i = 0; _i < 2; ++_i) glds16_s((const void*)((const char*)(gbase) + _i * r64), (voff), ldsb + (unsigned)(bufoff) + ldsw + _i * 8192u); } while (0)
; #define PG8_LDA(b, h) do { _Pragma("unroll") for (int m = 0; m < 4; ++m) { const int o_ = PG8_SA(b, h) + aoff + m * 2048; \
;         if constexpr (FP8) A8[m] = PG8_CAT8(o_); else { At[m][0] = PG8_LD16(o_); At[m][1] = PG8_LD16(o_ + 1024); } } } while (0)
; #define PG8_LDB(X, X8, b, h) do { _Pragma("unroll") for (int n = 0; n < 2; ++n) { const int o_ = PG8_SB(b, h) + boff + n * 2048; \
;         if constexpr (FP8) X8[n] = PG8_CAT8(o_); else { X[n][0] = PG8_LD16(o_); X[n][1] = PG8_LD16(o_ + 1024); } } } while (0)
; #define PG8_WAIT_V(n) asm volatile("s_waitcnt vmcnt(" #n ")" ::: "memory")
; #define PG8_WAIT_L(n) asm volatile("s_waitcnt lgkmcnt(" #n ")" ::: "memory")
; #define PG8_BAR __builtin_amdgcn_s_barrier()
; #define PG8_SCHED __builtin_amdgcn_sched_barrier(0)
; #define PG8_HI do { if constexpr (FP8) asm volatile("s_setprio 1"); } while (0)
; #define PG8_LO do { if constexpr (FP8) asm volatile("s_setprio 0"); } while (0)
; template <class Epi, class Sched, bool FP8 = false>
; __device__ __forceinline__ void gemm_phase(LAS unsigned char* lds, const int Kb, const int nt  , const Sched& S, const Epi& E) {
;     ...
;         for (int t = 0; t < nt; t += 2) {
;             const bool last = (t == nt - 2);
;             const char* a1 = cA + (size_t)(t + 1) * kstep;
;             const char* a2 = last ? nA : cA + (size_t)(t + 2) * kstep; const char* b2 = last ? nB : cB + (size_t)(t + 2) * kstep;
;             const char* a3 = a2 + kstep; const char* b3 = b2 + kstep;
;             PG8_LDB(B0, B08, 0, 0); PG8_SCHED; PG8_LDA(0, 0); PG8_STAGE(PG8_SA(1, 1), a1 + hstep, voffA);
;             PG8_WAIT_L(8); PG8_BAR; PG8_HI; PG8_WAIT_L(0); PG8_MMA(0, 0, B0, B08); PG8_BAR; PG8_LO; PG8_SCHED;
;             PG8_LDB(B1, B18, 0, 1); PG8_STAGE(PG8_SB(0, 0), b2, voffB);
;             PG8_BAR; PG8_HI; PG8_WAIT_L(0); PG8_MMA(0, 1, B1, B18); PG8_BAR; PG8_LO;
;             PG8_LDA(0, 1); PG8_STAGE(PG8_SA(0, 0), a2, voffA);
;             PG8_BAR; PG8_HI; PG8_WAIT_L(0); PG8_MMA(1, 0, B0, B08); PG8_BAR; PG8_LO; PG8_SCHED;
;             PG8_STAGE(PG8_SB(0, 1), b2 + hstep, voffB);
;             PG8_WAIT_V(6); PG8_BAR; PG8_HI; PG8_MMA(1, 1, B1, B18); PG8_BAR; PG8_LO;
.LBB0_299:
	ds_read_b128 v[132:135], v148
	ds_read_b128 v[136:139], v149
	ds_read_b128 v[140:143], v150
	ds_read_b128 v[166:169], v151
	s_add_u32 s22, s20, 0x100
	s_addc_u32 s23, s21, 0
	s_cmp_eq_u32 s59, 28
	s_cselect_b32 s26, s16, s22
	s_cselect_b32 s27, s17, s23
	s_cselect_b32 s24, s18, s13
	s_cselect_b32 s25, s19, s58
	s_add_u32 s28, s26, 0x80
	s_addc_u32 s29, s27, 0
	ds_read_b128 v[170:173], v164
	ds_read_b128 v[174:177], v164 offset:1024
	ds_read_b128 v[178:181], v164 offset:2048
	ds_read_b128 v[182:185], v164 offset:3072
	ds_read_b128 v[186:189], v164 offset:4096
	ds_read_b128 v[190:193], v164 offset:5120
	ds_read_b128 v[194:197], v164 offset:6144
	ds_read_b128 v[198:201], v164 offset:7168
	s_add_u32 s60, s20, 0x80080
	s_mov_b32 m0, s52
	s_addc_u32 s61, s21, 0
	global_load_lds_dwordx4 v1, s[60:61]
	s_add_u32 s20, s20, 0xc0080
	s_mov_b32 m0, s53
	s_addc_u32 s21, s21, 0
	global_load_lds_dwordx4 v1, s[20:21]
	s_waitcnt lgkmcnt(8)
	s_barrier
	s_waitcnt lgkmcnt(0)
	s_setprio 1
	v_mfma_f32_16x16x32_bf16 v[126:129], v[132:135], v[170:173], v[126:129]
	v_mfma_f32_16x16x32_bf16 v[122:125], v[140:143], v[170:173], v[122:125]
	v_mfma_f32_16x16x32_bf16 v[110:113], v[132:135], v[178:181], v[110:113]
	v_mfma_f32_16x16x32_bf16 v[106:109], v[140:143], v[178:181], v[106:109]
	v_mfma_f32_16x16x32_bf16 v[94:97], v[132:135], v[186:189], v[94:97]
	v_mfma_f32_16x16x32_bf16 v[90:93], v[140:143], v[186:189], v[90:93]
	v_mfma_f32_16x16x32_bf16 v[78:81], v[132:135], v[194:197], v[78:81]
	v_mfma_f32_16x16x32_bf16 v[74:77], v[140:143], v[194:197], v[74:77]
	v_mfma_f32_16x16x32_bf16 v[126:129], v[136:139], v[174:177], v[126:129]
	v_mfma_f32_16x16x32_bf16 v[122:125], v[166:169], v[174:177], v[122:125]
	v_mfma_f32_16x16x32_bf16 v[110:113], v[136:139], v[182:185], v[110:113]
	v_mfma_f32_16x16x32_bf16 v[106:109], v[166:169], v[182:185], v[106:109]
	v_mfma_f32_16x16x32_bf16 v[94:97], v[136:139], v[190:193], v[94:97]
	v_mfma_f32_16x16x32_bf16 v[90:93], v[166:169], v[190:193], v[90:93]
	v_mfma_f32_16x16x32_bf16 v[78:81], v[136:139], v[198:201], v[78:81]
	v_mfma_f32_16x16x32_bf16 v[74:77], v[166:169], v[198:201], v[74:77]
	s_setprio 0
	s_barrier
	ds_read_b128 v[202:205], v152
	ds_read_b128 v[206:209], v153
	ds_read_b128 v[210:213], v154
	s_mov_b32 m0, s37
	ds_read_b128 v[214:217], v155
	global_load_lds_dwordx4 v147, s[24:25]
	s_add_u32 s20, s24, 0x40000
	s_mov_b32 m0, s38
	s_addc_u32 s21, s25, 0
	global_load_lds_dwordx4 v147, s[20:21]
	s_barrier
	s_waitcnt lgkmcnt(0)
	s_setprio 1
	v_mfma_f32_16x16x32_bf16 v[118:121], v[202:205], v[170:173], v[118:121]
	v_mfma_f32_16x16x32_bf16 v[114:117], v[210:213], v[170:173], v[114:117]
	v_mfma_f32_16x16x32_bf16 v[102:105], v[202:205], v[178:181], v[102:105]
	v_mfma_f32_16x16x32_bf16 v[98:101], v[210:213], v[178:181], v[98:101]
	v_mfma_f32_16x16x32_bf16 v[86:89], v[202:205], v[186:189], v[86:89]
	v_mfma_f32_16x16x32_bf16 v[82:85], v[210:213], v[186:189], v[82:85]
	v_mfma_f32_16x16x32_bf16 v[70:73], v[202:205], v[194:197], v[70:73]
	v_mfma_f32_16x16x32_bf16 v[66:69], v[210:213], v[194:197], v[66:69]
	v_mfma_f32_16x16x32_bf16 v[118:121], v[206:209], v[174:177], v[118:121]
	v_mfma_f32_16x16x32_bf16 v[114:117], v[214:217], v[174:177], v[114:117]
	v_mfma_f32_16x16x32_bf16 v[102:105], v[206:209], v[182:185], v[102:105]
	v_mfma_f32_16x16x32_bf16 v[98:101], v[214:217], v[182:185], v[98:101]
	v_mfma_f32_16x16x32_bf16 v[86:89], v[206:209], v[190:193], v[86:89]
	v_mfma_f32_16x16x32_bf16 v[82:85], v[214:217], v[190:193], v[82:85]
	v_mfma_f32_16x16x32_bf16 v[70:73], v[206:209], v[198:201], v[70:73]
	v_mfma_f32_16x16x32_bf16 v[66:69], v[214:217], v[198:201], v[66:69]
	s_setprio 0
	s_barrier
	ds_read_b128 v[170:173], v164 offset:16384
	ds_read_b128 v[174:177], v164 offset:17408
	ds_read_b128 v[178:181], v164 offset:18432
	ds_read_b128 v[182:185], v164 offset:19456
	ds_read_b128 v[186:189], v164 offset:20480
	ds_read_b128 v[190:193], v164 offset:21504
	ds_read_b128 v[194:197], v164 offset:22528
	s_mov_b32 m0, s36
	ds_read_b128 v[198:201], v164 offset:23552
	global_load_lds_dwordx4 v1, s[26:27]
	s_add_u32 s20, s26, 0x40000
	s_mov_b32 m0, s39
	s_addc_u32 s21, s27, 0
	global_load_lds_dwordx4 v1, s[20:21]
	s_barrier
	s_waitcnt lgkmcnt(0)
	s_setprio 1
	v_mfma_f32_16x16x32_bf16 v[62:65], v[132:135], v[170:173], v[62:65]
	v_mfma_f32_16x16x32_bf16 v[58:61], v[140:143], v[170:173], v[58:61]
	v_mfma_f32_16x16x32_bf16 v[46:49], v[132:135], v[178:181], v[46:49]
	v_mfma_f32_16x16x32_bf16 v[42:45], v[140:143], v[178:181], v[42:45]
	v_mfma_f32_16x16x32_bf16 v[30:33], v[132:135], v[186:189], v[30:33]
	v_mfma_f32_16x16x32_bf16 v[26:29], v[140:143], v[186:189], v[26:29]
	v_mfma_f32_16x16x32_bf16 v[14:17], v[132:135], v[194:197], v[14:17]
	v_mfma_f32_16x16x32_bf16 v[10:13], v[140:143], v[194:197], v[10:13]
	v_mfma_f32_16x16x32_bf16 v[62:65], v[136:139], v[174:177], v[62:65]
	v_mfma_f32_16x16x32_bf16 v[58:61], v[166:169], v[174:177], v[58:61]
	v_mfma_f32_16x16x32_bf16 v[46:49], v[136:139], v[182:185], v[46:49]
	v_mfma_f32_16x16x32_bf16 v[42:45], v[166:169], v[182:185], v[42:45]
	v_mfma_f32_16x16x32_bf16 v[30:33], v[136:139], v[190:193], v[30:33]
	v_mfma_f32_16x16x32_bf16 v[26:29], v[166:169], v[190:193], v[26:29]
	v_mfma_f32_16x16x32_bf16 v[14:17], v[136:139], v[198:201], v[14:17]
	v_mfma_f32_16x16x32_bf16 v[10:13], v[166:169], v[198:201], v[10:13]
	s_setprio 0
	s_barrier
	s_add_u32 s20, s24, 0x80000
	s_mov_b32 m0, s40
	s_addc_u32 s21, s25, 0
	global_load_lds_dwordx4 v147, s[20:21]
	s_add_u32 s20, s24, 0xc0000
	s_mov_b32 m0, s41
	s_addc_u32 s21, s25, 0
	global_load_lds_dwordx4 v147, s[20:21]
	s_waitcnt vmcnt(6)
	s_barrier
; #define PG8_STAGE(bufoff, gbase, voff) do { _Pragma("unroll") for (int _i = 0; _i < 2; ++_i) glds16_s((const void*)((const char*)(gbase) + _i * r64), (voff), ldsb + (unsigned)(bufoff) + ldsw + _i * 8192u); } while (0)
; #define PG8_LDA(b, h) do { _Pragma("unroll") for (int m = 0; m < 4; ++m) { const int o_ = PG8_SA(b, h) + aoff + m * 2048; \
;         if constexpr (FP8) A8[m] = PG8_CAT8(o_); else { At[m][0] = PG8_LD16(o_); At[m][1] = PG8_LD16(o_ + 1024); } } } while (0)
; #define PG8_LDB(X, X8, b, h) do { _Pragma("unroll") for (int n = 0; n < 2; ++n) { const int o_ = PG8_SB(b, h) + boff + n * 2048; \
;         if constexpr (FP8) X8[n] = PG8_CAT8(o_); else { X[n][0] = PG8_LD16(o_); X[n][1] = PG8_LD16(o_ + 1024); } } } while (0)
; #define PG8_WAIT_V(n) asm volatile("s_waitcnt vmcnt(" #n ")" ::: "memory")
; #define PG8_WAIT_L(n) asm volatile("s_waitcnt lgkmcnt(" #n ")" ::: "memory")
; #define PG8_BAR __builtin_amdgcn_s_barrier()
; #define PG8_SCHED __builtin_amdgcn_sched_barrier(0)
; #define PG8_HI do { if constexpr (FP8) asm volatile("s_setprio 1"); } while (0)
; #define PG8_LO do { if constexpr (FP8) asm volatile("s_setprio 0"); } while (0)
; template <class Epi, class Sched, bool FP8 = false>
; __device__ __forceinline__ void gemm_phase(LAS unsigned char* lds, const int Kb, const int nt  , const Sched& S, const Epi& E) {
;     ...
;             PG8_WAIT_V(6); PG8_BAR; PG8_HI; PG8_MMA(1, 1, B1, B18); PG8_BAR; PG8_LO;
;             PG8_LDB(B0, B08, 1, 0); PG8_SCHED; PG8_LDA(1, 0); PG8_STAGE(PG8_SA(0, 1), a2 + hstep, voffA);
;             PG8_WAIT_L(8); PG8_BAR; PG8_HI; PG8_WAIT_L(0); PG8_MMA(0, 0, B0, B08); PG8_BAR; PG8_LO; PG8_SCHED;
;             PG8_LDB(B1, B18, 1, 1); PG8_STAGE(PG8_SB(1, 0), b3, voffB);
;             PG8_BAR; PG8_HI; PG8_WAIT_L(0); PG8_MMA(0, 1, B1, B18); PG8_BAR; PG8_LO;
	s_setprio 1
	v_mfma_f32_16x16x32_bf16 v[54:57], v[202:205], v[170:173], v[54:57]
	v_mfma_f32_16x16x32_bf16 v[50:53], v[210:213], v[170:173], v[50:53]
	v_mfma_f32_16x16x32_bf16 v[38:41], v[202:205], v[178:181], v[38:41]
	v_mfma_f32_16x16x32_bf16 v[34:37], v[210:213], v[178:181], v[34:37]
	v_mfma_f32_16x16x32_bf16 v[22:25], v[202:205], v[186:189], v[22:25]
	v_mfma_f32_16x16x32_bf16 v[18:21], v[210:213], v[186:189], v[18:21]
	v_mfma_f32_16x16x32_bf16 v[6:9], v[202:205], v[194:197], v[6:9]
	v_mfma_f32_16x16x32_bf16 v[2:5], v[210:213], v[194:197], v[2:5]
	v_mfma_f32_16x16x32_bf16 v[54:57], v[206:209], v[174:177], v[54:57]
	v_mfma_f32_16x16x32_bf16 v[50:53], v[214:217], v[174:177], v[50:53]
	v_mfma_f32_16x16x32_bf16 v[38:41], v[206:209], v[182:185], v[38:41]
	v_mfma_f32_16x16x32_bf16 v[34:37], v[214:217], v[182:185], v[34:37]
	v_mfma_f32_16x16x32_bf16 v[22:25], v[206:209], v[190:193], v[22:25]
	v_mfma_f32_16x16x32_bf16 v[18:21], v[214:217], v[190:193], v[18:21]
	v_mfma_f32_16x16x32_bf16 v[6:9], v[206:209], v[198:201], v[6:9]
	v_mfma_f32_16x16x32_bf16 v[2:5], v[214:217], v[198:201], v[2:5]
	s_setprio 0
	s_barrier
	ds_read_b128 v[132:135], v156
	ds_read_b128 v[136:139], v157
	ds_read_b128 v[140:143], v158
	ds_read_b128 v[166:169], v159
	ds_read_b128 v[170:173], v164 offset:32768
	ds_read_b128 v[174:177], v164 offset:33792
	ds_read_b128 v[178:181], v164 offset:34816
	ds_read_b128 v[182:185], v164 offset:35840
	ds_read_b128 v[186:189], v164 offset:36864
	ds_read_b128 v[190:193], v164 offset:37888
	ds_read_b128 v[194:197], v164 offset:38912
	ds_read_b128 v[198:201], v164 offset:39936
	s_add_u32 s20, s26, 0x80000
	s_mov_b32 m0, s42
	s_addc_u32 s21, s27, 0
	global_load_lds_dwordx4 v1, s[20:21]
	s_add_u32 s20, s26, 0xc0000
	s_mov_b32 m0, s43
	s_addc_u32 s21, s27, 0
	global_load_lds_dwordx4 v1, s[20:21]
	s_waitcnt lgkmcnt(8)
	s_barrier
	s_waitcnt lgkmcnt(0)
	s_setprio 1
	v_mfma_f32_16x16x32_bf16 v[126:129], v[132:135], v[170:173], v[126:129]
	v_mfma_f32_16x16x32_bf16 v[122:125], v[140:143], v[170:173], v[122:125]
	v_mfma_f32_16x16x32_bf16 v[110:113], v[132:135], v[178:181], v[110:113]
	v_mfma_f32_16x16x32_bf16 v[106:109], v[140:143], v[178:181], v[106:109]
	v_mfma_f32_16x16x32_bf16 v[94:97], v[132:135], v[186:189], v[94:97]
	v_mfma_f32_16x16x32_bf16 v[90:93], v[140:143], v[186:189], v[90:93]
	v_mfma_f32_16x16x32_bf16 v[78:81], v[132:135], v[194:197], v[78:81]
	v_mfma_f32_16x16x32_bf16 v[74:77], v[140:143], v[194:197], v[74:77]
	v_mfma_f32_16x16x32_bf16 v[126:129], v[136:139], v[174:177], v[126:129]
	v_mfma_f32_16x16x32_bf16 v[122:125], v[166:169], v[174:177], v[122:125]
	v_mfma_f32_16x16x32_bf16 v[110:113], v[136:139], v[182:185], v[110:113]
	v_mfma_f32_16x16x32_bf16 v[106:109], v[166:169], v[182:185], v[106:109]
	v_mfma_f32_16x16x32_bf16 v[94:97], v[136:139], v[190:193], v[94:97]
	v_mfma_f32_16x16x32_bf16 v[90:93], v[166:169], v[190:193], v[90:93]
	v_mfma_f32_16x16x32_bf16 v[78:81], v[136:139], v[198:201], v[78:81]
	v_mfma_f32_16x16x32_bf16 v[74:77], v[166:169], v[198:201], v[74:77]
	s_setprio 0
	s_barrier
	ds_read_b128 v[202:205], v160
	ds_read_b128 v[206:209], v161
	ds_read_b128 v[210:213], v162
	ds_read_b128 v[214:217], v163
	s_add_u32 s20, s24, 0x80
	s_mov_b32 m0, s46
	s_addc_u32 s21, s25, 0
	global_load_lds_dwordx4 v147, s[20:21]
	s_add_u32 s20, s24, 0x40080
	s_mov_b32 m0, s47
	s_addc_u32 s21, s25, 0
	global_load_lds_dwordx4 v147, s[20:21]
	s_barrier
	s_waitcnt lgkmcnt(0)
	s_setprio 1
	v_mfma_f32_16x16x32_bf16 v[118:121], v[202:205], v[170:173], v[118:121]
	v_mfma_f32_16x16x32_bf16 v[114:117], v[210:213], v[170:173], v[114:117]
	v_mfma_f32_16x16x32_bf16 v[102:105], v[202:205], v[178:181], v[102:105]
	v_mfma_f32_16x16x32_bf16 v[98:101], v[210:213], v[178:181], v[98:101]
	v_mfma_f32_16x16x32_bf16 v[86:89], v[202:205], v[186:189], v[86:89]
	v_mfma_f32_16x16x32_bf16 v[82:85], v[210:213], v[186:189], v[82:85]
	v_mfma_f32_16x16x32_bf16 v[70:73], v[202:205], v[194:197], v[70:73]
	v_mfma_f32_16x16x32_bf16 v[66:69], v[210:213], v[194:197], v[66:69]
	v_mfma_f32_16x16x32_bf16 v[118:121], v[206:209], v[174:177], v[118:121]
	v_mfma_f32_16x16x32_bf16 v[114:117], v[214:217], v[174:177], v[114:117]
	v_mfma_f32_16x16x32_bf16 v[102:105], v[206:209], v[182:185], v[102:105]
	v_mfma_f32_16x16x32_bf16 v[98:101], v[214:217], v[182:185], v[98:101]
	v_mfma_f32_16x16x32_bf16 v[86:89], v[206:209], v[190:193], v[86:89]
	v_mfma_f32_16x16x32_bf16 v[82:85], v[214:217], v[190:193], v[82:85]
	v_mfma_f32_16x16x32_bf16 v[70:73], v[206:209], v[198:201], v[70:73]
	v_mfma_f32_16x16x32_bf16 v[66:69], v[214:217], v[198:201], v[66:69]
	s_setprio 0
	s_barrier
; #define PG8_STAGE(bufoff, gbase, voff) do { _Pragma("unroll") for (int _i = 0; _i < 2; ++_i) glds16_s((const void*)((const char*)(gbase) + _i * r64), (voff), ldsb + (unsigned)(bufoff) + ldsw + _i * 8192u); } while (0)
; #define PG8_LDA(b, h) do { _Pragma("unroll") for (int m = 0; m < 4; ++m) { const int o_ = PG8_SA(b, h) + aoff + m * 2048; \
;         if constexpr (FP8) A8[m] = PG8_CAT8(o_); else { At[m][0] = PG8_LD16(o_); At[m][1] = PG8_LD16(o_ + 1024); } } } while (0)
; #define PG8_WAIT_V(n) asm volatile("s_waitcnt vmcnt(" #n ")" ::: "memory")
; #define PG8_WAIT_L(n) asm volatile("s_waitcnt lgkmcnt(" #n ")" ::: "memory")
; #define PG8_BAR __builtin_amdgcn_s_barrier()
; #define PG8_SCHED __builtin_amdgcn_sched_barrier(0)
; #define PG8_HI do { if constexpr (FP8) asm volatile("s_setprio 1"); } while (0)
; #define PG8_LO do { if constexpr (FP8) asm volatile("s_setprio 0"); } while (0)
;     __device__ __forceinline__ void operator()(const f32x4 (&acc)[2][2][4][2], const Unit& u, int wr, int wc, int fr, int fq) const {
;         const int row0 = u.pm * BM + wr * 64 + fr, seg = u.pn >> 2, scol0 = (u.pn & 3) * BM + wc * 32 + 8 * fq;
;         const int kind = (seg == 2 || seg == 6) ? 1 : ((seg == 7) ? 2 : 0);
;         bf16_t* const Vb = (seg == 2) ? VAo : VBo;
; template <class Epi, class Sched, bool FP8 = false>
; __device__ __forceinline__ void gemm_phase(LAS unsigned char* lds, const int Kb, const int nt  , const Sched& S, const Epi& E) {
;     ...
;             PG8_LDA(1, 1); PG8_STAGE(PG8_SA(1, 0), a3, voffA);
;             PG8_BAR; PG8_HI; PG8_WAIT_L(0); PG8_MMA(1, 0, B0, B08); PG8_BAR; PG8_LO; PG8_SCHED;
;             PG8_STAGE(PG8_SB(1, 1), b3 + hstep, voffB);
;             PG8_WAIT_V(6); PG8_BAR; PG8_HI; PG8_MMA(1, 1, B1, B18); PG8_BAR; PG8_LO;
;         }
;         { int l_; asm volatile("v_mbcnt_lo_u32_b32 %0, -1, 0\n\tv_mbcnt_hi_u32_b32 %0, -1, %0" : "=v"(l_));
	ds_read_b128 v[170:173], v164 offset:49152
	ds_read_b128 v[174:177], v164 offset:50176
	ds_read_b128 v[178:181], v164 offset:51200
	ds_read_b128 v[182:185], v164 offset:52224
	ds_read_b128 v[186:189], v164 offset:53248
	ds_read_b128 v[190:193], v164 offset:54272
	ds_read_b128 v[194:197], v164 offset:55296
	s_mov_b32 m0, s48
	ds_read_b128 v[198:201], v164 offset:56320
	global_load_lds_dwordx4 v1, s[28:29]
	s_add_u32 s20, s26, 0x40080
	s_mov_b32 m0, s49
	s_addc_u32 s21, s27, 0
	global_load_lds_dwordx4 v1, s[20:21]
	s_barrier
	s_waitcnt lgkmcnt(0)
	s_setprio 1
	v_mfma_f32_16x16x32_bf16 v[62:65], v[132:135], v[170:173], v[62:65]
	v_mfma_f32_16x16x32_bf16 v[58:61], v[140:143], v[170:173], v[58:61]
	v_mfma_f32_16x16x32_bf16 v[46:49], v[132:135], v[178:181], v[46:49]
	v_mfma_f32_16x16x32_bf16 v[42:45], v[140:143], v[178:181], v[42:45]
	v_mfma_f32_16x16x32_bf16 v[30:33], v[132:135], v[186:189], v[30:33]
	v_mfma_f32_16x16x32_bf16 v[26:29], v[140:143], v[186:189], v[26:29]
	v_mfma_f32_16x16x32_bf16 v[14:17], v[132:135], v[194:197], v[14:17]
	v_mfma_f32_16x16x32_bf16 v[10:13], v[140:143], v[194:197], v[10:13]
	v_mfma_f32_16x16x32_bf16 v[62:65], v[136:139], v[174:177], v[62:65]
	v_mfma_f32_16x16x32_bf16 v[58:61], v[166:169], v[174:177], v[58:61]
	v_mfma_f32_16x16x32_bf16 v[46:49], v[136:139], v[182:185], v[46:49]
	v_mfma_f32_16x16x32_bf16 v[42:45], v[166:169], v[182:185], v[42:45]
	v_mfma_f32_16x16x32_bf16 v[30:33], v[136:139], v[190:193], v[30:33]
	v_mfma_f32_16x16x32_bf16 v[26:29], v[166:169], v[190:193], v[26:29]
	v_mfma_f32_16x16x32_bf16 v[14:17], v[136:139], v[198:201], v[14:17]
	v_mfma_f32_16x16x32_bf16 v[10:13], v[166:169], v[198:201], v[10:13]
	s_setprio 0
	s_barrier
	s_add_u32 s20, s24, 0x80080
	s_mov_b32 m0, s50
	s_addc_u32 s21, s25, 0
	global_load_lds_dwordx4 v147, s[20:21]
	s_add_u32 s20, s24, 0xc0080
	s_mov_b32 m0, s51
	s_addc_u32 s21, s25, 0
	global_load_lds_dwordx4 v147, s[20:21]
	s_waitcnt vmcnt(6)
	s_barrier
	s_setprio 1
	v_mfma_f32_16x16x32_bf16 v[54:57], v[202:205], v[170:173], v[54:57]
	v_mfma_f32_16x16x32_bf16 v[50:53], v[210:213], v[170:173], v[50:53]
	v_mfma_f32_16x16x32_bf16 v[38:41], v[202:205], v[178:181], v[38:41]
	v_mfma_f32_16x16x32_bf16 v[34:37], v[210:213], v[178:181], v[34:37]
	v_mfma_f32_16x16x32_bf16 v[22:25], v[202:205], v[186:189], v[22:25]
	v_mfma_f32_16x16x32_bf16 v[18:21], v[210:213], v[186:189], v[18:21]
	v_mfma_f32_16x16x32_bf16 v[6:9], v[202:205], v[194:197], v[6:9]
	v_mfma_f32_16x16x32_bf16 v[2:5], v[210:213], v[194:197], v[2:5]
	v_mfma_f32_16x16x32_bf16 v[54:57], v[206:209], v[174:177], v[54:57]
	v_mfma_f32_16x16x32_bf16 v[50:53], v[214:217], v[174:177], v[50:53]
	v_mfma_f32_16x16x32_bf16 v[38:41], v[206:209], v[182:185], v[38:41]
	v_mfma_f32_16x16x32_bf16 v[34:37], v[214:217], v[182:185], v[34:37]
	v_mfma_f32_16x16x32_bf16 v[22:25], v[206:209], v[190:193], v[22:25]
	v_mfma_f32_16x16x32_bf16 v[18:21], v[214:217], v[190:193], v[18:21]
	v_mfma_f32_16x16x32_bf16 v[6:9], v[206:209], v[198:201], v[6:9]
	v_mfma_f32_16x16x32_bf16 v[2:5], v[214:217], v[198:201], v[2:5]
	s_setprio 0
	s_add_i32 s59, s59, 2
	s_add_u32 s13, s13, 0x100
	s_addc_u32 s58, s58, 0
	s_cmp_gt_u32 s59, 29
	s_mov_b64 s[20:21], s[22:23]
	s_barrier
	s_cbranch_scc0 .LBB0_299
	s_ashr_i32 s24, s57, 2
	s_cmp_lt_i32 s24, 6
	v_mbcnt_lo_u32_b32 v130, -1, 0
	v_mbcnt_hi_u32_b32 v130, -1, v130
	s_cbranch_scc1 .LBB0_302
	s_cmp_lg_u32 s24, 6
	s_cselect_b64 s[20:21], -1, 0
	s_cbranch_execz .LBB0_303
	s_branch .LBB0_304

; #define PG8_STAGE(bufoff, gbase, voff) do { _Pragma("unroll") for (int _i = 0; _i < 2; ++_i) glds16_s((const void*)((const char*)(gbase) + _i * r64), (voff), ldsb + (unsigned)(bufoff) + ldsw + _i * 8192u); } while (0)
; #define PG8_LDA(b, h) do { _Pragma("unroll") for (int m = 0; m < 4; ++m) { const int o_ = PG8_SA(b, h) + aoff + m * 2048; \
;         if constexpr (FP8) A8[m] = PG8_CAT8(o_); else { At[m][0] = PG8_LD16(o_); At[m][1] = PG8_LD16(o_ + 1024); } } } while (0)
; #define PG8_LDB(X, X8, b, h) do { _Pragma("unroll") for (int n = 0; n < 2; ++n) { const int o_ = PG8_SB(b, h) + boff + n * 2048; \
;         if constexpr (FP8) X8[n] = PG8_CAT8(o_); else { X[n][0] = PG8_LD16(o_); X[n][1] = PG8_LD16(o_ + 1024); } } } while (0)
; #define PG8_WAIT_V(n) asm volatile("s_waitcnt vmcnt(" #n ")" ::: "memory")
; #define PG8_WAIT_L(n) asm volatile("s_waitcnt lgkmcnt(" #n ")" ::: "memory")
; #define PG8_BAR __builtin_amdgcn_s_barrier()
; #define PG8_SCHED __builtin_amdgcn_sched_barrier(0)
; #define PG8_HI do { if constexpr (FP8) asm volatile("s_setprio 1"); } while (0)
; #define PG8_LO do { if constexpr (FP8) asm volatile("s_setprio 0"); } while (0)
; template <class Epi, class Sched, bool FP8 = false>
; __device__ __forceinline__ void gemm_phase(LAS unsigned char* lds, const int Kb, const int nt  , const Sched& S, const Epi& E) {
;     ...
;         for (int t = 0; t < nt; t += 2) {
;             const bool last = (t == nt - 2);
;             const char* a1 = cA + (size_t)(t + 1) * kstep;
;             const char* a2 = last ? nA : cA + (size_t)(t + 2) * kstep; const char* b2 = last ? nB : cB + (size_t)(t + 2) * kstep;
;             const char* a3 = a2 + kstep; const char* b3 = b2 + kstep;
;             PG8_LDB(B0, B08, 0, 0); PG8_SCHED; PG8_LDA(0, 0); PG8_STAGE(PG8_SA(1, 1), a1 + hstep, voffA);
;             PG8_WAIT_L(8); PG8_BAR; PG8_HI; PG8_WAIT_L(0); PG8_MMA(0, 0, B0, B08); PG8_BAR; PG8_LO; PG8_SCHED;
;             PG8_LDB(B1, B18, 0, 1); PG8_STAGE(PG8_SB(0, 0), b2, voffB);
;             PG8_BAR; PG8_HI; PG8_WAIT_L(0); PG8_MMA(0, 1, B1, B18); PG8_BAR; PG8_LO;
;             PG8_LDA(0, 1); PG8_STAGE(PG8_SA(0, 0), a2, voffA);
;             PG8_BAR; PG8_HI; PG8_WAIT_L(0); PG8_MMA(1, 0, B0, B08); PG8_BAR; PG8_LO; PG8_SCHED;
;             PG8_STAGE(PG8_SB(0, 1), b2 + hstep, voffB);
;             PG8_WAIT_V(6); PG8_BAR; PG8_HI; PG8_MMA(1, 1, B1, B18); PG8_BAR; PG8_LO;
.LBB0_1715:
	ds_read_b128 v[130:133], v138
	ds_read_b128 v[134:137], v139
	ds_read_b128 v[156:159], v140
	ds_read_b128 v[160:163], v141
	s_add_u32 s24, s22, 0xfff80080
	s_addc_u32 s25, s23, -1
	s_cmp_eq_u32 s57, 28
	s_cselect_b32 s26, s18, s24
	s_cselect_b32 s27, s19, s25
	s_cselect_b32 s24, s20, s3
	s_cselect_b32 s25, s21, s17
	s_add_u32 s28, s26, 0x80
	s_addc_u32 s29, s27, 0
	ds_read_b128 v[164:167], v154
	ds_read_b128 v[168:171], v154 offset:1024
	ds_read_b128 v[172:175], v154 offset:2048
	ds_read_b128 v[176:179], v154 offset:3072
	ds_read_b128 v[180:183], v154 offset:4096
	ds_read_b128 v[184:187], v154 offset:5120
	ds_read_b128 v[194:197], v154 offset:6144
	s_mov_b32 m0, s53
	ds_read_b128 v[198:201], v154 offset:7168
	global_load_lds_dwordx4 v1, s[22:23]
	s_add_u32 s58, s22, 0x40000
	s_mov_b32 m0, s54
	s_addc_u32 s59, s23, 0
	global_load_lds_dwordx4 v1, s[58:59]
	s_waitcnt lgkmcnt(8)
	s_barrier
	s_waitcnt lgkmcnt(0)
	s_setprio 1
	v_mfma_f32_16x16x32_bf16 v[126:129], v[130:133], v[164:167], v[126:129]
	v_mfma_f32_16x16x32_bf16 v[122:125], v[156:159], v[164:167], v[122:125]
	v_mfma_f32_16x16x32_bf16 v[110:113], v[130:133], v[172:175], v[110:113]
	v_mfma_f32_16x16x32_bf16 v[106:109], v[156:159], v[172:175], v[106:109]
	v_mfma_f32_16x16x32_bf16 v[94:97], v[130:133], v[180:183], v[94:97]
	v_mfma_f32_16x16x32_bf16 v[90:93], v[156:159], v[180:183], v[90:93]
	v_mfma_f32_16x16x32_bf16 v[78:81], v[130:133], v[194:197], v[78:81]
	v_mfma_f32_16x16x32_bf16 v[74:77], v[156:159], v[194:197], v[74:77]
	v_mfma_f32_16x16x32_bf16 v[126:129], v[134:137], v[168:171], v[126:129]
	v_mfma_f32_16x16x32_bf16 v[122:125], v[160:163], v[168:171], v[122:125]
	v_mfma_f32_16x16x32_bf16 v[110:113], v[134:137], v[176:179], v[110:113]
	v_mfma_f32_16x16x32_bf16 v[106:109], v[160:163], v[176:179], v[106:109]
	v_mfma_f32_16x16x32_bf16 v[94:97], v[134:137], v[184:187], v[94:97]
	v_mfma_f32_16x16x32_bf16 v[90:93], v[160:163], v[184:187], v[90:93]
	v_mfma_f32_16x16x32_bf16 v[78:81], v[134:137], v[198:201], v[78:81]
	v_mfma_f32_16x16x32_bf16 v[74:77], v[160:163], v[198:201], v[74:77]
	s_setprio 0
	s_barrier
	ds_read_b128 v[202:205], v142
	ds_read_b128 v[206:209], v143
	ds_read_b128 v[210:213], v144
	s_mov_b32 m0, s38
	ds_read_b128 v[214:217], v145
	global_load_lds_dwordx4 v1, s[24:25]
	s_add_u32 s58, s24, 0x40000
	s_mov_b32 m0, s39
	s_addc_u32 s59, s25, 0
	global_load_lds_dwordx4 v1, s[58:59]
	s_barrier
	s_waitcnt lgkmcnt(0)
	s_setprio 1
	v_mfma_f32_16x16x32_bf16 v[118:121], v[202:205], v[164:167], v[118:121]
	v_mfma_f32_16x16x32_bf16 v[114:117], v[210:213], v[164:167], v[114:117]
	v_mfma_f32_16x16x32_bf16 v[102:105], v[202:205], v[172:175], v[102:105]
	v_mfma_f32_16x16x32_bf16 v[98:101], v[210:213], v[172:175], v[98:101]
	v_mfma_f32_16x16x32_bf16 v[86:89], v[202:205], v[180:183], v[86:89]
	v_mfma_f32_16x16x32_bf16 v[82:85], v[210:213], v[180:183], v[82:85]
	v_mfma_f32_16x16x32_bf16 v[70:73], v[202:205], v[194:197], v[70:73]
	v_mfma_f32_16x16x32_bf16 v[66:69], v[210:213], v[194:197], v[66:69]
	v_mfma_f32_16x16x32_bf16 v[118:121], v[206:209], v[168:171], v[118:121]
	v_mfma_f32_16x16x32_bf16 v[114:117], v[214:217], v[168:171], v[114:117]
	v_mfma_f32_16x16x32_bf16 v[102:105], v[206:209], v[176:179], v[102:105]
	v_mfma_f32_16x16x32_bf16 v[98:101], v[214:217], v[176:179], v[98:101]
	v_mfma_f32_16x16x32_bf16 v[86:89], v[206:209], v[184:187], v[86:89]
	v_mfma_f32_16x16x32_bf16 v[82:85], v[214:217], v[184:187], v[82:85]
	v_mfma_f32_16x16x32_bf16 v[70:73], v[206:209], v[198:201], v[70:73]
	v_mfma_f32_16x16x32_bf16 v[66:69], v[214:217], v[198:201], v[66:69]
	s_setprio 0
	s_barrier
	ds_read_b128 v[164:167], v154 offset:16384
	ds_read_b128 v[168:171], v154 offset:17408
	ds_read_b128 v[172:175], v154 offset:18432
	ds_read_b128 v[176:179], v154 offset:19456
	ds_read_b128 v[180:183], v154 offset:20480
	ds_read_b128 v[184:187], v154 offset:21504
	ds_read_b128 v[194:197], v154 offset:22528
	s_mov_b32 m0, s37
	ds_read_b128 v[198:201], v154 offset:23552
	global_load_lds_dwordx4 v1, s[26:27]
	s_add_u32 s58, s26, 0x40000
	s_mov_b32 m0, s40
	s_addc_u32 s59, s27, 0
	global_load_lds_dwordx4 v1, s[58:59]
	s_barrier
	s_waitcnt lgkmcnt(0)
	s_setprio 1
	v_mfma_f32_16x16x32_bf16 v[62:65], v[130:133], v[164:167], v[62:65]
	v_mfma_f32_16x16x32_bf16 v[58:61], v[156:159], v[164:167], v[58:61]
	v_mfma_f32_16x16x32_bf16 v[46:49], v[130:133], v[172:175], v[46:49]
	v_mfma_f32_16x16x32_bf16 v[42:45], v[156:159], v[172:175], v[42:45]
	v_mfma_f32_16x16x32_bf16 v[30:33], v[130:133], v[180:183], v[30:33]
	v_mfma_f32_16x16x32_bf16 v[26:29], v[156:159], v[180:183], v[26:29]
	v_mfma_f32_16x16x32_bf16 v[14:17], v[130:133], v[194:197], v[14:17]
	v_mfma_f32_16x16x32_bf16 v[10:13], v[156:159], v[194:197], v[10:13]
	v_mfma_f32_16x16x32_bf16 v[62:65], v[134:137], v[168:171], v[62:65]
	v_mfma_f32_16x16x32_bf16 v[58:61], v[160:163], v[168:171], v[58:61]
	v_mfma_f32_16x16x32_bf16 v[46:49], v[134:137], v[176:179], v[46:49]
	v_mfma_f32_16x16x32_bf16 v[42:45], v[160:163], v[176:179], v[42:45]
	v_mfma_f32_16x16x32_bf16 v[30:33], v[134:137], v[184:187], v[30:33]
	v_mfma_f32_16x16x32_bf16 v[26:29], v[160:163], v[184:187], v[26:29]
	v_mfma_f32_16x16x32_bf16 v[14:17], v[134:137], v[198:201], v[14:17]
	v_mfma_f32_16x16x32_bf16 v[10:13], v[160:163], v[198:201], v[10:13]
	s_setprio 0
	s_barrier
	s_add_u32 s58, s24, 0x80000
	s_mov_b32 m0, s41
	s_addc_u32 s59, s25, 0
	global_load_lds_dwordx4 v1, s[58:59]
	s_add_u32 s58, s24, 0xc0000
	s_mov_b32 m0, s42
	s_addc_u32 s59, s25, 0
	global_load_lds_dwordx4 v1, s[58:59]
	s_waitcnt vmcnt(6)
	s_barrier
; #define PG8_STAGE(bufoff, gbase, voff) do { _Pragma("unroll") for (int _i = 0; _i < 2; ++_i) glds16_s((const void*)((const char*)(gbase) + _i * r64), (voff), ldsb + (unsigned)(bufoff) + ldsw + _i * 8192u); } while (0)
; #define PG8_LDA(b, h) do { _Pragma("unroll") for (int m = 0; m < 4; ++m) { const int o_ = PG8_SA(b, h) + aoff + m * 2048; \
;         if constexpr (FP8) A8[m] = PG8_CAT8(o_); else { At[m][0] = PG8_LD16(o_); At[m][1] = PG8_LD16(o_ + 1024); } } } while (0)
; #define PG8_LDB(X, X8, b, h) do { _Pragma("unroll") for (int n = 0; n < 2; ++n) { const int o_ = PG8_SB(b, h) + boff + n * 2048; \
;         if constexpr (FP8) X8[n] = PG8_CAT8(o_); else { X[n][0] = PG8_LD16(o_); X[n][1] = PG8_LD16(o_ + 1024); } } } while (0)
; #define PG8_WAIT_V(n) asm volatile("s_waitcnt vmcnt(" #n ")" ::: "memory")
; #define PG8_WAIT_L(n) asm volatile("s_waitcnt lgkmcnt(" #n ")" ::: "memory")
; #define PG8_BAR __builtin_amdgcn_s_barrier()
; #define PG8_SCHED __builtin_amdgcn_sched_barrier(0)
; #define PG8_HI do { if constexpr (FP8) asm volatile("s_setprio 1"); } while (0)
; #define PG8_LO do { if constexpr (FP8) asm volatile("s_setprio 0"); } while (0)
; template <class Epi, class Sched, bool FP8 = false>
; __device__ __forceinline__ void gemm_phase(LAS unsigned char* lds, const int Kb, const int nt  , const Sched& S, const Epi& E) {
;     ...
;             PG8_WAIT_V(6); PG8_BAR; PG8_HI; PG8_MMA(1, 1, B1, B18); PG8_BAR; PG8_LO;
;             PG8_LDB(B0, B08, 1, 0); PG8_SCHED; PG8_LDA(1, 0); PG8_STAGE(PG8_SA(0, 1), a2 + hstep, voffA);
;             PG8_WAIT_L(8); PG8_BAR; PG8_HI; PG8_WAIT_L(0); PG8_MMA(0, 0, B0, B08); PG8_BAR; PG8_LO; PG8_SCHED;
;             PG8_LDB(B1, B18, 1, 1); PG8_STAGE(PG8_SB(1, 0), b3, voffB);
;             PG8_BAR; PG8_HI; PG8_WAIT_L(0); PG8_MMA(0, 1, B1, B18); PG8_BAR; PG8_LO;
	s_setprio 1
	v_mfma_f32_16x16x32_bf16 v[54:57], v[202:205], v[164:167], v[54:57]
	v_mfma_f32_16x16x32_bf16 v[50:53], v[210:213], v[164:167], v[50:53]
	v_mfma_f32_16x16x32_bf16 v[38:41], v[202:205], v[172:175], v[38:41]
	v_mfma_f32_16x16x32_bf16 v[34:37], v[210:213], v[172:175], v[34:37]
	v_mfma_f32_16x16x32_bf16 v[22:25], v[202:205], v[180:183], v[22:25]
	v_mfma_f32_16x16x32_bf16 v[18:21], v[210:213], v[180:183], v[18:21]
	v_mfma_f32_16x16x32_bf16 v[6:9], v[202:205], v[194:197], v[6:9]
	v_mfma_f32_16x16x32_bf16 v[2:5], v[210:213], v[194:197], v[2:5]
	v_mfma_f32_16x16x32_bf16 v[54:57], v[206:209], v[168:171], v[54:57]
	v_mfma_f32_16x16x32_bf16 v[50:53], v[214:217], v[168:171], v[50:53]
	v_mfma_f32_16x16x32_bf16 v[38:41], v[206:209], v[176:179], v[38:41]
	v_mfma_f32_16x16x32_bf16 v[34:37], v[214:217], v[176:179], v[34:37]
	v_mfma_f32_16x16x32_bf16 v[22:25], v[206:209], v[184:187], v[22:25]
	v_mfma_f32_16x16x32_bf16 v[18:21], v[214:217], v[184:187], v[18:21]
	v_mfma_f32_16x16x32_bf16 v[6:9], v[206:209], v[198:201], v[6:9]
	v_mfma_f32_16x16x32_bf16 v[2:5], v[214:217], v[198:201], v[2:5]
	s_setprio 0
	s_barrier
	ds_read_b128 v[130:133], v146
	ds_read_b128 v[134:137], v147
	ds_read_b128 v[156:159], v148
	ds_read_b128 v[160:163], v149
	ds_read_b128 v[164:167], v154 offset:32768
	ds_read_b128 v[168:171], v154 offset:33792
	ds_read_b128 v[172:175], v154 offset:34816
	ds_read_b128 v[176:179], v154 offset:35840
	ds_read_b128 v[180:183], v154 offset:36864
	ds_read_b128 v[184:187], v154 offset:37888
	ds_read_b128 v[194:197], v154 offset:38912
	ds_read_b128 v[198:201], v154 offset:39936
	s_add_u32 s58, s26, 0x80000
	s_mov_b32 m0, s43
	s_addc_u32 s59, s27, 0
	global_load_lds_dwordx4 v1, s[58:59]
	s_add_u32 s58, s26, 0xc0000
	s_mov_b32 m0, s44
	s_addc_u32 s59, s27, 0
	global_load_lds_dwordx4 v1, s[58:59]
	s_waitcnt lgkmcnt(8)
	s_barrier
	s_waitcnt lgkmcnt(0)
	s_setprio 1
	v_mfma_f32_16x16x32_bf16 v[126:129], v[130:133], v[164:167], v[126:129]
	v_mfma_f32_16x16x32_bf16 v[122:125], v[156:159], v[164:167], v[122:125]
	v_mfma_f32_16x16x32_bf16 v[110:113], v[130:133], v[172:175], v[110:113]
	v_mfma_f32_16x16x32_bf16 v[106:109], v[156:159], v[172:175], v[106:109]
	v_mfma_f32_16x16x32_bf16 v[94:97], v[130:133], v[180:183], v[94:97]
	v_mfma_f32_16x16x32_bf16 v[90:93], v[156:159], v[180:183], v[90:93]
	v_mfma_f32_16x16x32_bf16 v[78:81], v[130:133], v[194:197], v[78:81]
	v_mfma_f32_16x16x32_bf16 v[74:77], v[156:159], v[194:197], v[74:77]
	v_mfma_f32_16x16x32_bf16 v[126:129], v[134:137], v[168:171], v[126:129]
	v_mfma_f32_16x16x32_bf16 v[122:125], v[160:163], v[168:171], v[122:125]
	v_mfma_f32_16x16x32_bf16 v[110:113], v[134:137], v[176:179], v[110:113]
	v_mfma_f32_16x16x32_bf16 v[106:109], v[160:163], v[176:179], v[106:109]
	v_mfma_f32_16x16x32_bf16 v[94:97], v[134:137], v[184:187], v[94:97]
	v_mfma_f32_16x16x32_bf16 v[90:93], v[160:163], v[184:187], v[90:93]
	v_mfma_f32_16x16x32_bf16 v[78:81], v[134:137], v[198:201], v[78:81]
	v_mfma_f32_16x16x32_bf16 v[74:77], v[160:163], v[198:201], v[74:77]
	s_setprio 0
	s_barrier
	ds_read_b128 v[202:205], v150
	ds_read_b128 v[206:209], v151
	ds_read_b128 v[210:213], v152
	ds_read_b128 v[214:217], v153
	s_add_u32 s58, s24, 0x80
	s_mov_b32 m0, s47
	s_addc_u32 s59, s25, 0
	global_load_lds_dwordx4 v1, s[58:59]
	s_add_u32 s58, s24, 0x40080
	s_mov_b32 m0, s48
	s_addc_u32 s59, s25, 0
	global_load_lds_dwordx4 v1, s[58:59]
	s_barrier
	s_waitcnt lgkmcnt(0)
	s_setprio 1
	v_mfma_f32_16x16x32_bf16 v[118:121], v[202:205], v[164:167], v[118:121]
	v_mfma_f32_16x16x32_bf16 v[114:117], v[210:213], v[164:167], v[114:117]
	v_mfma_f32_16x16x32_bf16 v[102:105], v[202:205], v[172:175], v[102:105]
	v_mfma_f32_16x16x32_bf16 v[98:101], v[210:213], v[172:175], v[98:101]
	v_mfma_f32_16x16x32_bf16 v[86:89], v[202:205], v[180:183], v[86:89]
	v_mfma_f32_16x16x32_bf16 v[82:85], v[210:213], v[180:183], v[82:85]
	v_mfma_f32_16x16x32_bf16 v[70:73], v[202:205], v[194:197], v[70:73]
	v_mfma_f32_16x16x32_bf16 v[66:69], v[210:213], v[194:197], v[66:69]
	v_mfma_f32_16x16x32_bf16 v[118:121], v[206:209], v[168:171], v[118:121]
	v_mfma_f32_16x16x32_bf16 v[114:117], v[214:217], v[168:171], v[114:117]
	v_mfma_f32_16x16x32_bf16 v[102:105], v[206:209], v[176:179], v[102:105]
	v_mfma_f32_16x16x32_bf16 v[98:101], v[214:217], v[176:179], v[98:101]
	v_mfma_f32_16x16x32_bf16 v[86:89], v[206:209], v[184:187], v[86:89]
	v_mfma_f32_16x16x32_bf16 v[82:85], v[214:217], v[184:187], v[82:85]
	v_mfma_f32_16x16x32_bf16 v[70:73], v[206:209], v[198:201], v[70:73]
	v_mfma_f32_16x16x32_bf16 v[66:69], v[214:217], v[198:201], v[66:69]
	s_setprio 0
	s_barrier
; #define PG8_STAGE(bufoff, gbase, voff) do { _Pragma("unroll") for (int _i = 0; _i < 2; ++_i) glds16_s((const void*)((const char*)(gbase) + _i * r64), (voff), ldsb + (unsigned)(bufoff) + ldsw + _i * 8192u); } while (0)
; #define PG8_LDA(b, h) do { _Pragma("unroll") for (int m = 0; m < 4; ++m) { const int o_ = PG8_SA(b, h) + aoff + m * 2048; \
;         if constexpr (FP8) A8[m] = PG8_CAT8(o_); else { At[m][0] = PG8_LD16(o_); At[m][1] = PG8_LD16(o_ + 1024); } } } while (0)
; #define PG8_WAIT_V(n) asm volatile("s_waitcnt vmcnt(" #n ")" ::: "memory")
; #define PG8_WAIT_L(n) asm volatile("s_waitcnt lgkmcnt(" #n ")" ::: "memory")
; #define PG8_BAR __builtin_amdgcn_s_barrier()
; #define PG8_SCHED __builtin_amdgcn_sched_barrier(0)
;     __device__ __forceinline__ void operator()(const f32x4 (&acc)[2][2][4][2], const Unit& u, int wr, int wc, int fr, int fq) const {
;         const int row0 = u.pm * BM + wr * 64 + fr, col0 = u.pn * BM + wc * 32 + 4 * fq;
;         f32x4 cs[2][2];
; #pragma unroll
;         for (int bj = 0; bj < 2; ++bj)
; #pragma unroll
;             for (int n = 0; n < 2; ++n) cs[bj][n] = (cscale ? *(const f32x4*)(cscale + col0 + bj * HALF + n * 16) : (f32x4){1.f, 1.f, 1.f, 1.f}) * ascale;
; #pragma unroll
;         for (int ai = 0; ai < 2; ++ai)
; #pragma unroll
;             for (int m = 0; m < 4; ++m) { const size_t off = (size_t)(row0 + ai * HALF + m * 16) * ldc + col0;
; #pragma unroll
;                 for (int bj = 0; bj < 2; ++bj)
; #pragma unroll
;                     for (int n = 0; n < 2; ++n) { f32x4 v = acc[ai][bj][m][n] * cs[bj][n];
;                         if (res) v += *(const f32x4*)(res + off + bj * HALF + n * 16);
; template <class Epi, class Sched, bool FP8 = false>
; __device__ __forceinline__ void gemm_phase(LAS unsigned char* lds, const int Kb, const int nt  , const Sched& S, const Epi& E) {
;     ...
;             PG8_LDA(1, 1); PG8_STAGE(PG8_SA(1, 0), a3, voffA);
;             PG8_BAR; PG8_HI; PG8_WAIT_L(0); PG8_MMA(1, 0, B0, B08); PG8_BAR; PG8_LO; PG8_SCHED;
;             PG8_STAGE(PG8_SB(1, 1), b3 + hstep, voffB);
;             PG8_WAIT_V(6); PG8_BAR; PG8_HI; PG8_MMA(1, 1, B1, B18); PG8_BAR; PG8_LO;
;         }
;         { int l_; asm volatile("v_mbcnt_lo_u32_b32 %0, -1, 0\n\tv_mbcnt_hi_u32_b32 %0, -1, %0" : "=v"(l_));
;           E(acc, cur, wr, wc, l_ & 15, l_ >> 4); }
	ds_read_b128 v[164:167], v154 offset:49152
	ds_read_b128 v[168:171], v154 offset:50176
	ds_read_b128 v[172:175], v154 offset:51200
	ds_read_b128 v[176:179], v154 offset:52224
	ds_read_b128 v[180:183], v154 offset:53248
	ds_read_b128 v[184:187], v154 offset:54272
	ds_read_b128 v[194:197], v154 offset:55296
	s_mov_b32 m0, s49
	ds_read_b128 v[198:201], v154 offset:56320
	global_load_lds_dwordx4 v1, s[28:29]
	s_add_u32 s26, s26, 0x40080
	s_mov_b32 m0, s50
	s_addc_u32 s27, s27, 0
	global_load_lds_dwordx4 v1, s[26:27]
	s_barrier
	s_waitcnt lgkmcnt(0)
	s_setprio 1
	v_mfma_f32_16x16x32_bf16 v[62:65], v[130:133], v[164:167], v[62:65]
	v_mfma_f32_16x16x32_bf16 v[58:61], v[156:159], v[164:167], v[58:61]
	v_mfma_f32_16x16x32_bf16 v[46:49], v[130:133], v[172:175], v[46:49]
	v_mfma_f32_16x16x32_bf16 v[42:45], v[156:159], v[172:175], v[42:45]
	v_mfma_f32_16x16x32_bf16 v[30:33], v[130:133], v[180:183], v[30:33]
	v_mfma_f32_16x16x32_bf16 v[26:29], v[156:159], v[180:183], v[26:29]
	v_mfma_f32_16x16x32_bf16 v[14:17], v[130:133], v[194:197], v[14:17]
	v_mfma_f32_16x16x32_bf16 v[10:13], v[156:159], v[194:197], v[10:13]
	v_mfma_f32_16x16x32_bf16 v[62:65], v[134:137], v[168:171], v[62:65]
	v_mfma_f32_16x16x32_bf16 v[58:61], v[160:163], v[168:171], v[58:61]
	v_mfma_f32_16x16x32_bf16 v[46:49], v[134:137], v[176:179], v[46:49]
	v_mfma_f32_16x16x32_bf16 v[42:45], v[160:163], v[176:179], v[42:45]
	v_mfma_f32_16x16x32_bf16 v[30:33], v[134:137], v[184:187], v[30:33]
	v_mfma_f32_16x16x32_bf16 v[26:29], v[160:163], v[184:187], v[26:29]
	v_mfma_f32_16x16x32_bf16 v[14:17], v[134:137], v[198:201], v[14:17]
	v_mfma_f32_16x16x32_bf16 v[10:13], v[160:163], v[198:201], v[10:13]
	s_setprio 0
	s_barrier
	s_add_u32 s26, s24, 0x80080
	s_mov_b32 m0, s51
	s_addc_u32 s27, s25, 0
	global_load_lds_dwordx4 v1, s[26:27]
	s_add_u32 s24, s24, 0xc0080
	s_mov_b32 m0, s52
	s_addc_u32 s25, s25, 0
	global_load_lds_dwordx4 v1, s[24:25]
	s_waitcnt vmcnt(6)
	s_barrier
	s_setprio 1
	v_mfma_f32_16x16x32_bf16 v[54:57], v[202:205], v[164:167], v[54:57]
	v_mfma_f32_16x16x32_bf16 v[50:53], v[210:213], v[164:167], v[50:53]
	v_mfma_f32_16x16x32_bf16 v[38:41], v[202:205], v[172:175], v[38:41]
	v_mfma_f32_16x16x32_bf16 v[34:37], v[210:213], v[172:175], v[34:37]
	v_mfma_f32_16x16x32_bf16 v[22:25], v[202:205], v[180:183], v[22:25]
	v_mfma_f32_16x16x32_bf16 v[18:21], v[210:213], v[180:183], v[18:21]
	v_mfma_f32_16x16x32_bf16 v[6:9], v[202:205], v[194:197], v[6:9]
	v_mfma_f32_16x16x32_bf16 v[2:5], v[210:213], v[194:197], v[2:5]
	v_mfma_f32_16x16x32_bf16 v[54:57], v[206:209], v[168:171], v[54:57]
	v_mfma_f32_16x16x32_bf16 v[50:53], v[214:217], v[168:171], v[50:53]
	v_mfma_f32_16x16x32_bf16 v[38:41], v[206:209], v[176:179], v[38:41]
	v_mfma_f32_16x16x32_bf16 v[34:37], v[214:217], v[176:179], v[34:37]
	v_mfma_f32_16x16x32_bf16 v[22:25], v[206:209], v[184:187], v[22:25]
	v_mfma_f32_16x16x32_bf16 v[18:21], v[214:217], v[184:187], v[18:21]
	v_mfma_f32_16x16x32_bf16 v[6:9], v[206:209], v[198:201], v[6:9]
	v_mfma_f32_16x16x32_bf16 v[2:5], v[214:217], v[198:201], v[2:5]
	s_setprio 0
	s_add_i32 s57, s57, 2
	s_add_u32 s22, s22, 0x100
	s_addc_u32 s23, s23, 0
	s_add_u32 s3, s3, 0x100
	s_addc_u32 s17, s17, 0
	s_cmp_gt_u32 s57, 29
	s_barrier
	s_cbranch_scc0 .LBB0_1715
	s_lshl_b32 s2, s2, 8
	v_mbcnt_lo_u32_b32 v132, -1, 0
	v_mbcnt_hi_u32_b32 v132, -1, v132
	s_add_i32 s2, s2, s45
	s_lshl_b32 s3, s56, 8
	v_ashrrev_i32_e32 v130, 2, v132
	s_or_b32 s3, s3, s46
	v_and_b32_e32 v130, -4, v130
	v_and_or_b32 v132, v132, 15, s2
	v_add_u32_e32 v130, s3, v130
	v_ashrrev_i32_e32 v133, 31, v132
	v_ashrrev_i32_e32 v131, 31, v130
	v_lshlrev_b64 v[134:135], 11, v[132:133]
	v_lshl_add_u64 v[136:137], v[134:135], 0, v[130:131]
	v_cndmask_b32_e64 v134, 0, 1, s[6:7]
	v_cmp_ne_u32_e64 s[2:3], 1, v134
	s_andn2_b64 vcc, exec, s[6:7]
	v_lshl_add_u64 v[134:135], v[136:137], 2, s[76:77]
	s_cbranch_vccnz .LBB0_1718
	global_load_dwordx4 v[156:159], v[134:135], off
	s_waitcnt vmcnt(0)
	v_pk_add_f32 v[128:129], v[128:129], v[158:159]
	v_pk_add_f32 v[126:127], v[126:127], v[156:157]

; #define PG8_STAGE(bufoff, gbase, voff) do { _Pragma("unroll") for (int _i = 0; _i < 2; ++_i) glds16_s((const void*)((const char*)(gbase) + _i * r64), (voff), ldsb + (unsigned)(bufoff) + ldsw + _i * 8192u); } while (0)
; #define PG8_LDA(b, h) do { _Pragma("unroll") for (int m = 0; m < 4; ++m) { const int o_ = PG8_SA(b, h) + aoff + m * 2048; \
;         if constexpr (FP8) A8[m] = PG8_CAT8(o_); else { At[m][0] = PG8_LD16(o_); At[m][1] = PG8_LD16(o_ + 1024); } } } while (0)
; #define PG8_LDB(X, X8, b, h) do { _Pragma("unroll") for (int n = 0; n < 2; ++n) { const int o_ = PG8_SB(b, h) + boff + n * 2048; \
;         if constexpr (FP8) X8[n] = PG8_CAT8(o_); else { X[n][0] = PG8_LD16(o_); X[n][1] = PG8_LD16(o_ + 1024); } } } while (0)
; #define PG8_WAIT_V(n) asm volatile("s_waitcnt vmcnt(" #n ")" ::: "memory")
; #define PG8_WAIT_L(n) asm volatile("s_waitcnt lgkmcnt(" #n ")" ::: "memory")
; #define PG8_BAR __builtin_amdgcn_s_barrier()
; #define PG8_SCHED __builtin_amdgcn_sched_barrier(0)
; #define PG8_HI do { if constexpr (FP8) asm volatile("s_setprio 1"); } while (0)
; #define PG8_LO do { if constexpr (FP8) asm volatile("s_setprio 0"); } while (0)
; template <class Epi, class Sched, bool FP8 = false>
; __device__ __forceinline__ void gemm_phase(LAS unsigned char* lds, const int Kb, const int nt  , const Sched& S, const Epi& E) {
;     ...
;         for (int t = 0; t < nt; t += 2) {
;             const bool last = (t == nt - 2);
;             const char* a1 = cA + (size_t)(t + 1) * kstep;
;             const char* a2 = last ? nA : cA + (size_t)(t + 2) * kstep; const char* b2 = last ? nB : cB + (size_t)(t + 2) * kstep;
;             const char* a3 = a2 + kstep; const char* b3 = b2 + kstep;
;             PG8_LDB(B0, B08, 0, 0); PG8_SCHED; PG8_LDA(0, 0); PG8_STAGE(PG8_SA(1, 1), a1 + hstep, voffA);
;             PG8_WAIT_L(8); PG8_BAR; PG8_HI; PG8_WAIT_L(0); PG8_MMA(0, 0, B0, B08); PG8_BAR; PG8_LO; PG8_SCHED;
;             PG8_LDB(B1, B18, 0, 1); PG8_STAGE(PG8_SB(0, 0), b2, voffB);
;             PG8_BAR; PG8_HI; PG8_WAIT_L(0); PG8_MMA(0, 1, B1, B18); PG8_BAR; PG8_LO;
;             PG8_LDA(0, 1); PG8_STAGE(PG8_SA(0, 0), a2, voffA);
;             PG8_BAR; PG8_HI; PG8_WAIT_L(0); PG8_MMA(1, 0, B0, B08); PG8_BAR; PG8_LO; PG8_SCHED;
;             PG8_STAGE(PG8_SB(0, 1), b2 + hstep, voffB);
;             PG8_WAIT_V(6); PG8_BAR; PG8_HI; PG8_MMA(1, 1, B1, B18); PG8_BAR; PG8_LO;
.LBB0_1946:
	ds_read_b128 v[150:153], v133
	ds_read_b128 v[154:157], v134
	ds_read_b128 v[158:161], v135
	ds_read_b128 v[162:165], v136
	s_add_u32 s16, s14, 0x100
	s_addc_u32 s17, s15, 0
	s_cmp_eq_u32 s53, 28
	s_cselect_b32 s20, s8, s16
	s_cselect_b32 s21, s9, s17
	s_cselect_b32 s18, s10, s5
	s_cselect_b32 s19, s11, s52
	s_add_u32 s22, s20, 0x80
	s_addc_u32 s23, s21, 0
	ds_read_b128 v[166:169], v149
	ds_read_b128 v[170:173], v149 offset:1024
	ds_read_b128 v[174:177], v149 offset:2048
	ds_read_b128 v[178:181], v149 offset:3072
	ds_read_b128 v[182:185], v149 offset:4096
	ds_read_b128 v[186:189], v149 offset:5120
	ds_read_b128 v[194:197], v149 offset:6144
	ds_read_b128 v[198:201], v149 offset:7168
	s_add_u32 s54, s14, 0x80080
	s_mov_b32 m0, s47
	s_addc_u32 s55, s15, 0
	global_load_lds_dwordx4 v1, s[54:55]
	s_add_u32 s14, s14, 0xc0080
	s_mov_b32 m0, s48
	s_addc_u32 s15, s15, 0
	global_load_lds_dwordx4 v1, s[14:15]
	s_waitcnt lgkmcnt(8)
	s_barrier
	s_waitcnt lgkmcnt(0)
	s_setprio 1
	v_mfma_f32_16x16x32_bf16 v[126:129], v[150:153], v[166:169], v[126:129]
	v_mfma_f32_16x16x32_bf16 v[122:125], v[158:161], v[166:169], v[122:125]
	v_mfma_f32_16x16x32_bf16 v[110:113], v[150:153], v[174:177], v[110:113]
	v_mfma_f32_16x16x32_bf16 v[106:109], v[158:161], v[174:177], v[106:109]
	v_mfma_f32_16x16x32_bf16 v[94:97], v[150:153], v[182:185], v[94:97]
	v_mfma_f32_16x16x32_bf16 v[90:93], v[158:161], v[182:185], v[90:93]
	v_mfma_f32_16x16x32_bf16 v[78:81], v[150:153], v[194:197], v[78:81]
	v_mfma_f32_16x16x32_bf16 v[74:77], v[158:161], v[194:197], v[74:77]
	v_mfma_f32_16x16x32_bf16 v[126:129], v[154:157], v[170:173], v[126:129]
	v_mfma_f32_16x16x32_bf16 v[122:125], v[162:165], v[170:173], v[122:125]
	v_mfma_f32_16x16x32_bf16 v[110:113], v[154:157], v[178:181], v[110:113]
	v_mfma_f32_16x16x32_bf16 v[106:109], v[162:165], v[178:181], v[106:109]
	v_mfma_f32_16x16x32_bf16 v[94:97], v[154:157], v[186:189], v[94:97]
	v_mfma_f32_16x16x32_bf16 v[90:93], v[162:165], v[186:189], v[90:93]
	v_mfma_f32_16x16x32_bf16 v[78:81], v[154:157], v[198:201], v[78:81]
	v_mfma_f32_16x16x32_bf16 v[74:77], v[162:165], v[198:201], v[74:77]
	s_setprio 0
	s_barrier
	ds_read_b128 v[202:205], v137
	ds_read_b128 v[206:209], v138
	ds_read_b128 v[210:213], v139
	s_mov_b32 m0, s31
	ds_read_b128 v[214:217], v140
	global_load_lds_dwordx4 v132, s[18:19]
	s_add_u32 s14, s18, 0x40000
	s_mov_b32 m0, s33
	s_addc_u32 s15, s19, 0
	global_load_lds_dwordx4 v132, s[14:15]
	s_barrier
	s_waitcnt lgkmcnt(0)
	s_setprio 1
	v_mfma_f32_16x16x32_bf16 v[118:121], v[202:205], v[166:169], v[118:121]
	v_mfma_f32_16x16x32_bf16 v[114:117], v[210:213], v[166:169], v[114:117]
	v_mfma_f32_16x16x32_bf16 v[102:105], v[202:205], v[174:177], v[102:105]
	v_mfma_f32_16x16x32_bf16 v[98:101], v[210:213], v[174:177], v[98:101]
	v_mfma_f32_16x16x32_bf16 v[86:89], v[202:205], v[182:185], v[86:89]
	v_mfma_f32_16x16x32_bf16 v[82:85], v[210:213], v[182:185], v[82:85]
	v_mfma_f32_16x16x32_bf16 v[70:73], v[202:205], v[194:197], v[70:73]
	v_mfma_f32_16x16x32_bf16 v[66:69], v[210:213], v[194:197], v[66:69]
	v_mfma_f32_16x16x32_bf16 v[118:121], v[206:209], v[170:173], v[118:121]
	v_mfma_f32_16x16x32_bf16 v[114:117], v[214:217], v[170:173], v[114:117]
	v_mfma_f32_16x16x32_bf16 v[102:105], v[206:209], v[178:181], v[102:105]
	v_mfma_f32_16x16x32_bf16 v[98:101], v[214:217], v[178:181], v[98:101]
	v_mfma_f32_16x16x32_bf16 v[86:89], v[206:209], v[186:189], v[86:89]
	v_mfma_f32_16x16x32_bf16 v[82:85], v[214:217], v[186:189], v[82:85]
	v_mfma_f32_16x16x32_bf16 v[70:73], v[206:209], v[198:201], v[70:73]
	v_mfma_f32_16x16x32_bf16 v[66:69], v[214:217], v[198:201], v[66:69]
	s_setprio 0
	s_barrier
	ds_read_b128 v[166:169], v149 offset:16384
	ds_read_b128 v[170:173], v149 offset:17408
	ds_read_b128 v[174:177], v149 offset:18432
	ds_read_b128 v[178:181], v149 offset:19456
	ds_read_b128 v[182:185], v149 offset:20480
	ds_read_b128 v[186:189], v149 offset:21504
	ds_read_b128 v[194:197], v149 offset:22528
	s_mov_b32 m0, s13
	ds_read_b128 v[198:201], v149 offset:23552
	global_load_lds_dwordx4 v1, s[20:21]
	s_add_u32 s14, s20, 0x40000
	s_mov_b32 m0, s34
	s_addc_u32 s15, s21, 0
	global_load_lds_dwordx4 v1, s[14:15]
	s_barrier
	s_waitcnt lgkmcnt(0)
	s_setprio 1
	v_mfma_f32_16x16x32_bf16 v[62:65], v[150:153], v[166:169], v[62:65]
	v_mfma_f32_16x16x32_bf16 v[58:61], v[158:161], v[166:169], v[58:61]
	v_mfma_f32_16x16x32_bf16 v[46:49], v[150:153], v[174:177], v[46:49]
	v_mfma_f32_16x16x32_bf16 v[42:45], v[158:161], v[174:177], v[42:45]
	v_mfma_f32_16x16x32_bf16 v[30:33], v[150:153], v[182:185], v[30:33]
	v_mfma_f32_16x16x32_bf16 v[26:29], v[158:161], v[182:185], v[26:29]
	v_mfma_f32_16x16x32_bf16 v[14:17], v[150:153], v[194:197], v[14:17]
	v_mfma_f32_16x16x32_bf16 v[10:13], v[158:161], v[194:197], v[10:13]
	v_mfma_f32_16x16x32_bf16 v[62:65], v[154:157], v[170:173], v[62:65]
	v_mfma_f32_16x16x32_bf16 v[58:61], v[162:165], v[170:173], v[58:61]
	v_mfma_f32_16x16x32_bf16 v[46:49], v[154:157], v[178:181], v[46:49]
	v_mfma_f32_16x16x32_bf16 v[42:45], v[162:165], v[178:181], v[42:45]
	v_mfma_f32_16x16x32_bf16 v[30:33], v[154:157], v[186:189], v[30:33]
	v_mfma_f32_16x16x32_bf16 v[26:29], v[162:165], v[186:189], v[26:29]
	v_mfma_f32_16x16x32_bf16 v[14:17], v[154:157], v[198:201], v[14:17]
	v_mfma_f32_16x16x32_bf16 v[10:13], v[162:165], v[198:201], v[10:13]
	s_setprio 0
	s_barrier
	s_add_u32 s14, s18, 0x80000
	s_mov_b32 m0, s35
	s_addc_u32 s15, s19, 0
	global_load_lds_dwordx4 v132, s[14:15]
	s_add_u32 s14, s18, 0xc0000
	s_mov_b32 m0, s36
	s_addc_u32 s15, s19, 0
	global_load_lds_dwordx4 v132, s[14:15]
	s_waitcnt vmcnt(6)
	s_barrier
; #define PG8_STAGE(bufoff, gbase, voff) do { _Pragma("unroll") for (int _i = 0; _i < 2; ++_i) glds16_s((const void*)((const char*)(gbase) + _i * r64), (voff), ldsb + (unsigned)(bufoff) + ldsw + _i * 8192u); } while (0)
; #define PG8_LDA(b, h) do { _Pragma("unroll") for (int m = 0; m < 4; ++m) { const int o_ = PG8_SA(b, h) + aoff + m * 2048; \
;         if constexpr (FP8) A8[m] = PG8_CAT8(o_); else { At[m][0] = PG8_LD16(o_); At[m][1] = PG8_LD16(o_ + 1024); } } } while (0)
; #define PG8_LDB(X, X8, b, h) do { _Pragma("unroll") for (int n = 0; n < 2; ++n) { const int o_ = PG8_SB(b, h) + boff + n * 2048; \
;         if constexpr (FP8) X8[n] = PG8_CAT8(o_); else { X[n][0] = PG8_LD16(o_); X[n][1] = PG8_LD16(o_ + 1024); } } } while (0)
; #define PG8_WAIT_V(n) asm volatile("s_waitcnt vmcnt(" #n ")" ::: "memory")
; #define PG8_WAIT_L(n) asm volatile("s_waitcnt lgkmcnt(" #n ")" ::: "memory")
; #define PG8_BAR __builtin_amdgcn_s_barrier()
; #define PG8_SCHED __builtin_amdgcn_sched_barrier(0)
; #define PG8_HI do { if constexpr (FP8) asm volatile("s_setprio 1"); } while (0)
; #define PG8_LO do { if constexpr (FP8) asm volatile("s_setprio 0"); } while (0)
; template <class Epi, class Sched, bool FP8 = false>
; __device__ __forceinline__ void gemm_phase(LAS unsigned char* lds, const int Kb, const int nt  , const Sched& S, const Epi& E) {
;     ...
;             PG8_WAIT_V(6); PG8_BAR; PG8_HI; PG8_MMA(1, 1, B1, B18); PG8_BAR; PG8_LO;
;             PG8_LDB(B0, B08, 1, 0); PG8_SCHED; PG8_LDA(1, 0); PG8_STAGE(PG8_SA(0, 1), a2 + hstep, voffA);
;             PG8_WAIT_L(8); PG8_BAR; PG8_HI; PG8_WAIT_L(0); PG8_MMA(0, 0, B0, B08); PG8_BAR; PG8_LO; PG8_SCHED;
;             PG8_LDB(B1, B18, 1, 1); PG8_STAGE(PG8_SB(1, 0), b3, voffB);
;             PG8_BAR; PG8_HI; PG8_WAIT_L(0); PG8_MMA(0, 1, B1, B18); PG8_BAR; PG8_LO;
;             PG8_LDA(1, 1); PG8_STAGE(PG8_SA(1, 0), a3, voffA);
	s_setprio 1
	v_mfma_f32_16x16x32_bf16 v[54:57], v[202:205], v[166:169], v[54:57]
	v_mfma_f32_16x16x32_bf16 v[50:53], v[210:213], v[166:169], v[50:53]
	v_mfma_f32_16x16x32_bf16 v[38:41], v[202:205], v[174:177], v[38:41]
	v_mfma_f32_16x16x32_bf16 v[34:37], v[210:213], v[174:177], v[34:37]
	v_mfma_f32_16x16x32_bf16 v[22:25], v[202:205], v[182:185], v[22:25]
	v_mfma_f32_16x16x32_bf16 v[18:21], v[210:213], v[182:185], v[18:21]
	v_mfma_f32_16x16x32_bf16 v[6:9], v[202:205], v[194:197], v[6:9]
	v_mfma_f32_16x16x32_bf16 v[2:5], v[210:213], v[194:197], v[2:5]
	v_mfma_f32_16x16x32_bf16 v[54:57], v[206:209], v[170:173], v[54:57]
	v_mfma_f32_16x16x32_bf16 v[50:53], v[214:217], v[170:173], v[50:53]
	v_mfma_f32_16x16x32_bf16 v[38:41], v[206:209], v[178:181], v[38:41]
	v_mfma_f32_16x16x32_bf16 v[34:37], v[214:217], v[178:181], v[34:37]
	v_mfma_f32_16x16x32_bf16 v[22:25], v[206:209], v[186:189], v[22:25]
	v_mfma_f32_16x16x32_bf16 v[18:21], v[214:217], v[186:189], v[18:21]
	v_mfma_f32_16x16x32_bf16 v[6:9], v[206:209], v[198:201], v[6:9]
	v_mfma_f32_16x16x32_bf16 v[2:5], v[214:217], v[198:201], v[2:5]
	s_setprio 0
	s_barrier
	ds_read_b128 v[150:153], v141
	ds_read_b128 v[154:157], v142
	ds_read_b128 v[158:161], v143
	ds_read_b128 v[162:165], v144
	ds_read_b128 v[166:169], v149 offset:32768
	ds_read_b128 v[170:173], v149 offset:33792
	ds_read_b128 v[174:177], v149 offset:34816
	ds_read_b128 v[178:181], v149 offset:35840
	ds_read_b128 v[182:185], v149 offset:36864
	ds_read_b128 v[186:189], v149 offset:37888
	ds_read_b128 v[194:197], v149 offset:38912
	ds_read_b128 v[198:201], v149 offset:39936
	s_add_u32 s14, s20, 0x80000
	s_mov_b32 m0, s37
	s_addc_u32 s15, s21, 0
	global_load_lds_dwordx4 v1, s[14:15]
	s_add_u32 s14, s20, 0xc0000
	s_mov_b32 m0, s38
	s_addc_u32 s15, s21, 0
	global_load_lds_dwordx4 v1, s[14:15]
	s_waitcnt lgkmcnt(8)
	s_barrier
	s_waitcnt lgkmcnt(0)
	s_setprio 1
	v_mfma_f32_16x16x32_bf16 v[126:129], v[150:153], v[166:169], v[126:129]
	v_mfma_f32_16x16x32_bf16 v[122:125], v[158:161], v[166:169], v[122:125]
	v_mfma_f32_16x16x32_bf16 v[110:113], v[150:153], v[174:177], v[110:113]
	v_mfma_f32_16x16x32_bf16 v[106:109], v[158:161], v[174:177], v[106:109]
	v_mfma_f32_16x16x32_bf16 v[94:97], v[150:153], v[182:185], v[94:97]
	v_mfma_f32_16x16x32_bf16 v[90:93], v[158:161], v[182:185], v[90:93]
	v_mfma_f32_16x16x32_bf16 v[78:81], v[150:153], v[194:197], v[78:81]
	v_mfma_f32_16x16x32_bf16 v[74:77], v[158:161], v[194:197], v[74:77]
	v_mfma_f32_16x16x32_bf16 v[126:129], v[154:157], v[170:173], v[126:129]
	v_mfma_f32_16x16x32_bf16 v[122:125], v[162:165], v[170:173], v[122:125]
	v_mfma_f32_16x16x32_bf16 v[110:113], v[154:157], v[178:181], v[110:113]
	v_mfma_f32_16x16x32_bf16 v[106:109], v[162:165], v[178:181], v[106:109]
	v_mfma_f32_16x16x32_bf16 v[94:97], v[154:157], v[186:189], v[94:97]
	v_mfma_f32_16x16x32_bf16 v[90:93], v[162:165], v[186:189], v[90:93]
	v_mfma_f32_16x16x32_bf16 v[78:81], v[154:157], v[198:201], v[78:81]
	v_mfma_f32_16x16x32_bf16 v[74:77], v[162:165], v[198:201], v[74:77]
	s_setprio 0
	s_barrier
	ds_read_b128 v[202:205], v145
	ds_read_b128 v[206:209], v146
	ds_read_b128 v[210:213], v147
	ds_read_b128 v[214:217], v148
	s_add_u32 s14, s18, 0x80
	s_mov_b32 m0, s41
	s_addc_u32 s15, s19, 0
	global_load_lds_dwordx4 v132, s[14:15]
	s_add_u32 s14, s18, 0x40080
	s_mov_b32 m0, s42
	s_addc_u32 s15, s19, 0
	global_load_lds_dwordx4 v132, s[14:15]
	s_barrier
	s_waitcnt lgkmcnt(0)
	s_setprio 1
	v_mfma_f32_16x16x32_bf16 v[118:121], v[202:205], v[166:169], v[118:121]
	v_mfma_f32_16x16x32_bf16 v[114:117], v[210:213], v[166:169], v[114:117]
	v_mfma_f32_16x16x32_bf16 v[102:105], v[202:205], v[174:177], v[102:105]
	v_mfma_f32_16x16x32_bf16 v[98:101], v[210:213], v[174:177], v[98:101]
	v_mfma_f32_16x16x32_bf16 v[86:89], v[202:205], v[182:185], v[86:89]
	v_mfma_f32_16x16x32_bf16 v[82:85], v[210:213], v[182:185], v[82:85]
	v_mfma_f32_16x16x32_bf16 v[70:73], v[202:205], v[194:197], v[70:73]
	v_mfma_f32_16x16x32_bf16 v[66:69], v[210:213], v[194:197], v[66:69]
	v_mfma_f32_16x16x32_bf16 v[118:121], v[206:209], v[170:173], v[118:121]
	v_mfma_f32_16x16x32_bf16 v[114:117], v[214:217], v[170:173], v[114:117]
	v_mfma_f32_16x16x32_bf16 v[102:105], v[206:209], v[178:181], v[102:105]
	v_mfma_f32_16x16x32_bf16 v[98:101], v[214:217], v[178:181], v[98:101]
	v_mfma_f32_16x16x32_bf16 v[86:89], v[206:209], v[186:189], v[86:89]
	v_mfma_f32_16x16x32_bf16 v[82:85], v[214:217], v[186:189], v[82:85]
	v_mfma_f32_16x16x32_bf16 v[70:73], v[206:209], v[198:201], v[70:73]
	v_mfma_f32_16x16x32_bf16 v[66:69], v[214:217], v[198:201], v[66:69]
	s_setprio 0
	s_barrier
	ds_read_b128 v[166:169], v149 offset:49152
	ds_read_b128 v[170:173], v149 offset:50176
	ds_read_b128 v[174:177], v149 offset:51200
	ds_read_b128 v[178:181], v149 offset:52224
	ds_read_b128 v[182:185], v149 offset:53248
	ds_read_b128 v[186:189], v149 offset:54272
	ds_read_b128 v[194:197], v149 offset:55296
	s_mov_b32 m0, s43
	ds_read_b128 v[198:201], v149 offset:56320
	global_load_lds_dwordx4 v1, s[22:23]
	s_add_u32 s14, s20, 0x40080
	s_mov_b32 m0, s44
	s_addc_u32 s15, s21, 0
	global_load_lds_dwordx4 v1, s[14:15]
	s_barrier
; __device__ __forceinline__ unsigned cvt_pk_bf16(float lo, float hi) { unsigned r; asm volatile("v_cvt_pk_bf16_f32 %0, %1, %2" : "=v"(r) : "v"(lo), "v"(hi)); return r; }
; #define PG8_STAGE(bufoff, gbase, voff) do { _Pragma("unroll") for (int _i = 0; _i < 2; ++_i) glds16_s((const void*)((const char*)(gbase) + _i * r64), (voff), ldsb + (unsigned)(bufoff) + ldsw + _i * 8192u); } while (0)
; #define PG8_WAIT_V(n) asm volatile("s_waitcnt vmcnt(" #n ")" ::: "memory")
; #define PG8_WAIT_L(n) asm volatile("s_waitcnt lgkmcnt(" #n ")" ::: "memory")
; #define PG8_BAR __builtin_amdgcn_s_barrier()
; #define PG8_SCHED __builtin_amdgcn_sched_barrier(0)
; #define PG8_HI do { if constexpr (FP8) asm volatile("s_setprio 1"); } while (0)
; #define PG8_LO do { if constexpr (FP8) asm volatile("s_setprio 0"); } while (0)
;     __device__ __forceinline__ void operator()(const f32x4 (&acc)[2][2][4][2], const Unit& u, int wr, int wc, int fr, int fq) const {
;         const int row0 = u.pm * BM + wr * 64 + fr, col0 = u.pn * HALF + wc * 32 + 8 * fq;
; #pragma unroll
;         for (int ai = 0; ai < 2; ++ai)
; #pragma unroll
;             for (int m = 0; m < 4; ++m) { bf16_t* rowp = O + (size_t)(row0 + ai * HALF + m * 16) * ldc + col0;
;                 f32x4 v[2];
; #pragma unroll
;                 for (int n = 0; n < 2; ++n) { const f32x4 g = acc[ai][0][m][n], up = acc[ai][1][m][n];
; #pragma unroll
;                     for (int j = 0; j < 4; ++j) { const float e = __builtin_amdgcn_exp2f(-1.4426950408889634f * g[j]); v[n][j] = g[j] * __builtin_amdgcn_rcpf(1.f + e) * up[j]; } }
;                 u32x4 w; w.x = cvt_pk_bf16(v[0][0], v[0][1]); w.y = cvt_pk_bf16(v[0][2], v[0][3]); w.z = cvt_pk_bf16(v[1][0], v[1][1]); w.w = cvt_pk_bf16(v[1][2], v[1][3]);
;                 *(u32x4*)rowp = w; }
; template <class Epi, class Sched, bool FP8 = false>
; __device__ __forceinline__ void gemm_phase(LAS unsigned char* lds, const int Kb, const int nt  , const Sched& S, const Epi& E) {
;     ...
;             PG8_BAR; PG8_HI; PG8_WAIT_L(0); PG8_MMA(1, 0, B0, B08); PG8_BAR; PG8_LO; PG8_SCHED;
;             PG8_STAGE(PG8_SB(1, 1), b3 + hstep, voffB);
;             PG8_WAIT_V(6); PG8_BAR; PG8_HI; PG8_MMA(1, 1, B1, B18); PG8_BAR; PG8_LO;
;         }
;         { int l_; asm volatile("v_mbcnt_lo_u32_b32 %0, -1, 0\n\tv_mbcnt_hi_u32_b32 %0, -1, %0" : "=v"(l_));
;           E(acc, cur, wr, wc, l_ & 15, l_ >> 4); }
	s_waitcnt lgkmcnt(0)
	s_setprio 1
	v_mfma_f32_16x16x32_bf16 v[62:65], v[150:153], v[166:169], v[62:65]
	v_mfma_f32_16x16x32_bf16 v[58:61], v[158:161], v[166:169], v[58:61]
	v_mfma_f32_16x16x32_bf16 v[46:49], v[150:153], v[174:177], v[46:49]
	v_mfma_f32_16x16x32_bf16 v[42:45], v[158:161], v[174:177], v[42:45]
	v_mfma_f32_16x16x32_bf16 v[30:33], v[150:153], v[182:185], v[30:33]
	v_mfma_f32_16x16x32_bf16 v[26:29], v[158:161], v[182:185], v[26:29]
	v_mfma_f32_16x16x32_bf16 v[14:17], v[150:153], v[194:197], v[14:17]
	v_mfma_f32_16x16x32_bf16 v[10:13], v[158:161], v[194:197], v[10:13]
	v_mfma_f32_16x16x32_bf16 v[62:65], v[154:157], v[170:173], v[62:65]
	v_mfma_f32_16x16x32_bf16 v[58:61], v[162:165], v[170:173], v[58:61]
	v_mfma_f32_16x16x32_bf16 v[46:49], v[154:157], v[178:181], v[46:49]
	v_mfma_f32_16x16x32_bf16 v[42:45], v[162:165], v[178:181], v[42:45]
	v_mfma_f32_16x16x32_bf16 v[30:33], v[154:157], v[186:189], v[30:33]
	v_mfma_f32_16x16x32_bf16 v[26:29], v[162:165], v[186:189], v[26:29]
	v_mfma_f32_16x16x32_bf16 v[14:17], v[154:157], v[198:201], v[14:17]
	v_mfma_f32_16x16x32_bf16 v[10:13], v[162:165], v[198:201], v[10:13]
	s_setprio 0
	s_barrier
	s_add_u32 s14, s18, 0x80080
	s_mov_b32 m0, s45
	s_addc_u32 s15, s19, 0
	global_load_lds_dwordx4 v132, s[14:15]
	s_add_u32 s14, s18, 0xc0080
	s_mov_b32 m0, s46
	s_addc_u32 s15, s19, 0
	global_load_lds_dwordx4 v132, s[14:15]
	s_waitcnt vmcnt(6)
	s_barrier
	s_setprio 1
	v_mfma_f32_16x16x32_bf16 v[54:57], v[202:205], v[166:169], v[54:57]
	v_mfma_f32_16x16x32_bf16 v[50:53], v[210:213], v[166:169], v[50:53]
	v_mfma_f32_16x16x32_bf16 v[38:41], v[202:205], v[174:177], v[38:41]
	v_mfma_f32_16x16x32_bf16 v[34:37], v[210:213], v[174:177], v[34:37]
	v_mfma_f32_16x16x32_bf16 v[22:25], v[202:205], v[182:185], v[22:25]
	v_mfma_f32_16x16x32_bf16 v[18:21], v[210:213], v[182:185], v[18:21]
	v_mfma_f32_16x16x32_bf16 v[6:9], v[202:205], v[194:197], v[6:9]
	v_mfma_f32_16x16x32_bf16 v[2:5], v[210:213], v[194:197], v[2:5]
	v_mfma_f32_16x16x32_bf16 v[54:57], v[206:209], v[170:173], v[54:57]
	v_mfma_f32_16x16x32_bf16 v[50:53], v[214:217], v[170:173], v[50:53]
	v_mfma_f32_16x16x32_bf16 v[38:41], v[206:209], v[178:181], v[38:41]
	v_mfma_f32_16x16x32_bf16 v[34:37], v[214:217], v[178:181], v[34:37]
	v_mfma_f32_16x16x32_bf16 v[22:25], v[206:209], v[186:189], v[22:25]
	v_mfma_f32_16x16x32_bf16 v[18:21], v[214:217], v[186:189], v[18:21]
	v_mfma_f32_16x16x32_bf16 v[6:9], v[206:209], v[198:201], v[6:9]
	v_mfma_f32_16x16x32_bf16 v[2:5], v[214:217], v[198:201], v[2:5]
	s_setprio 0
	s_add_i32 s53, s53, 2
	s_add_u32 s5, s5, 0x100
	s_addc_u32 s52, s52, 0
	s_cmp_gt_u32 s53, 29
	s_mov_b64 s[14:15], s[16:17]
	s_barrier
	s_cbranch_scc0 .LBB0_1946
	s_lshl_b32 s5, s12, 8
	v_mbcnt_lo_u32_b32 v130, -1, 0
	v_mbcnt_hi_u32_b32 v130, -1, v130
	s_add_i32 s5, s5, s39
	v_and_or_b32 v150, v130, 15, s5
	s_lshl_b32 s5, s51, 7
	v_ashrrev_i32_e32 v130, 1, v130
	s_or_b32 s5, s5, s40
	v_and_b32_e32 v130, -8, v130
	v_add_u32_e32 v152, s5, v130
	v_mul_f32_e32 v130, 0xbfb8aa3b, v126
	v_exp_f32_e32 v151, v130
	v_mul_f32_e32 v130, 0xbfb8aa3b, v127
	v_exp_f32_e32 v154, v130
	v_ashrrev_i32_e32 v153, 31, v152
	v_add_f32_e32 v151, 1.0, v151
	v_rcp_f32_e32 v151, v151
	v_add_f32_e32 v154, 1.0, v154
	v_rcp_f32_e32 v156, v154
	v_mov_b64_e32 v[130:131], s[2:3]
	v_mul_f32_e32 v126, v126, v151
	v_mul_f32_e32 v118, v126, v118
	v_mul_f32_e32 v126, v127, v156
	v_mul_f32_e32 v127, 0xbfb8aa3b, v128
	v_exp_f32_e32 v127, v127
	v_mul_f32_e32 v151, 0xbfb8aa3b, v129
	v_exp_f32_e32 v151, v151
	v_mul_f32_e32 v119, v126, v119
	v_add_f32_e32 v126, 1.0, v127
	v_rcp_f32_e32 v126, v126
	v_add_f32_e32 v127, 1.0, v151
	v_mul_f32_e32 v151, 0xbfb8aa3b, v122
	v_rcp_f32_e32 v127, v127
	v_exp_f32_e32 v151, v151
	v_mul_f32_e32 v126, v128, v126
	v_mul_f32_e32 v126, v126, v120
	v_mul_f32_e32 v120, v129, v127
	v_add_f32_e32 v127, 1.0, v151
	v_rcp_f32_e32 v127, v127
	v_mul_f32_e32 v128, 0xbfb8aa3b, v123
	v_mul_f32_e32 v129, v120, v121
	v_exp_f32_e32 v128, v128
	v_mul_f32_e32 v120, v122, v127
	v_mul_f32_e32 v122, v120, v114
	v_mul_f32_e32 v120, 0xbfb8aa3b, v124
	v_exp_f32_e32 v120, v120
	v_mul_f32_e32 v121, 0xbfb8aa3b, v125
	v_exp_f32_e32 v121, v121
	v_add_f32_e32 v114, 1.0, v128
	v_rcp_f32_e32 v114, v114
	v_add_f32_e32 v120, 1.0, v120
	v_rcp_f32_e32 v120, v120
	v_add_f32_e32 v121, 1.0, v121
	v_rcp_f32_e32 v121, v121
	v_mul_f32_e32 v114, v123, v114
	v_mul_f32_e32 v123, v114, v115
	v_mul_f32_e32 v114, v124, v120
	v_mul_f32_e32 v124, v114, v116
	v_mul_f32_e32 v114, v125, v121
	v_mad_i64_i32 v[154:155], s[14:15], v150, s49, v[130:131]
	v_mul_f32_e32 v125, v114, v117
	v_lshlrev_b64 v[114:115], 1, v[152:153]
	v_lshl_add_u64 v[120:121], v[154:155], 0, v[114:115]
	v_cvt_pk_bf16_f32 v116, v118, v119
	v_cvt_pk_bf16_f32 v117, v126, v129
	v_cvt_pk_bf16_f32 v118, v122, v123
	v_cvt_pk_bf16_f32 v119, v124, v125
	global_store_dwordx4 v[120:121], v[116:119], off
	s_and_b64 vcc, exec, s[6:7]
	s_mov_b32 s51, s50
	v_mul_f32_e32 v116, 0xbfb8aa3b, v110
	v_exp_f32_e32 v116, v116
	v_mul_f32_e32 v117, 0xbfb8aa3b, v111
	v_exp_f32_e32 v117, v117
	v_or_b32_e32 v118, 16, v150
	v_add_f32_e32 v116, 1.0, v116
	v_rcp_f32_e32 v119, v116
	v_add_f32_e32 v116, 1.0, v117
	v_rcp_f32_e32 v120, v116
	v_mad_i64_i32 v[116:117], s[14:15], v118, s49, v[130:131]
	v_mul_f32_e32 v110, v110, v119
	v_mul_f32_e32 v110, v110, v102
	v_mul_f32_e32 v102, v111, v120
	v_mul_f32_e32 v111, 0xbfb8aa3b, v112
	v_exp_f32_e32 v111, v111
	v_mul_f32_e32 v118, 0xbfb8aa3b, v113
	v_exp_f32_e32 v118, v118
	v_mul_f32_e32 v119, v102, v103
	v_add_f32_e32 v102, 1.0, v111
	v_rcp_f32_e32 v102, v102
	v_add_f32_e32 v103, 1.0, v118
	v_mul_f32_e32 v111, 0xbfb8aa3b, v106
; __device__ __forceinline__ unsigned cvt_pk_bf16(float lo, float hi) { unsigned r; asm volatile("v_cvt_pk_bf16_f32 %0, %1, %2" : "=v"(r) : "v"(lo), "v"(hi)); return r; }
;     __device__ __forceinline__ void operator()(const f32x4 (&acc)[2][2][4][2], const Unit& u, int wr, int wc, int fr, int fq) const {
;         const int row0 = u.pm * BM + wr * 64 + fr, col0 = u.pn * HALF + wc * 32 + 8 * fq;
; #pragma unroll
;         for (int ai = 0; ai < 2; ++ai)
; #pragma unroll
;             for (int m = 0; m < 4; ++m) { bf16_t* rowp = O + (size_t)(row0 + ai * HALF + m * 16) * ldc + col0;
;                 f32x4 v[2];
; #pragma unroll
;                 for (int n = 0; n < 2; ++n) { const f32x4 g = acc[ai][0][m][n], up = acc[ai][1][m][n];
; #pragma unroll
;                     for (int j = 0; j < 4; ++j) { const float e = __builtin_amdgcn_exp2f(-1.4426950408889634f * g[j]); v[n][j] = g[j] * __builtin_amdgcn_rcpf(1.f + e) * up[j]; } }
;                 u32x4 w; w.x = cvt_pk_bf16(v[0][0], v[0][1]); w.y = cvt_pk_bf16(v[0][2], v[0][3]); w.z = cvt_pk_bf16(v[1][0], v[1][1]); w.w = cvt_pk_bf16(v[1][2], v[1][3]);
;                 *(u32x4*)rowp = w; }
	v_rcp_f32_e32 v103, v103
	v_exp_f32_e32 v111, v111
	v_mul_f32_e32 v102, v112, v102
	v_mul_f32_e32 v104, v102, v104
	v_mul_f32_e32 v102, v113, v103
	v_add_f32_e32 v103, 1.0, v111
	v_rcp_f32_e32 v103, v103
	v_mul_f32_e32 v111, 0xbfb8aa3b, v107
	v_mul_f32_e32 v105, v102, v105
	v_exp_f32_e32 v111, v111
	v_mul_f32_e32 v102, v106, v103
	v_mul_f32_e32 v106, v102, v98
	v_mul_f32_e32 v102, 0xbfb8aa3b, v108
	v_exp_f32_e32 v102, v102
	v_mul_f32_e32 v103, 0xbfb8aa3b, v109
	v_exp_f32_e32 v103, v103
	v_add_f32_e32 v98, 1.0, v111
	v_rcp_f32_e32 v98, v98
	v_add_f32_e32 v102, 1.0, v102
	v_rcp_f32_e32 v102, v102
	v_add_f32_e32 v103, 1.0, v103
	v_rcp_f32_e32 v103, v103
	v_mul_f32_e32 v98, v107, v98
	v_mul_f32_e32 v107, v98, v99
	v_mul_f32_e32 v98, v108, v102
	v_mul_f32_e32 v108, v98, v100
	v_mul_f32_e32 v98, v109, v103
	v_mul_f32_e32 v101, v98, v101
	v_lshl_add_u64 v[102:103], v[116:117], 0, v[114:115]
	v_cvt_pk_bf16_f32 v98, v110, v119
	v_cvt_pk_bf16_f32 v99, v104, v105
	v_cvt_pk_bf16_f32 v100, v106, v107
	v_cvt_pk_bf16_f32 v101, v108, v101
	global_store_dwordx4 v[102:103], v[98:101], off
	s_mov_b32 s12, s4
	s_mov_b64 s[16:17], s[10:11]
	v_mul_f32_e32 v98, 0xbfb8aa3b, v94
	v_exp_f32_e32 v98, v98
	v_mul_f32_e32 v99, 0xbfb8aa3b, v95
	v_exp_f32_e32 v99, v99
	v_or_b32_e32 v100, 32, v150
	v_add_f32_e32 v98, 1.0, v98
	v_rcp_f32_e32 v101, v98
	v_add_f32_e32 v98, 1.0, v99
	v_rcp_f32_e32 v102, v98
	v_mad_i64_i32 v[98:99], s[14:15], v100, s49, v[130:131]
	v_mul_f32_e32 v94, v94, v101
	v_mul_f32_e32 v94, v94, v86
	v_mul_f32_e32 v86, v95, v102
	v_mul_f32_e32 v95, 0xbfb8aa3b, v96
	v_exp_f32_e32 v95, v95
	v_mul_f32_e32 v100, 0xbfb8aa3b, v97
	v_exp_f32_e32 v100, v100
	v_mul_f32_e32 v101, v86, v87
	v_add_f32_e32 v86, 1.0, v95
	v_rcp_f32_e32 v86, v86
	v_add_f32_e32 v87, 1.0, v100
	v_mul_f32_e32 v95, 0xbfb8aa3b, v90
	v_rcp_f32_e32 v87, v87
	v_exp_f32_e32 v95, v95
	v_mul_f32_e32 v86, v96, v86
	v_mul_f32_e32 v88, v86, v88
	v_mul_f32_e32 v86, v97, v87
	v_add_f32_e32 v87, 1.0, v95
	v_rcp_f32_e32 v87, v87
	v_mul_f32_e32 v95, 0xbfb8aa3b, v91
	v_mul_f32_e32 v89, v86, v89
	v_exp_f32_e32 v95, v95
	v_mul_f32_e32 v86, v90, v87
	v_mul_f32_e32 v90, v86, v82
	v_mul_f32_e32 v86, 0xbfb8aa3b, v92
	v_exp_f32_e32 v86, v86
	v_mul_f32_e32 v87, 0xbfb8aa3b, v93
	v_exp_f32_e32 v87, v87
	v_add_f32_e32 v82, 1.0, v95
	v_rcp_f32_e32 v82, v82
	v_add_f32_e32 v86, 1.0, v86
	v_rcp_f32_e32 v86, v86
	v_add_f32_e32 v87, 1.0, v87
	v_rcp_f32_e32 v87, v87
	v_mul_f32_e32 v82, v91, v82
	v_mul_f32_e32 v91, v82, v83
	v_mul_f32_e32 v82, v92, v86
	v_mul_f32_e32 v92, v82, v84
	v_mul_f32_e32 v82, v93, v87
	v_mul_f32_e32 v85, v82, v85
	v_lshl_add_u64 v[86:87], v[98:99], 0, v[114:115]
	v_cvt_pk_bf16_f32 v82, v94, v101
	v_cvt_pk_bf16_f32 v83, v88, v89
	v_cvt_pk_bf16_f32 v84, v90, v91
	v_cvt_pk_bf16_f32 v85, v92, v85
	global_store_dwordx4 v[86:87], v[82:85], off
	s_nop 1
	v_mul_f32_e32 v82, 0xbfb8aa3b, v78
	v_exp_f32_e32 v82, v82
	v_mul_f32_e32 v83, 0xbfb8aa3b, v79
	v_exp_f32_e32 v83, v83
	v_or_b32_e32 v84, 48, v150
	v_add_f32_e32 v82, 1.0, v82
	v_rcp_f32_e32 v85, v82
	v_add_f32_e32 v82, 1.0, v83
	v_rcp_f32_e32 v86, v82
	v_mad_i64_i32 v[82:83], s[14:15], v84, s49, v[130:131]
	v_mul_f32_e32 v78, v78, v85
	v_mul_f32_e32 v78, v78, v70
	v_mul_f32_e32 v70, v79, v86
	v_mul_f32_e32 v79, 0xbfb8aa3b, v80
	v_exp_f32_e32 v79, v79
	v_mul_f32_e32 v84, 0xbfb8aa3b, v81
	v_exp_f32_e32 v84, v84
	v_mul_f32_e32 v85, v70, v71
	v_add_f32_e32 v70, 1.0, v79
	v_rcp_f32_e32 v70, v70
	v_add_f32_e32 v71, 1.0, v84
	v_mul_f32_e32 v79, 0xbfb8aa3b, v74
	v_rcp_f32_e32 v71, v71
	v_exp_f32_e32 v79, v79
	v_mul_f32_e32 v70, v80, v70
	v_mul_f32_e32 v72, v70, v72
	v_mul_f32_e32 v70, v81, v71
	v_add_f32_e32 v71, 1.0, v79
	v_rcp_f32_e32 v71, v71
	v_mul_f32_e32 v79, 0xbfb8aa3b, v75
	v_mul_f32_e32 v73, v70, v73
	v_exp_f32_e32 v79, v79
	v_mul_f32_e32 v70, v74, v71
	v_mul_f32_e32 v74, v70, v66
	v_mul_f32_e32 v70, 0xbfb8aa3b, v76
	v_exp_f32_e32 v70, v70
	v_mul_f32_e32 v71, 0xbfb8aa3b, v77
	v_exp_f32_e32 v71, v71
	v_add_f32_e32 v66, 1.0, v79
	v_rcp_f32_e32 v66, v66
	v_add_f32_e32 v70, 1.0, v70
	v_rcp_f32_e32 v70, v70
	v_add_f32_e32 v71, 1.0, v71
	v_rcp_f32_e32 v71, v71
	v_mul_f32_e32 v66, v75, v66
	v_mul_f32_e32 v75, v66, v67
	v_mul_f32_e32 v66, v76, v70
	v_mul_f32_e32 v76, v66, v68
	v_mul_f32_e32 v66, v77, v71
	v_mul_f32_e32 v69, v66, v69
	v_lshl_add_u64 v[70:71], v[82:83], 0, v[114:115]
	v_cvt_pk_bf16_f32 v66, v78, v85
	v_cvt_pk_bf16_f32 v67, v72, v73
	v_cvt_pk_bf16_f32 v68, v74, v75
	v_cvt_pk_bf16_f32 v69, v76, v69
	global_store_dwordx4 v[70:71], v[66:69], off
	s_nop 1
	v_mul_f32_e32 v66, 0xbfb8aa3b, v62
	v_exp_f32_e32 v66, v66
	v_mul_f32_e32 v67, 0xbfb8aa3b, v63
	v_exp_f32_e32 v67, v67
	v_add_u32_e32 v68, 0x80, v150
	v_add_f32_e32 v66, 1.0, v66
	v_rcp_f32_e32 v69, v66
	v_add_f32_e32 v66, 1.0, v67
	v_rcp_f32_e32 v70, v66
	v_mad_i64_i32 v[66:67], s[14:15], v68, s49, v[130:131]
	v_mul_f32_e32 v62, v62, v69
	v_mul_f32_e32 v62, v62, v54
	v_mul_f32_e32 v54, v63, v70
	v_mul_f32_e32 v63, 0xbfb8aa3b, v64
	v_exp_f32_e32 v63, v63
	v_mul_f32_e32 v68, 0xbfb8aa3b, v65
	v_exp_f32_e32 v68, v68
	v_mul_f32_e32 v69, v54, v55
	v_add_f32_e32 v54, 1.0, v63
	v_rcp_f32_e32 v54, v54
	v_add_f32_e32 v55, 1.0, v68
	v_mul_f32_e32 v63, 0xbfb8aa3b, v58
	v_rcp_f32_e32 v55, v55
	v_exp_f32_e32 v63, v63
	v_mul_f32_e32 v54, v64, v54
	v_mul_f32_e32 v56, v54, v56
	v_mul_f32_e32 v54, v65, v55
	v_add_f32_e32 v55, 1.0, v63
	v_rcp_f32_e32 v55, v55
	v_mul_f32_e32 v63, 0xbfb8aa3b, v59
	v_mul_f32_e32 v57, v54, v57
	v_exp_f32_e32 v63, v63
	v_mul_f32_e32 v54, v58, v55
	v_mul_f32_e32 v58, v54, v50
	v_mul_f32_e32 v54, 0xbfb8aa3b, v60
	v_exp_f32_e32 v54, v54
	v_mul_f32_e32 v55, 0xbfb8aa3b, v61
	v_exp_f32_e32 v55, v55
; __device__ __forceinline__ unsigned cvt_pk_bf16(float lo, float hi) { unsigned r; asm volatile("v_cvt_pk_bf16_f32 %0, %1, %2" : "=v"(r) : "v"(lo), "v"(hi)); return r; }
; #define PG8_WAIT_V(n) asm volatile("s_waitcnt vmcnt(" #n ")" ::: "memory")
; #define PG8_BAR __builtin_amdgcn_s_barrier()
;     __device__ __forceinline__ void operator()(const f32x4 (&acc)[2][2][4][2], const Unit& u, int wr, int wc, int fr, int fq) const {
;         const int row0 = u.pm * BM + wr * 64 + fr, col0 = u.pn * HALF + wc * 32 + 8 * fq;
; #pragma unroll
;         for (int ai = 0; ai < 2; ++ai)
; #pragma unroll
;             for (int m = 0; m < 4; ++m) { bf16_t* rowp = O + (size_t)(row0 + ai * HALF + m * 16) * ldc + col0;
;                 f32x4 v[2];
; #pragma unroll
;                 for (int n = 0; n < 2; ++n) { const f32x4 g = acc[ai][0][m][n], up = acc[ai][1][m][n];
; #pragma unroll
;                     for (int j = 0; j < 4; ++j) { const float e = __builtin_amdgcn_exp2f(-1.4426950408889634f * g[j]); v[n][j] = g[j] * __builtin_amdgcn_rcpf(1.f + e) * up[j]; } }
;                 u32x4 w; w.x = cvt_pk_bf16(v[0][0], v[0][1]); w.y = cvt_pk_bf16(v[0][2], v[0][3]); w.z = cvt_pk_bf16(v[1][0], v[1][1]); w.w = cvt_pk_bf16(v[1][2], v[1][3]);
;                 *(u32x4*)rowp = w; }
; template <class Epi, class Sched, bool FP8 = false>
; __device__ __forceinline__ void gemm_phase(LAS unsigned char* lds, const int Kb, const int nt  , const Sched& S, const Epi& E) {
;     ...
;         if (!has_next) break;
; #pragma unroll
;         for (int a = 0; a < 2; ++a)
; #pragma unroll
;             for (int b = 0; b < 2; ++b)
; #pragma unroll
;                 for (int m = 0; m < 4; ++m)
; #pragma unroll
;                     for (int n = 0; n < 2; ++n) acc[a][b][m][n] = (f32x4){0.f, 0.f, 0.f, 0.f};
;         cur = nxt; cA = nA; cB = nB; ++ui;
;     }
;     PG8_WAIT_V(0);
;     if (wr == 0) PG8_BAR;
;     PG8_BAR;
	v_add_f32_e32 v50, 1.0, v63
	v_rcp_f32_e32 v50, v50
	v_add_f32_e32 v54, 1.0, v54
	v_rcp_f32_e32 v54, v54
	v_add_f32_e32 v55, 1.0, v55
	v_rcp_f32_e32 v55, v55
	v_mul_f32_e32 v50, v59, v50
	v_mul_f32_e32 v59, v50, v51
	v_mul_f32_e32 v50, v60, v54
	v_mul_f32_e32 v60, v50, v52
	v_mul_f32_e32 v50, v61, v55
	v_mul_f32_e32 v53, v50, v53
	v_lshl_add_u64 v[54:55], v[66:67], 0, v[114:115]
	v_cvt_pk_bf16_f32 v50, v62, v69
	v_cvt_pk_bf16_f32 v51, v56, v57
	v_cvt_pk_bf16_f32 v52, v58, v59
	v_cvt_pk_bf16_f32 v53, v60, v53
	global_store_dwordx4 v[54:55], v[50:53], off
	s_nop 1
	v_mul_f32_e32 v50, 0xbfb8aa3b, v46
	v_exp_f32_e32 v50, v50
	v_mul_f32_e32 v51, 0xbfb8aa3b, v47
	v_exp_f32_e32 v51, v51
	v_add_u32_e32 v52, 0x90, v150
	v_add_f32_e32 v50, 1.0, v50
	v_rcp_f32_e32 v53, v50
	v_add_f32_e32 v50, 1.0, v51
	v_rcp_f32_e32 v54, v50
	v_mad_i64_i32 v[50:51], s[14:15], v52, s49, v[130:131]
	v_mul_f32_e32 v46, v46, v53
	v_mul_f32_e32 v46, v46, v38
	v_mul_f32_e32 v38, v47, v54
	v_mul_f32_e32 v47, 0xbfb8aa3b, v48
	v_exp_f32_e32 v47, v47
	v_mul_f32_e32 v52, 0xbfb8aa3b, v49
	v_exp_f32_e32 v52, v52
	v_mul_f32_e32 v53, v38, v39
	v_add_f32_e32 v38, 1.0, v47
	v_rcp_f32_e32 v38, v38
	v_add_f32_e32 v39, 1.0, v52
	v_mul_f32_e32 v47, 0xbfb8aa3b, v42
	v_rcp_f32_e32 v39, v39
	v_exp_f32_e32 v47, v47
	v_mul_f32_e32 v38, v48, v38
	v_mul_f32_e32 v40, v38, v40
	v_mul_f32_e32 v38, v49, v39
	v_add_f32_e32 v39, 1.0, v47
	v_rcp_f32_e32 v39, v39
	v_mul_f32_e32 v47, 0xbfb8aa3b, v43
	v_mul_f32_e32 v41, v38, v41
	v_exp_f32_e32 v47, v47
	v_mul_f32_e32 v38, v42, v39
	v_mul_f32_e32 v42, v38, v34
	v_mul_f32_e32 v38, 0xbfb8aa3b, v44
	v_exp_f32_e32 v38, v38
	v_mul_f32_e32 v39, 0xbfb8aa3b, v45
	v_exp_f32_e32 v39, v39
	v_add_f32_e32 v34, 1.0, v47
	v_rcp_f32_e32 v34, v34
	v_add_f32_e32 v38, 1.0, v38
	v_rcp_f32_e32 v38, v38
	v_add_f32_e32 v39, 1.0, v39
	v_rcp_f32_e32 v39, v39
	v_mul_f32_e32 v34, v43, v34
	v_mul_f32_e32 v43, v34, v35
	v_mul_f32_e32 v34, v44, v38
	v_mul_f32_e32 v44, v34, v36
	v_mul_f32_e32 v34, v45, v39
	v_mul_f32_e32 v37, v34, v37
	v_lshl_add_u64 v[38:39], v[50:51], 0, v[114:115]
	v_cvt_pk_bf16_f32 v34, v46, v53
	v_cvt_pk_bf16_f32 v35, v40, v41
	v_cvt_pk_bf16_f32 v36, v42, v43
	v_cvt_pk_bf16_f32 v37, v44, v37
	global_store_dwordx4 v[38:39], v[34:37], off
	s_nop 1
	v_mul_f32_e32 v34, 0xbfb8aa3b, v30
	v_exp_f32_e32 v34, v34
	v_mul_f32_e32 v35, 0xbfb8aa3b, v31
	v_exp_f32_e32 v35, v35
	v_add_u32_e32 v36, 0xa0, v150
	v_add_f32_e32 v34, 1.0, v34
	v_rcp_f32_e32 v37, v34
	v_add_f32_e32 v34, 1.0, v35
	v_rcp_f32_e32 v38, v34
	v_mad_i64_i32 v[34:35], s[14:15], v36, s49, v[130:131]
	v_mul_f32_e32 v30, v30, v37
	v_mul_f32_e32 v30, v30, v22
	v_mul_f32_e32 v22, v31, v38
	v_mul_f32_e32 v31, 0xbfb8aa3b, v32
	v_exp_f32_e32 v31, v31
	v_mul_f32_e32 v36, 0xbfb8aa3b, v33
	v_exp_f32_e32 v36, v36
	v_mul_f32_e32 v37, v22, v23
	v_add_f32_e32 v22, 1.0, v31
	v_rcp_f32_e32 v22, v22
	v_add_f32_e32 v23, 1.0, v36
	v_mul_f32_e32 v31, 0xbfb8aa3b, v26
	v_rcp_f32_e32 v23, v23
	v_exp_f32_e32 v31, v31
	v_mul_f32_e32 v22, v32, v22
	v_mul_f32_e32 v24, v22, v24
	v_mul_f32_e32 v22, v33, v23
	v_add_f32_e32 v23, 1.0, v31
	v_rcp_f32_e32 v23, v23
	v_mul_f32_e32 v31, 0xbfb8aa3b, v27
	v_mul_f32_e32 v25, v22, v25
	v_exp_f32_e32 v31, v31
	v_mul_f32_e32 v22, v26, v23
	v_mul_f32_e32 v26, v22, v18
	v_mul_f32_e32 v22, 0xbfb8aa3b, v28
	v_exp_f32_e32 v22, v22
	v_mul_f32_e32 v23, 0xbfb8aa3b, v29
	v_exp_f32_e32 v23, v23
	v_add_f32_e32 v18, 1.0, v31
	v_rcp_f32_e32 v18, v18
	v_add_f32_e32 v22, 1.0, v22
	v_rcp_f32_e32 v22, v22
	v_add_f32_e32 v23, 1.0, v23
	v_rcp_f32_e32 v23, v23
	v_mul_f32_e32 v18, v27, v18
	v_mul_f32_e32 v27, v18, v19
	v_mul_f32_e32 v18, v28, v22
	v_mul_f32_e32 v28, v18, v20
	v_mul_f32_e32 v18, v29, v23
	v_mul_f32_e32 v21, v18, v21
	v_lshl_add_u64 v[22:23], v[34:35], 0, v[114:115]
	v_cvt_pk_bf16_f32 v18, v30, v37
	v_cvt_pk_bf16_f32 v19, v24, v25
	v_cvt_pk_bf16_f32 v20, v26, v27
	v_cvt_pk_bf16_f32 v21, v28, v21
	global_store_dwordx4 v[22:23], v[18:21], off
	s_nop 1
	v_mul_f32_e32 v18, 0xbfb8aa3b, v14
	v_exp_f32_e32 v18, v18
	v_mul_f32_e32 v19, 0xbfb8aa3b, v15
	v_exp_f32_e32 v19, v19
	v_add_u32_e32 v20, 0xb0, v150
	v_add_f32_e32 v18, 1.0, v18
	v_rcp_f32_e32 v21, v18
	v_add_f32_e32 v18, 1.0, v19
	v_rcp_f32_e32 v22, v18
	v_mad_i64_i32 v[18:19], s[14:15], v20, s49, v[130:131]
	v_mul_f32_e32 v14, v14, v21
	v_mul_f32_e32 v14, v14, v6
	v_mul_f32_e32 v6, v15, v22
	v_mul_f32_e32 v15, 0xbfb8aa3b, v16
	v_exp_f32_e32 v15, v15
	v_mul_f32_e32 v20, 0xbfb8aa3b, v17
	v_exp_f32_e32 v20, v20
	v_mul_f32_e32 v21, v6, v7
	v_add_f32_e32 v6, 1.0, v15
	v_rcp_f32_e32 v6, v6
	v_add_f32_e32 v7, 1.0, v20
	v_mul_f32_e32 v15, 0xbfb8aa3b, v10
	v_rcp_f32_e32 v7, v7
	v_exp_f32_e32 v15, v15
	v_mul_f32_e32 v6, v16, v6
	v_mul_f32_e32 v8, v6, v8
	v_mul_f32_e32 v6, v17, v7
	v_add_f32_e32 v7, 1.0, v15
	v_rcp_f32_e32 v7, v7
	v_mul_f32_e32 v15, 0xbfb8aa3b, v11
	v_mul_f32_e32 v9, v6, v9
	v_exp_f32_e32 v15, v15
	v_mul_f32_e32 v6, v10, v7
	v_mul_f32_e32 v10, v6, v2
	v_mul_f32_e32 v6, 0xbfb8aa3b, v12
	v_exp_f32_e32 v6, v6
	v_mul_f32_e32 v7, 0xbfb8aa3b, v13
	v_exp_f32_e32 v7, v7
	v_add_f32_e32 v2, 1.0, v15
	v_rcp_f32_e32 v2, v2
	v_add_f32_e32 v6, 1.0, v6
	v_rcp_f32_e32 v6, v6
	v_add_f32_e32 v7, 1.0, v7
	v_rcp_f32_e32 v7, v7
	v_mul_f32_e32 v2, v11, v2
	v_mul_f32_e32 v11, v2, v3
	v_mul_f32_e32 v2, v12, v6
	v_mul_f32_e32 v12, v2, v4
	v_mul_f32_e32 v2, v13, v7
	v_mul_f32_e32 v5, v2, v5
	v_lshl_add_u64 v[6:7], v[18:19], 0, v[114:115]
	s_mov_b64 s[14:15], s[8:9]
	v_cvt_pk_bf16_f32 v2, v14, v21
	v_cvt_pk_bf16_f32 v3, v8, v9
	v_cvt_pk_bf16_f32 v4, v10, v11
	v_cvt_pk_bf16_f32 v5, v12, v5
	global_store_dwordx4 v[6:7], v[2:5], off
	s_cbranch_vccz .LBB0_1943
	s_waitcnt vmcnt(0)
	s_cmpk_gt_u32 s24, 0xff
	s_cbranch_scc1 .LBB0_1950
	s_barrier

; #define PG8_STAGE(bufoff, gbase, voff) do { _Pragma("unroll") for (int _i = 0; _i < 2; ++_i) glds16_s((const void*)((const char*)(gbase) + _i * r64), (voff), ldsb + (unsigned)(bufoff) + ldsw + _i * 8192u); } while (0)
; #define PG8_LDA(b, h) do { _Pragma("unroll") for (int m = 0; m < 4; ++m) { const int o_ = PG8_SA(b, h) + aoff + m * 2048; \
;         if constexpr (FP8) A8[m] = PG8_CAT8(o_); else { At[m][0] = PG8_LD16(o_); At[m][1] = PG8_LD16(o_ + 1024); } } } while (0)
; #define PG8_LDB(X, X8, b, h) do { _Pragma("unroll") for (int n = 0; n < 2; ++n) { const int o_ = PG8_SB(b, h) + boff + n * 2048; \
;         if constexpr (FP8) X8[n] = PG8_CAT8(o_); else { X[n][0] = PG8_LD16(o_); X[n][1] = PG8_LD16(o_ + 1024); } } } while (0)
; #define PG8_WAIT_V(n) asm volatile("s_waitcnt vmcnt(" #n ")" ::: "memory")
; #define PG8_WAIT_L(n) asm volatile("s_waitcnt lgkmcnt(" #n ")" ::: "memory")
; #define PG8_BAR __builtin_amdgcn_s_barrier()
; #define PG8_SCHED __builtin_amdgcn_sched_barrier(0)
; #define PG8_HI do { if constexpr (FP8) asm volatile("s_setprio 1"); } while (0)
; #define PG8_LO do { if constexpr (FP8) asm volatile("s_setprio 0"); } while (0)
; template <class Epi, class Sched, bool FP8 = false>
; __device__ __forceinline__ void gemm_phase(LAS unsigned char* lds, const int Kb, const int nt  , const Sched& S, const Epi& E) {
;     ...
;         for (int t = 0; t < nt; t += 2) {
;             const bool last = (t == nt - 2);
;             const char* a1 = cA + (size_t)(t + 1) * kstep;
;             const char* a2 = last ? nA : cA + (size_t)(t + 2) * kstep; const char* b2 = last ? nB : cB + (size_t)(t + 2) * kstep;
;             const char* a3 = a2 + kstep; const char* b3 = b2 + kstep;
;             PG8_LDB(B0, B08, 0, 0); PG8_SCHED; PG8_LDA(0, 0); PG8_STAGE(PG8_SA(1, 1), a1 + hstep, voffA);
;             PG8_WAIT_L(8); PG8_BAR; PG8_HI; PG8_WAIT_L(0); PG8_MMA(0, 0, B0, B08); PG8_BAR; PG8_LO; PG8_SCHED;
;             PG8_LDB(B1, B18, 0, 1); PG8_STAGE(PG8_SB(0, 0), b2, voffB);
;             PG8_BAR; PG8_HI; PG8_WAIT_L(0); PG8_MMA(0, 1, B1, B18); PG8_BAR; PG8_LO;
;             PG8_LDA(0, 1); PG8_STAGE(PG8_SA(0, 0), a2, voffA);
;             PG8_BAR; PG8_HI; PG8_WAIT_L(0); PG8_MMA(1, 0, B0, B08); PG8_BAR; PG8_LO; PG8_SCHED;
;             PG8_STAGE(PG8_SB(0, 1), b2 + hstep, voffB);
;             PG8_WAIT_V(6); PG8_BAR; PG8_HI; PG8_MMA(1, 1, B1, B18); PG8_BAR; PG8_LO;
.LBB0_2043:
	ds_read_b128 v[150:153], v132
	ds_read_b128 v[154:157], v133
	ds_read_b128 v[158:161], v134
	ds_read_b128 v[162:165], v135
	s_add_u32 s22, s20, 0xffea0080
	s_addc_u32 s23, s21, -1
	s_cmpk_eq_i32 s59, 0x54
	s_cselect_b32 s24, s16, s22
	s_cselect_b32 s25, s17, s23
	s_cselect_b32 s22, s18, s57
	s_cselect_b32 s23, s19, s58
	s_add_u32 s26, s24, 0x80
	s_addc_u32 s27, s25, 0
	ds_read_b128 v[166:169], v148
	ds_read_b128 v[170:173], v148 offset:1024
	ds_read_b128 v[174:177], v148 offset:2048
	ds_read_b128 v[178:181], v148 offset:3072
	ds_read_b128 v[182:185], v148 offset:4096
	ds_read_b128 v[186:189], v148 offset:5120
	ds_read_b128 v[194:197], v148 offset:6144
	s_mov_b32 m0, s51
	ds_read_b128 v[198:201], v148 offset:7168
	global_load_lds_dwordx4 v1, s[20:21]
	s_add_u32 s60, s20, 0xb0000
	s_mov_b32 m0, s52
	s_addc_u32 s61, s21, 0
	global_load_lds_dwordx4 v1, s[60:61]
	s_waitcnt lgkmcnt(8)
	s_barrier
	s_waitcnt lgkmcnt(0)
	s_setprio 1
	v_mfma_f32_16x16x32_bf16 v[126:129], v[150:153], v[166:169], v[126:129]
	v_mfma_f32_16x16x32_bf16 v[122:125], v[158:161], v[166:169], v[122:125]
	v_mfma_f32_16x16x32_bf16 v[110:113], v[150:153], v[174:177], v[110:113]
	v_mfma_f32_16x16x32_bf16 v[106:109], v[158:161], v[174:177], v[106:109]
	v_mfma_f32_16x16x32_bf16 v[94:97], v[150:153], v[182:185], v[94:97]
	v_mfma_f32_16x16x32_bf16 v[90:93], v[158:161], v[182:185], v[90:93]
	v_mfma_f32_16x16x32_bf16 v[78:81], v[150:153], v[194:197], v[78:81]
	v_mfma_f32_16x16x32_bf16 v[74:77], v[158:161], v[194:197], v[74:77]
	v_mfma_f32_16x16x32_bf16 v[126:129], v[154:157], v[170:173], v[126:129]
	v_mfma_f32_16x16x32_bf16 v[122:125], v[162:165], v[170:173], v[122:125]
	v_mfma_f32_16x16x32_bf16 v[110:113], v[154:157], v[178:181], v[110:113]
	v_mfma_f32_16x16x32_bf16 v[106:109], v[162:165], v[178:181], v[106:109]
	v_mfma_f32_16x16x32_bf16 v[94:97], v[154:157], v[186:189], v[94:97]
	v_mfma_f32_16x16x32_bf16 v[90:93], v[162:165], v[186:189], v[90:93]
	v_mfma_f32_16x16x32_bf16 v[78:81], v[154:157], v[198:201], v[78:81]
	v_mfma_f32_16x16x32_bf16 v[74:77], v[162:165], v[198:201], v[74:77]
	s_setprio 0
	s_barrier
	ds_read_b128 v[202:205], v136
	ds_read_b128 v[206:209], v137
	ds_read_b128 v[210:213], v138
	s_mov_b32 m0, s36
	ds_read_b128 v[214:217], v139
	global_load_lds_dwordx4 v1, s[22:23]
	s_add_u32 s60, s22, 0xb0000
	s_mov_b32 m0, s37
	s_addc_u32 s61, s23, 0
	global_load_lds_dwordx4 v1, s[60:61]
	s_barrier
	s_waitcnt lgkmcnt(0)
	s_setprio 1
	v_mfma_f32_16x16x32_bf16 v[118:121], v[202:205], v[166:169], v[118:121]
	v_mfma_f32_16x16x32_bf16 v[114:117], v[210:213], v[166:169], v[114:117]
	v_mfma_f32_16x16x32_bf16 v[102:105], v[202:205], v[174:177], v[102:105]
	v_mfma_f32_16x16x32_bf16 v[98:101], v[210:213], v[174:177], v[98:101]
	v_mfma_f32_16x16x32_bf16 v[86:89], v[202:205], v[182:185], v[86:89]
	v_mfma_f32_16x16x32_bf16 v[82:85], v[210:213], v[182:185], v[82:85]
	v_mfma_f32_16x16x32_bf16 v[70:73], v[202:205], v[194:197], v[70:73]
	v_mfma_f32_16x16x32_bf16 v[66:69], v[210:213], v[194:197], v[66:69]
	v_mfma_f32_16x16x32_bf16 v[118:121], v[206:209], v[170:173], v[118:121]
	v_mfma_f32_16x16x32_bf16 v[114:117], v[214:217], v[170:173], v[114:117]
	v_mfma_f32_16x16x32_bf16 v[102:105], v[206:209], v[178:181], v[102:105]
	v_mfma_f32_16x16x32_bf16 v[98:101], v[214:217], v[178:181], v[98:101]
	v_mfma_f32_16x16x32_bf16 v[86:89], v[206:209], v[186:189], v[86:89]
	v_mfma_f32_16x16x32_bf16 v[82:85], v[214:217], v[186:189], v[82:85]
	v_mfma_f32_16x16x32_bf16 v[70:73], v[206:209], v[198:201], v[70:73]
	v_mfma_f32_16x16x32_bf16 v[66:69], v[214:217], v[198:201], v[66:69]
	s_setprio 0
	s_barrier
	ds_read_b128 v[166:169], v148 offset:16384
	ds_read_b128 v[170:173], v148 offset:17408
	ds_read_b128 v[174:177], v148 offset:18432
	ds_read_b128 v[178:181], v148 offset:19456
	ds_read_b128 v[182:185], v148 offset:20480
	ds_read_b128 v[186:189], v148 offset:21504
	ds_read_b128 v[194:197], v148 offset:22528
	s_mov_b32 m0, s35
	ds_read_b128 v[198:201], v148 offset:23552
	global_load_lds_dwordx4 v1, s[24:25]
	s_add_u32 s60, s24, 0xb0000
	s_mov_b32 m0, s38
	s_addc_u32 s61, s25, 0
	global_load_lds_dwordx4 v1, s[60:61]
	s_barrier
	s_waitcnt lgkmcnt(0)
	s_setprio 1
	v_mfma_f32_16x16x32_bf16 v[62:65], v[150:153], v[166:169], v[62:65]
	v_mfma_f32_16x16x32_bf16 v[58:61], v[158:161], v[166:169], v[58:61]
	v_mfma_f32_16x16x32_bf16 v[46:49], v[150:153], v[174:177], v[46:49]
	v_mfma_f32_16x16x32_bf16 v[42:45], v[158:161], v[174:177], v[42:45]
	v_mfma_f32_16x16x32_bf16 v[30:33], v[150:153], v[182:185], v[30:33]
	v_mfma_f32_16x16x32_bf16 v[26:29], v[158:161], v[182:185], v[26:29]
	v_mfma_f32_16x16x32_bf16 v[14:17], v[150:153], v[194:197], v[14:17]
	v_mfma_f32_16x16x32_bf16 v[10:13], v[158:161], v[194:197], v[10:13]
	v_mfma_f32_16x16x32_bf16 v[62:65], v[154:157], v[170:173], v[62:65]
	v_mfma_f32_16x16x32_bf16 v[58:61], v[162:165], v[170:173], v[58:61]
	v_mfma_f32_16x16x32_bf16 v[46:49], v[154:157], v[178:181], v[46:49]
	v_mfma_f32_16x16x32_bf16 v[42:45], v[162:165], v[178:181], v[42:45]
	v_mfma_f32_16x16x32_bf16 v[30:33], v[154:157], v[186:189], v[30:33]
	v_mfma_f32_16x16x32_bf16 v[26:29], v[162:165], v[186:189], v[26:29]
	v_mfma_f32_16x16x32_bf16 v[14:17], v[154:157], v[198:201], v[14:17]
	v_mfma_f32_16x16x32_bf16 v[10:13], v[162:165], v[198:201], v[10:13]
	s_setprio 0
	s_barrier
	s_add_u32 s60, s22, 0x160000
	s_mov_b32 m0, s39
	s_addc_u32 s61, s23, 0
	global_load_lds_dwordx4 v1, s[60:61]
	s_add_u32 s60, s22, 0x210000
	s_mov_b32 m0, s40
	s_addc_u32 s61, s23, 0
	global_load_lds_dwordx4 v1, s[60:61]
	s_waitcnt vmcnt(6)
	s_barrier
; #define PG8_STAGE(bufoff, gbase, voff) do { _Pragma("unroll") for (int _i = 0; _i < 2; ++_i) glds16_s((const void*)((const char*)(gbase) + _i * r64), (voff), ldsb + (unsigned)(bufoff) + ldsw + _i * 8192u); } while (0)
; #define PG8_LDA(b, h) do { _Pragma("unroll") for (int m = 0; m < 4; ++m) { const int o_ = PG8_SA(b, h) + aoff + m * 2048; \
;         if constexpr (FP8) A8[m] = PG8_CAT8(o_); else { At[m][0] = PG8_LD16(o_); At[m][1] = PG8_LD16(o_ + 1024); } } } while (0)
; #define PG8_LDB(X, X8, b, h) do { _Pragma("unroll") for (int n = 0; n < 2; ++n) { const int o_ = PG8_SB(b, h) + boff + n * 2048; \
;         if constexpr (FP8) X8[n] = PG8_CAT8(o_); else { X[n][0] = PG8_LD16(o_); X[n][1] = PG8_LD16(o_ + 1024); } } } while (0)
; #define PG8_WAIT_V(n) asm volatile("s_waitcnt vmcnt(" #n ")" ::: "memory")
; #define PG8_WAIT_L(n) asm volatile("s_waitcnt lgkmcnt(" #n ")" ::: "memory")
; #define PG8_BAR __builtin_amdgcn_s_barrier()
; #define PG8_SCHED __builtin_amdgcn_sched_barrier(0)
; #define PG8_HI do { if constexpr (FP8) asm volatile("s_setprio 1"); } while (0)
; #define PG8_LO do { if constexpr (FP8) asm volatile("s_setprio 0"); } while (0)
; template <class Epi, class Sched, bool FP8 = false>
; __device__ __forceinline__ void gemm_phase(LAS unsigned char* lds, const int Kb, const int nt  , const Sched& S, const Epi& E) {
;     ...
;             PG8_WAIT_V(6); PG8_BAR; PG8_HI; PG8_MMA(1, 1, B1, B18); PG8_BAR; PG8_LO;
;             PG8_LDB(B0, B08, 1, 0); PG8_SCHED; PG8_LDA(1, 0); PG8_STAGE(PG8_SA(0, 1), a2 + hstep, voffA);
;             PG8_WAIT_L(8); PG8_BAR; PG8_HI; PG8_WAIT_L(0); PG8_MMA(0, 0, B0, B08); PG8_BAR; PG8_LO; PG8_SCHED;
;             PG8_LDB(B1, B18, 1, 1); PG8_STAGE(PG8_SB(1, 0), b3, voffB);
;             PG8_BAR; PG8_HI; PG8_WAIT_L(0); PG8_MMA(0, 1, B1, B18); PG8_BAR; PG8_LO;
;             PG8_LDA(1, 1); PG8_STAGE(PG8_SA(1, 0), a3, voffA);
	s_setprio 1
	v_mfma_f32_16x16x32_bf16 v[54:57], v[202:205], v[166:169], v[54:57]
	v_mfma_f32_16x16x32_bf16 v[50:53], v[210:213], v[166:169], v[50:53]
	v_mfma_f32_16x16x32_bf16 v[38:41], v[202:205], v[174:177], v[38:41]
	v_mfma_f32_16x16x32_bf16 v[34:37], v[210:213], v[174:177], v[34:37]
	v_mfma_f32_16x16x32_bf16 v[22:25], v[202:205], v[182:185], v[22:25]
	v_mfma_f32_16x16x32_bf16 v[18:21], v[210:213], v[182:185], v[18:21]
	v_mfma_f32_16x16x32_bf16 v[6:9], v[202:205], v[194:197], v[6:9]
	v_mfma_f32_16x16x32_bf16 v[2:5], v[210:213], v[194:197], v[2:5]
	v_mfma_f32_16x16x32_bf16 v[54:57], v[206:209], v[170:173], v[54:57]
	v_mfma_f32_16x16x32_bf16 v[50:53], v[214:217], v[170:173], v[50:53]
	v_mfma_f32_16x16x32_bf16 v[38:41], v[206:209], v[178:181], v[38:41]
	v_mfma_f32_16x16x32_bf16 v[34:37], v[214:217], v[178:181], v[34:37]
	v_mfma_f32_16x16x32_bf16 v[22:25], v[206:209], v[186:189], v[22:25]
	v_mfma_f32_16x16x32_bf16 v[18:21], v[214:217], v[186:189], v[18:21]
	v_mfma_f32_16x16x32_bf16 v[6:9], v[206:209], v[198:201], v[6:9]
	v_mfma_f32_16x16x32_bf16 v[2:5], v[214:217], v[198:201], v[2:5]
	s_setprio 0
	s_barrier
	ds_read_b128 v[150:153], v140
	ds_read_b128 v[154:157], v141
	ds_read_b128 v[158:161], v142
	ds_read_b128 v[162:165], v143
	ds_read_b128 v[166:169], v148 offset:32768
	ds_read_b128 v[170:173], v148 offset:33792
	ds_read_b128 v[174:177], v148 offset:34816
	ds_read_b128 v[178:181], v148 offset:35840
	ds_read_b128 v[182:185], v148 offset:36864
	ds_read_b128 v[186:189], v148 offset:37888
	ds_read_b128 v[194:197], v148 offset:38912
	ds_read_b128 v[198:201], v148 offset:39936
	s_add_u32 s60, s24, 0x160000
	s_mov_b32 m0, s41
	s_addc_u32 s61, s25, 0
	global_load_lds_dwordx4 v1, s[60:61]
	s_add_u32 s60, s24, 0x210000
	s_mov_b32 m0, s42
	s_addc_u32 s61, s25, 0
	global_load_lds_dwordx4 v1, s[60:61]
	s_waitcnt lgkmcnt(8)
	s_barrier
	s_waitcnt lgkmcnt(0)
	s_setprio 1
	v_mfma_f32_16x16x32_bf16 v[126:129], v[150:153], v[166:169], v[126:129]
	v_mfma_f32_16x16x32_bf16 v[122:125], v[158:161], v[166:169], v[122:125]
	v_mfma_f32_16x16x32_bf16 v[110:113], v[150:153], v[174:177], v[110:113]
	v_mfma_f32_16x16x32_bf16 v[106:109], v[158:161], v[174:177], v[106:109]
	v_mfma_f32_16x16x32_bf16 v[94:97], v[150:153], v[182:185], v[94:97]
	v_mfma_f32_16x16x32_bf16 v[90:93], v[158:161], v[182:185], v[90:93]
	v_mfma_f32_16x16x32_bf16 v[78:81], v[150:153], v[194:197], v[78:81]
	v_mfma_f32_16x16x32_bf16 v[74:77], v[158:161], v[194:197], v[74:77]
	v_mfma_f32_16x16x32_bf16 v[126:129], v[154:157], v[170:173], v[126:129]
	v_mfma_f32_16x16x32_bf16 v[122:125], v[162:165], v[170:173], v[122:125]
	v_mfma_f32_16x16x32_bf16 v[110:113], v[154:157], v[178:181], v[110:113]
	v_mfma_f32_16x16x32_bf16 v[106:109], v[162:165], v[178:181], v[106:109]
	v_mfma_f32_16x16x32_bf16 v[94:97], v[154:157], v[186:189], v[94:97]
	v_mfma_f32_16x16x32_bf16 v[90:93], v[162:165], v[186:189], v[90:93]
	v_mfma_f32_16x16x32_bf16 v[78:81], v[154:157], v[198:201], v[78:81]
	v_mfma_f32_16x16x32_bf16 v[74:77], v[162:165], v[198:201], v[74:77]
	s_setprio 0
	s_barrier
	ds_read_b128 v[202:205], v144
	ds_read_b128 v[206:209], v145
	ds_read_b128 v[210:213], v146
	ds_read_b128 v[214:217], v147
	s_add_u32 s60, s22, 0x80
	s_mov_b32 m0, s45
	s_addc_u32 s61, s23, 0
	global_load_lds_dwordx4 v1, s[60:61]
	s_add_u32 s60, s22, 0xb0080
	s_mov_b32 m0, s46
	s_addc_u32 s61, s23, 0
	global_load_lds_dwordx4 v1, s[60:61]
	s_barrier
	s_waitcnt lgkmcnt(0)
	s_setprio 1
	v_mfma_f32_16x16x32_bf16 v[118:121], v[202:205], v[166:169], v[118:121]
	v_mfma_f32_16x16x32_bf16 v[114:117], v[210:213], v[166:169], v[114:117]
	v_mfma_f32_16x16x32_bf16 v[102:105], v[202:205], v[174:177], v[102:105]
	v_mfma_f32_16x16x32_bf16 v[98:101], v[210:213], v[174:177], v[98:101]
	v_mfma_f32_16x16x32_bf16 v[86:89], v[202:205], v[182:185], v[86:89]
	v_mfma_f32_16x16x32_bf16 v[82:85], v[210:213], v[182:185], v[82:85]
	v_mfma_f32_16x16x32_bf16 v[70:73], v[202:205], v[194:197], v[70:73]
	v_mfma_f32_16x16x32_bf16 v[66:69], v[210:213], v[194:197], v[66:69]
	v_mfma_f32_16x16x32_bf16 v[118:121], v[206:209], v[170:173], v[118:121]
	v_mfma_f32_16x16x32_bf16 v[114:117], v[214:217], v[170:173], v[114:117]
	v_mfma_f32_16x16x32_bf16 v[102:105], v[206:209], v[178:181], v[102:105]
	v_mfma_f32_16x16x32_bf16 v[98:101], v[214:217], v[178:181], v[98:101]
	v_mfma_f32_16x16x32_bf16 v[86:89], v[206:209], v[186:189], v[86:89]
	v_mfma_f32_16x16x32_bf16 v[82:85], v[214:217], v[186:189], v[82:85]
	v_mfma_f32_16x16x32_bf16 v[70:73], v[206:209], v[198:201], v[70:73]
	v_mfma_f32_16x16x32_bf16 v[66:69], v[214:217], v[198:201], v[66:69]
	s_setprio 0
	s_barrier
	ds_read_b128 v[166:169], v148 offset:49152
	ds_read_b128 v[170:173], v148 offset:50176
	ds_read_b128 v[174:177], v148 offset:51200
	ds_read_b128 v[178:181], v148 offset:52224
	ds_read_b128 v[182:185], v148 offset:53248
	ds_read_b128 v[186:189], v148 offset:54272
	ds_read_b128 v[194:197], v148 offset:55296
	s_mov_b32 m0, s47
	ds_read_b128 v[198:201], v148 offset:56320
	global_load_lds_dwordx4 v1, s[26:27]
	s_add_u32 s24, s24, 0xb0080
	s_mov_b32 m0, s48
	s_addc_u32 s25, s25, 0
	global_load_lds_dwordx4 v1, s[24:25]
	s_barrier
; #define PG8_STAGE(bufoff, gbase, voff) do { _Pragma("unroll") for (int _i = 0; _i < 2; ++_i) glds16_s((const void*)((const char*)(gbase) + _i * r64), (voff), ldsb + (unsigned)(bufoff) + ldsw + _i * 8192u); } while (0)
; #define PG8_LDA(b, h) do { _Pragma("unroll") for (int m = 0; m < 4; ++m) { const int o_ = PG8_SA(b, h) + aoff + m * 2048; \
;         if constexpr (FP8) A8[m] = PG8_CAT8(o_); else { At[m][0] = PG8_LD16(o_); At[m][1] = PG8_LD16(o_ + 1024); } } } while (0)
; #define PG8_WAIT_V(n) asm volatile("s_waitcnt vmcnt(" #n ")" ::: "memory")
; #define PG8_BAR __builtin_amdgcn_s_barrier()
;     __device__ __forceinline__ void operator()(const f32x4 (&acc)[2][2][4][2], const Unit& u, int wr, int wc, int fr, int fq) const {
;         const int row0 = u.pm * BM + wr * 64 + fr, col0 = u.pn * BM + wc * 32 + 4 * fq;
;         f32x4 cs[2][2];
; #pragma unroll
;         for (int bj = 0; bj < 2; ++bj)
; #pragma unroll
;             for (int n = 0; n < 2; ++n) cs[bj][n] = (cscale ? *(const f32x4*)(cscale + col0 + bj * HALF + n * 16) : (f32x4){1.f, 1.f, 1.f, 1.f}) * ascale;
; #pragma unroll
;         for (int ai = 0; ai < 2; ++ai)
; #pragma unroll
;             for (int m = 0; m < 4; ++m) { const size_t off = (size_t)(row0 + ai * HALF + m * 16) * ldc + col0;
; #pragma unroll
;                 for (int bj = 0; bj < 2; ++bj)
; #pragma unroll
;                     for (int n = 0; n < 2; ++n) { f32x4 v = acc[ai][bj][m][n] * cs[bj][n];
;                         if (res) v += *(const f32x4*)(res + off + bj * HALF + n * 16);
;                         *(f32x4*)(out + off + bj * HALF + n * 16) = v; }
; template <class Epi, class Sched, bool FP8 = false>
; __device__ __forceinline__ void gemm_phase(LAS unsigned char* lds, const int Kb, const int nt  , const Sched& S, const Epi& E) {
;     ...
;             PG8_WAIT_L(8); PG8_BAR; PG8_HI; PG8_WAIT_L(0); PG8_MMA(0, 0, B0, B08); PG8_BAR; PG8_LO; PG8_SCHED;
;             PG8_LDB(B1, B18, 1, 1); PG8_STAGE(PG8_SB(1, 0), b3, voffB);
;             PG8_BAR; PG8_HI; PG8_WAIT_L(0); PG8_MMA(0, 1, B1, B18); PG8_BAR; PG8_LO;
;             PG8_LDA(1, 1); PG8_STAGE(PG8_SA(1, 0), a3, voffA);
;             PG8_BAR; PG8_HI; PG8_WAIT_L(0); PG8_MMA(1, 0, B0, B08); PG8_BAR; PG8_LO; PG8_SCHED;
;             PG8_STAGE(PG8_SB(1, 1), b3 + hstep, voffB);
;             PG8_WAIT_V(6); PG8_BAR; PG8_HI; PG8_MMA(1, 1, B1, B18); PG8_BAR; PG8_LO;
	s_waitcnt lgkmcnt(0)
	s_setprio 1
	v_mfma_f32_16x16x32_bf16 v[62:65], v[150:153], v[166:169], v[62:65]
	v_mfma_f32_16x16x32_bf16 v[58:61], v[158:161], v[166:169], v[58:61]
	v_mfma_f32_16x16x32_bf16 v[46:49], v[150:153], v[174:177], v[46:49]
	v_mfma_f32_16x16x32_bf16 v[42:45], v[158:161], v[174:177], v[42:45]
	v_mfma_f32_16x16x32_bf16 v[30:33], v[150:153], v[182:185], v[30:33]
	v_mfma_f32_16x16x32_bf16 v[26:29], v[158:161], v[182:185], v[26:29]
	v_mfma_f32_16x16x32_bf16 v[14:17], v[150:153], v[194:197], v[14:17]
	v_mfma_f32_16x16x32_bf16 v[10:13], v[158:161], v[194:197], v[10:13]
	v_mfma_f32_16x16x32_bf16 v[62:65], v[154:157], v[170:173], v[62:65]
	v_mfma_f32_16x16x32_bf16 v[58:61], v[162:165], v[170:173], v[58:61]
	v_mfma_f32_16x16x32_bf16 v[46:49], v[154:157], v[178:181], v[46:49]
	v_mfma_f32_16x16x32_bf16 v[42:45], v[162:165], v[178:181], v[42:45]
	v_mfma_f32_16x16x32_bf16 v[30:33], v[154:157], v[186:189], v[30:33]
	v_mfma_f32_16x16x32_bf16 v[26:29], v[162:165], v[186:189], v[26:29]
	v_mfma_f32_16x16x32_bf16 v[14:17], v[154:157], v[198:201], v[14:17]
	v_mfma_f32_16x16x32_bf16 v[10:13], v[162:165], v[198:201], v[10:13]
	s_setprio 0
	s_barrier
	s_add_u32 s24, s22, 0x160080
	s_mov_b32 m0, s49
	s_addc_u32 s25, s23, 0
	global_load_lds_dwordx4 v1, s[24:25]
	s_add_u32 s22, s22, 0x210080
	s_mov_b32 m0, s50
	s_addc_u32 s23, s23, 0
	global_load_lds_dwordx4 v1, s[22:23]
	s_waitcnt vmcnt(6)
	s_barrier
	s_setprio 1
	v_mfma_f32_16x16x32_bf16 v[54:57], v[202:205], v[166:169], v[54:57]
	v_mfma_f32_16x16x32_bf16 v[50:53], v[210:213], v[166:169], v[50:53]
	v_mfma_f32_16x16x32_bf16 v[38:41], v[202:205], v[174:177], v[38:41]
	v_mfma_f32_16x16x32_bf16 v[34:37], v[210:213], v[174:177], v[34:37]
	v_mfma_f32_16x16x32_bf16 v[22:25], v[202:205], v[182:185], v[22:25]
	v_mfma_f32_16x16x32_bf16 v[18:21], v[210:213], v[182:185], v[18:21]
	v_mfma_f32_16x16x32_bf16 v[6:9], v[202:205], v[194:197], v[6:9]
	v_mfma_f32_16x16x32_bf16 v[2:5], v[210:213], v[194:197], v[2:5]
	v_mfma_f32_16x16x32_bf16 v[54:57], v[206:209], v[170:173], v[54:57]
	v_mfma_f32_16x16x32_bf16 v[50:53], v[214:217], v[170:173], v[50:53]
	v_mfma_f32_16x16x32_bf16 v[38:41], v[206:209], v[178:181], v[38:41]
	v_mfma_f32_16x16x32_bf16 v[34:37], v[214:217], v[178:181], v[34:37]
	v_mfma_f32_16x16x32_bf16 v[22:25], v[206:209], v[186:189], v[22:25]
	v_mfma_f32_16x16x32_bf16 v[18:21], v[214:217], v[186:189], v[18:21]
	v_mfma_f32_16x16x32_bf16 v[6:9], v[206:209], v[198:201], v[6:9]
	v_mfma_f32_16x16x32_bf16 v[2:5], v[214:217], v[198:201], v[2:5]
	s_setprio 0
	s_add_i32 s59, s59, 2
	s_add_u32 s20, s20, 0x100
	s_addc_u32 s21, s21, 0
	s_add_u32 s57, s57, 0x100
	s_addc_u32 s58, s58, 0
	s_cmpk_gt_u32 s59, 0x55
	s_barrier
	s_cbranch_scc0 .LBB0_2043
	s_lshl_b32 s20, s55, 8
	v_mbcnt_lo_u32_b32 v130, -1, 0
	v_mbcnt_hi_u32_b32 v130, -1, v130
	s_add_i32 s20, s20, s43
	s_lshl_b32 s21, s56, 8
	v_ashrrev_i32_e32 v131, 2, v130
	s_or_b32 s21, s21, s44
	v_and_b32_e32 v131, -4, v131
	v_and_or_b32 v168, v130, 15, s20
	v_add_u32_e32 v166, s21, v131
	v_ashrrev_i32_e32 v169, 31, v168
	v_ashrrev_i32_e32 v167, 31, v166
	v_lshlrev_b64 v[130:131], 11, v[168:169]
	v_lshl_add_u64 v[130:131], v[130:131], 0, v[166:167]
	v_lshlrev_b64 v[130:131], 2, v[130:131]
	v_lshl_add_u64 v[162:163], s[4:5], 0, v[130:131]
	global_load_dwordx4 v[150:153], v[162:163], off
	global_load_dwordx4 v[154:157], v[162:163], off offset:64
	global_load_dwordx4 v[158:161], v[162:163], off offset:512
	s_nop 0
	global_load_dwordx4 v[162:165], v[162:163], off offset:576
	v_or_b32_e32 v170, 16, v168
	v_ashrrev_i32_e32 v171, 31, v170
	v_lshlrev_b64 v[170:171], 11, v[170:171]
	v_lshl_add_u64 v[170:171], v[170:171], 0, v[166:167]
	v_lshl_add_u64 v[172:173], s[6:7], 0, v[130:131]
	v_lshlrev_b64 v[170:171], 2, v[170:171]
	v_lshl_add_u64 v[174:175], s[4:5], 0, v[170:171]
	s_and_b64 vcc, exec, s[14:15]
	s_mov_b32 s56, s54
	s_mov_b32 s55, s53
	s_mov_b64 s[22:23], s[18:19]
	s_mov_b64 s[20:21], s[16:17]
	s_waitcnt vmcnt(3)
	v_pk_add_f32 v[128:129], v[128:129], v[152:153]
	v_pk_add_f32 v[126:127], v[126:127], v[150:151]
	s_waitcnt vmcnt(2)
	v_pk_add_f32 v[124:125], v[124:125], v[156:157]
	v_pk_add_f32 v[122:123], v[122:123], v[154:155]
	s_waitcnt vmcnt(1)
	v_pk_add_f32 v[120:121], v[120:121], v[160:161]
	v_pk_add_f32 v[118:119], v[118:119], v[158:159]
	s_waitcnt vmcnt(0)
	v_pk_add_f32 v[116:117], v[116:117], v[164:165]
	v_pk_add_f32 v[114:115], v[114:115], v[162:163]
	global_store_dwordx4 v[172:173], v[126:129], off
	global_store_dwordx4 v[172:173], v[122:125], off offset:64
	global_store_dwordx4 v[172:173], v[118:121], off offset:512
	global_store_dwordx4 v[172:173], v[114:117], off offset:576
	global_load_dwordx4 v[114:117], v[174:175], off
	global_load_dwordx4 v[118:121], v[174:175], off offset:64
	global_load_dwordx4 v[122:125], v[174:175], off offset:512
	global_load_dwordx4 v[126:129], v[174:175], off offset:576
	v_or_b32_e32 v150, 32, v168
	v_ashrrev_i32_e32 v151, 31, v150
	v_lshlrev_b64 v[150:151], 11, v[150:151]
	v_lshl_add_u64 v[150:151], v[150:151], 0, v[166:167]
	v_lshl_add_u64 v[152:153], s[6:7], 0, v[170:171]
	v_lshlrev_b64 v[150:151], 2, v[150:151]
	v_lshl_add_u64 v[154:155], s[4:5], 0, v[150:151]
	s_waitcnt vmcnt(3)
	v_pk_add_f32 v[112:113], v[112:113], v[116:117]
	v_pk_add_f32 v[110:111], v[110:111], v[114:115]
	s_waitcnt vmcnt(2)
	v_pk_add_f32 v[108:109], v[108:109], v[120:121]
	v_pk_add_f32 v[106:107], v[106:107], v[118:119]
	s_waitcnt vmcnt(1)
	v_pk_add_f32 v[104:105], v[104:105], v[124:125]
	v_pk_add_f32 v[102:103], v[102:103], v[122:123]
	s_waitcnt vmcnt(0)
; #define PG8_WAIT_V(n) asm volatile("s_waitcnt vmcnt(" #n ")" ::: "memory")
; #define PG8_BAR __builtin_amdgcn_s_barrier()
;     __device__ __forceinline__ void operator()(const f32x4 (&acc)[2][2][4][2], const Unit& u, int wr, int wc, int fr, int fq) const {
;     ...
;             for (int m = 0; m < 4; ++m) { const size_t off = (size_t)(row0 + ai * HALF + m * 16) * ldc + col0;
; #pragma unroll
;                 for (int bj = 0; bj < 2; ++bj)
; #pragma unroll
;                     for (int n = 0; n < 2; ++n) { f32x4 v = acc[ai][bj][m][n] * cs[bj][n];
;                         if (res) v += *(const f32x4*)(res + off + bj * HALF + n * 16);
;                         *(f32x4*)(out + off + bj * HALF + n * 16) = v; }
;                 asm volatile("" ::: "memory"); }
; template <class Epi, class Sched, bool FP8 = false>
; __device__ __forceinline__ void gemm_phase(LAS unsigned char* lds, const int Kb, const int nt  , const Sched& S, const Epi& E) {
;     ...
;         if (!has_next) break;
; #pragma unroll
;         for (int a = 0; a < 2; ++a)
; #pragma unroll
;             for (int b = 0; b < 2; ++b)
; #pragma unroll
;                 for (int m = 0; m < 4; ++m)
; #pragma unroll
;                     for (int n = 0; n < 2; ++n) acc[a][b][m][n] = (f32x4){0.f, 0.f, 0.f, 0.f};
;         cur = nxt; cA = nA; cB = nB; ++ui;
;     }
;     PG8_WAIT_V(0);
;     if (wr == 0) PG8_BAR;
	v_pk_add_f32 v[100:101], v[100:101], v[128:129]
	v_pk_add_f32 v[98:99], v[98:99], v[126:127]
	global_store_dwordx4 v[152:153], v[110:113], off
	global_store_dwordx4 v[152:153], v[106:109], off offset:64
	global_store_dwordx4 v[152:153], v[102:105], off offset:512
	global_store_dwordx4 v[152:153], v[98:101], off offset:576
	global_load_dwordx4 v[98:101], v[154:155], off
	global_load_dwordx4 v[102:105], v[154:155], off offset:64
	global_load_dwordx4 v[106:109], v[154:155], off offset:512
	global_load_dwordx4 v[110:113], v[154:155], off offset:576
	v_or_b32_e32 v114, 48, v168
	v_ashrrev_i32_e32 v115, 31, v114
	v_lshlrev_b64 v[114:115], 11, v[114:115]
	v_lshl_add_u64 v[114:115], v[114:115], 0, v[166:167]
	v_lshl_add_u64 v[116:117], s[6:7], 0, v[150:151]
	v_lshlrev_b64 v[114:115], 2, v[114:115]
	v_lshl_add_u64 v[118:119], s[4:5], 0, v[114:115]
	s_waitcnt vmcnt(3)
	v_pk_add_f32 v[96:97], v[96:97], v[100:101]
	v_pk_add_f32 v[94:95], v[94:95], v[98:99]
	s_waitcnt vmcnt(2)
	v_pk_add_f32 v[92:93], v[92:93], v[104:105]
	v_pk_add_f32 v[90:91], v[90:91], v[102:103]
	s_waitcnt vmcnt(1)
	v_pk_add_f32 v[88:89], v[88:89], v[108:109]
	v_pk_add_f32 v[86:87], v[86:87], v[106:107]
	s_waitcnt vmcnt(0)
	v_pk_add_f32 v[84:85], v[84:85], v[112:113]
	v_pk_add_f32 v[82:83], v[82:83], v[110:111]
	global_store_dwordx4 v[116:117], v[94:97], off
	global_store_dwordx4 v[116:117], v[90:93], off offset:64
	global_store_dwordx4 v[116:117], v[86:89], off offset:512
	global_store_dwordx4 v[116:117], v[82:85], off offset:576
	global_load_dwordx4 v[82:85], v[118:119], off
	global_load_dwordx4 v[86:89], v[118:119], off offset:64
	global_load_dwordx4 v[90:93], v[118:119], off offset:512
	global_load_dwordx4 v[94:97], v[118:119], off offset:576
	v_lshl_add_u64 v[100:101], s[6:7], 0, v[114:115]
	v_lshl_add_u64 v[98:99], v[130:131], 0, s[8:9]
	v_lshl_add_u64 v[102:103], s[4:5], 0, v[98:99]
	s_waitcnt vmcnt(3)
	v_pk_add_f32 v[80:81], v[80:81], v[84:85]
	v_pk_add_f32 v[78:79], v[78:79], v[82:83]
	s_waitcnt vmcnt(2)
	v_pk_add_f32 v[76:77], v[76:77], v[88:89]
	v_pk_add_f32 v[74:75], v[74:75], v[86:87]
	s_waitcnt vmcnt(1)
	v_pk_add_f32 v[72:73], v[72:73], v[92:93]
	v_pk_add_f32 v[70:71], v[70:71], v[90:91]
	s_waitcnt vmcnt(0)
	v_pk_add_f32 v[68:69], v[68:69], v[96:97]
	v_pk_add_f32 v[66:67], v[66:67], v[94:95]
	global_store_dwordx4 v[100:101], v[78:81], off
	global_store_dwordx4 v[100:101], v[74:77], off offset:64
	global_store_dwordx4 v[100:101], v[70:73], off offset:512
	global_store_dwordx4 v[100:101], v[66:69], off offset:576
	global_load_dwordx4 v[66:69], v[102:103], off
	global_load_dwordx4 v[70:73], v[102:103], off offset:64
	global_load_dwordx4 v[74:77], v[102:103], off offset:512
	global_load_dwordx4 v[78:81], v[102:103], off offset:576
	v_lshl_add_u64 v[84:85], s[6:7], 0, v[98:99]
	v_lshl_add_u64 v[82:83], v[130:131], 0, s[10:11]
	v_lshl_add_u64 v[86:87], s[4:5], 0, v[82:83]
	s_waitcnt vmcnt(3)
	v_pk_add_f32 v[64:65], v[64:65], v[68:69]
	v_pk_add_f32 v[62:63], v[62:63], v[66:67]
	s_waitcnt vmcnt(2)
	v_pk_add_f32 v[60:61], v[60:61], v[72:73]
	v_pk_add_f32 v[58:59], v[58:59], v[70:71]
	s_waitcnt vmcnt(1)
	v_pk_add_f32 v[56:57], v[56:57], v[76:77]
	v_pk_add_f32 v[54:55], v[54:55], v[74:75]
	s_waitcnt vmcnt(0)
	v_pk_add_f32 v[52:53], v[52:53], v[80:81]
	v_pk_add_f32 v[50:51], v[50:51], v[78:79]
	global_store_dwordx4 v[84:85], v[62:65], off
	global_store_dwordx4 v[84:85], v[58:61], off offset:64
	global_store_dwordx4 v[84:85], v[54:57], off offset:512
	global_store_dwordx4 v[84:85], v[50:53], off offset:576
	global_load_dwordx4 v[50:53], v[86:87], off
	global_load_dwordx4 v[54:57], v[86:87], off offset:64
	global_load_dwordx4 v[58:61], v[86:87], off offset:512
	global_load_dwordx4 v[62:65], v[86:87], off offset:576
	v_lshl_add_u64 v[68:69], s[6:7], 0, v[82:83]
	v_lshl_add_u64 v[66:67], v[130:131], 0, s[12:13]
	v_lshl_add_u64 v[70:71], s[4:5], 0, v[66:67]
	s_waitcnt vmcnt(3)
	v_pk_add_f32 v[48:49], v[48:49], v[52:53]
	v_pk_add_f32 v[46:47], v[46:47], v[50:51]
	s_waitcnt vmcnt(2)
	v_pk_add_f32 v[44:45], v[44:45], v[56:57]
	v_pk_add_f32 v[42:43], v[42:43], v[54:55]
	s_waitcnt vmcnt(1)
	v_pk_add_f32 v[40:41], v[40:41], v[60:61]
	v_pk_add_f32 v[38:39], v[38:39], v[58:59]
	s_waitcnt vmcnt(0)
	v_pk_add_f32 v[36:37], v[36:37], v[64:65]
	v_pk_add_f32 v[34:35], v[34:35], v[62:63]
	global_store_dwordx4 v[68:69], v[46:49], off
	global_store_dwordx4 v[68:69], v[42:45], off offset:64
	global_store_dwordx4 v[68:69], v[38:41], off offset:512
	global_store_dwordx4 v[68:69], v[34:37], off offset:576
	global_load_dwordx4 v[34:37], v[70:71], off
	global_load_dwordx4 v[38:41], v[70:71], off offset:64
	global_load_dwordx4 v[42:45], v[70:71], off offset:512
	global_load_dwordx4 v[46:49], v[70:71], off offset:576
	v_lshl_add_u64 v[52:53], s[6:7], 0, v[66:67]
	v_lshl_add_u64 v[50:51], v[130:131], 0, s[2:3]
	v_lshl_add_u64 v[54:55], s[4:5], 0, v[50:51]
	s_waitcnt vmcnt(3)
	v_pk_add_f32 v[32:33], v[32:33], v[36:37]
	v_pk_add_f32 v[30:31], v[30:31], v[34:35]
	s_waitcnt vmcnt(2)
	v_pk_add_f32 v[28:29], v[28:29], v[40:41]
	v_pk_add_f32 v[26:27], v[26:27], v[38:39]
	s_waitcnt vmcnt(1)
	v_pk_add_f32 v[24:25], v[24:25], v[44:45]
	v_pk_add_f32 v[22:23], v[22:23], v[42:43]
	s_waitcnt vmcnt(0)
	v_pk_add_f32 v[20:21], v[20:21], v[48:49]
	v_pk_add_f32 v[18:19], v[18:19], v[46:47]
	global_store_dwordx4 v[52:53], v[30:33], off
	global_store_dwordx4 v[52:53], v[26:29], off offset:64
	global_store_dwordx4 v[52:53], v[22:25], off offset:512
	global_store_dwordx4 v[52:53], v[18:21], off offset:576
	global_load_dwordx4 v[18:21], v[54:55], off
	global_load_dwordx4 v[22:25], v[54:55], off offset:64
	global_load_dwordx4 v[26:29], v[54:55], off offset:512
	global_load_dwordx4 v[30:33], v[54:55], off offset:576
	v_lshl_add_u64 v[34:35], s[6:7], 0, v[50:51]
	s_waitcnt vmcnt(3)
	v_pk_add_f32 v[16:17], v[16:17], v[20:21]
	v_pk_add_f32 v[14:15], v[14:15], v[18:19]
	s_waitcnt vmcnt(2)
	v_pk_add_f32 v[12:13], v[12:13], v[24:25]
	v_pk_add_f32 v[10:11], v[10:11], v[22:23]
	s_waitcnt vmcnt(1)
	v_pk_add_f32 v[8:9], v[8:9], v[28:29]
	v_pk_add_f32 v[6:7], v[6:7], v[26:27]
	s_waitcnt vmcnt(0)
	v_pk_add_f32 v[4:5], v[4:5], v[32:33]
	v_pk_add_f32 v[2:3], v[2:3], v[30:31]
	global_store_dwordx4 v[34:35], v[14:17], off
	global_store_dwordx4 v[34:35], v[10:13], off offset:64
	global_store_dwordx4 v[34:35], v[6:9], off offset:512
	global_store_dwordx4 v[34:35], v[2:5], off offset:576
	s_cbranch_vccz .LBB0_2036
	s_waitcnt vmcnt(0)
	s_cmpk_gt_u32 s28, 0xff
	s_cbranch_scc1 .LBB0_2047
	s_barrier

;     __device__ __forceinline__ bool next(int i, Unit& u) const { if (!order_tile(i, G, c, nM, nN, u.pm, u.pn)) return false; u.A = A0 + (size_t)u.pm * tstep; u.B = B0 + (size_t)u.pn * tstep; return true; }
;     __device__ __forceinline__ bool next(int i, Unit& u) const { if (!order_tile(i, G, c, nM, nN, u.pm, u.pn)) return false; u.A = A0 + (size_t)(u.pn >> 1) * groupA + (size_t)u.pm * tstep; u.B = B0 + (size_t)u.pn * tstep; return true; }
; #define PG8_STAGE(bufoff, gbase, voff) do { _Pragma("unroll") for (int _i = 0; _i < 2; ++_i) glds16_s((const void*)((const char*)(gbase) + _i * r64), (voff), ldsb + (unsigned)(bufoff) + ldsw + _i * 8192u); } while (0)
; #define PG8_WAIT_V(n) asm volatile("s_waitcnt vmcnt(" #n ")" ::: "memory")
; #define PG8_WAIT_L(n) asm volatile("s_waitcnt lgkmcnt(" #n ")" ::: "memory")
; #define PG8_BAR __builtin_amdgcn_s_barrier()
; template <class Epi, class Sched, bool FP8 = false>
; __device__ __forceinline__ void gemm_phase(LAS unsigned char* lds, const int Kb, const int nt  , const Sched& S, const Epi& E) {
;     ...
;         const bool has_next = S.next(ui + 1, nxt);
;         const char* nA = has_next ? nxt.A : cA; const char* nB = has_next ? nxt.B : cB;
;         for (int t = 0; t < nt; t += 2) {
;             const bool last = (t == nt - 2);
;             const char* a1 = cA + (size_t)(t + 1) * kstep;
;             const char* a2 = last ? nA : cA + (size_t)(t + 2) * kstep; const char* b2 = last ? nB : cB + (size_t)(t + 2) * kstep;
;             const char* a3 = a2 + kstep; const char* b3 = b2 + kstep;
;             PG8_LDB(B0, B08, 0, 0); PG8_SCHED; PG8_LDA(0, 0); PG8_STAGE(PG8_SA(1, 1), a1 + hstep, voffA);
;             PG8_WAIT_L(8); PG8_BAR; PG8_HI; PG8_WAIT_L(0); PG8_MMA(0, 0, B0, B08); PG8_BAR; PG8_LO; PG8_SCHED;
;             PG8_LDB(B1, B18, 0, 1); PG8_STAGE(PG8_SB(0, 0), b2, voffB);
;             PG8_BAR; PG8_HI; PG8_WAIT_L(0); PG8_MMA(0, 1, B1, B18); PG8_BAR; PG8_LO;
;             PG8_LDA(0, 1); PG8_STAGE(PG8_SA(0, 0), a2, voffA);
;             PG8_BAR; PG8_HI; PG8_WAIT_L(0); PG8_MMA(1, 0, B0, B08); PG8_BAR; PG8_LO; PG8_SCHED;
;             PG8_STAGE(PG8_SB(0, 1), b2 + hstep, voffB);
;             PG8_WAIT_V(6); PG8_BAR; PG8_HI; PG8_MMA(1, 1, B1, B18); PG8_BAR; PG8_LO;
;             PG8_LDB(B0, B08, 1, 0); PG8_SCHED; PG8_LDA(1, 0); PG8_STAGE(PG8_SA(0, 1), a2 + hstep, voffA);
.LBB0_2332:
	ds_read_b128 v[130:133], v150
	ds_read_b128 v[134:137], v151
	ds_read_b128 v[138:141], v152
	ds_read_b128 v[142:145], v153
	s_add_u32 s28, s0, 0x100
	s_addc_u32 s29, s1, 0
	s_cmp_eq_u32 s63, 4
	s_cselect_b32 s34, s22, s28
	s_cselect_b32 s35, s23, s29
	s_cselect_b32 s30, s24, s21
	s_cselect_b32 s31, s25, s62
	s_add_u32 s36, s34, 0x80
	s_addc_u32 s37, s35, 0
	ds_read_b128 v[146:149], v166
	ds_read_b128 v[168:171], v166 offset:1024
	ds_read_b128 v[172:175], v166 offset:2048
	ds_read_b128 v[176:179], v166 offset:3072
	ds_read_b128 v[180:183], v166 offset:4096
	ds_read_b128 v[184:187], v166 offset:5120
	ds_read_b128 v[194:197], v166 offset:6144
	ds_read_b128 v[198:201], v166 offset:7168
	s_add_u32 s64, s0, 0x20080
	s_mov_b32 m0, s58
	s_addc_u32 s65, s1, 0
	global_load_lds_dwordx4 v1, s[64:65]
	s_add_u32 s0, s0, 0x30080
	s_mov_b32 m0, s59
	s_addc_u32 s1, s1, 0
	global_load_lds_dwordx4 v1, s[0:1]
	s_waitcnt lgkmcnt(8)
	s_barrier
	s_waitcnt lgkmcnt(0)
	s_setprio 1
	v_mfma_f32_16x16x32_bf16 v[126:129], v[130:133], v[146:149], v[126:129]
	v_mfma_f32_16x16x32_bf16 v[122:125], v[138:141], v[146:149], v[122:125]
	v_mfma_f32_16x16x32_bf16 v[110:113], v[130:133], v[172:175], v[110:113]
	v_mfma_f32_16x16x32_bf16 v[106:109], v[138:141], v[172:175], v[106:109]
	v_mfma_f32_16x16x32_bf16 v[94:97], v[130:133], v[180:183], v[94:97]
	v_mfma_f32_16x16x32_bf16 v[90:93], v[138:141], v[180:183], v[90:93]
	v_mfma_f32_16x16x32_bf16 v[78:81], v[130:133], v[194:197], v[78:81]
	v_mfma_f32_16x16x32_bf16 v[74:77], v[138:141], v[194:197], v[74:77]
	v_mfma_f32_16x16x32_bf16 v[126:129], v[134:137], v[168:171], v[126:129]
	v_mfma_f32_16x16x32_bf16 v[122:125], v[142:145], v[168:171], v[122:125]
	v_mfma_f32_16x16x32_bf16 v[110:113], v[134:137], v[176:179], v[110:113]
	v_mfma_f32_16x16x32_bf16 v[106:109], v[142:145], v[176:179], v[106:109]
	v_mfma_f32_16x16x32_bf16 v[94:97], v[134:137], v[184:187], v[94:97]
	v_mfma_f32_16x16x32_bf16 v[90:93], v[142:145], v[184:187], v[90:93]
	v_mfma_f32_16x16x32_bf16 v[78:81], v[134:137], v[198:201], v[78:81]
	v_mfma_f32_16x16x32_bf16 v[74:77], v[142:145], v[198:201], v[74:77]
	s_setprio 0
	s_barrier
	ds_read_b128 v[202:205], v154
	ds_read_b128 v[206:209], v155
	ds_read_b128 v[210:213], v156
	s_mov_b32 m0, s43
	ds_read_b128 v[214:217], v157
	global_load_lds_dwordx4 v1, s[30:31]
	s_add_u32 s0, s30, 0x10000
	s_mov_b32 m0, s44
	s_addc_u32 s1, s31, 0
	global_load_lds_dwordx4 v1, s[0:1]
	s_barrier
	s_waitcnt lgkmcnt(0)
	s_setprio 1
	v_mfma_f32_16x16x32_bf16 v[118:121], v[202:205], v[146:149], v[118:121]
	v_mfma_f32_16x16x32_bf16 v[114:117], v[210:213], v[146:149], v[114:117]
	v_mfma_f32_16x16x32_bf16 v[102:105], v[202:205], v[172:175], v[102:105]
	v_mfma_f32_16x16x32_bf16 v[98:101], v[210:213], v[172:175], v[98:101]
	v_mfma_f32_16x16x32_bf16 v[86:89], v[202:205], v[180:183], v[86:89]
	v_mfma_f32_16x16x32_bf16 v[82:85], v[210:213], v[180:183], v[82:85]
	v_mfma_f32_16x16x32_bf16 v[70:73], v[202:205], v[194:197], v[70:73]
	v_mfma_f32_16x16x32_bf16 v[66:69], v[210:213], v[194:197], v[66:69]
	v_mfma_f32_16x16x32_bf16 v[118:121], v[206:209], v[168:171], v[118:121]
	v_mfma_f32_16x16x32_bf16 v[114:117], v[214:217], v[168:171], v[114:117]
	v_mfma_f32_16x16x32_bf16 v[102:105], v[206:209], v[176:179], v[102:105]
	v_mfma_f32_16x16x32_bf16 v[98:101], v[214:217], v[176:179], v[98:101]
	v_mfma_f32_16x16x32_bf16 v[86:89], v[206:209], v[184:187], v[86:89]
	v_mfma_f32_16x16x32_bf16 v[82:85], v[214:217], v[184:187], v[82:85]
	v_mfma_f32_16x16x32_bf16 v[70:73], v[206:209], v[198:201], v[70:73]
	v_mfma_f32_16x16x32_bf16 v[66:69], v[214:217], v[198:201], v[66:69]
	s_setprio 0
	s_barrier
	ds_read_b128 v[146:149], v166 offset:16384
	ds_read_b128 v[168:171], v166 offset:17408
	ds_read_b128 v[172:175], v166 offset:18432
	ds_read_b128 v[176:179], v166 offset:19456
	ds_read_b128 v[180:183], v166 offset:20480
	ds_read_b128 v[184:187], v166 offset:21504
	ds_read_b128 v[194:197], v166 offset:22528
	s_mov_b32 m0, s42
	ds_read_b128 v[198:201], v166 offset:23552
	global_load_lds_dwordx4 v1, s[34:35]
	s_add_u32 s0, s34, 0x10000
	s_mov_b32 m0, s45
	s_addc_u32 s1, s35, 0
	global_load_lds_dwordx4 v1, s[0:1]
	s_barrier
	s_waitcnt lgkmcnt(0)
	s_setprio 1
	v_mfma_f32_16x16x32_bf16 v[62:65], v[130:133], v[146:149], v[62:65]
	v_mfma_f32_16x16x32_bf16 v[58:61], v[138:141], v[146:149], v[58:61]
	v_mfma_f32_16x16x32_bf16 v[46:49], v[130:133], v[172:175], v[46:49]
	v_mfma_f32_16x16x32_bf16 v[42:45], v[138:141], v[172:175], v[42:45]
	v_mfma_f32_16x16x32_bf16 v[30:33], v[130:133], v[180:183], v[30:33]
	v_mfma_f32_16x16x32_bf16 v[26:29], v[138:141], v[180:183], v[26:29]
	v_mfma_f32_16x16x32_bf16 v[14:17], v[130:133], v[194:197], v[14:17]
	v_mfma_f32_16x16x32_bf16 v[10:13], v[138:141], v[194:197], v[10:13]
	v_mfma_f32_16x16x32_bf16 v[62:65], v[134:137], v[168:171], v[62:65]
	v_mfma_f32_16x16x32_bf16 v[58:61], v[142:145], v[168:171], v[58:61]
	v_mfma_f32_16x16x32_bf16 v[46:49], v[134:137], v[176:179], v[46:49]
	v_mfma_f32_16x16x32_bf16 v[42:45], v[142:145], v[176:179], v[42:45]
	v_mfma_f32_16x16x32_bf16 v[30:33], v[134:137], v[184:187], v[30:33]
	v_mfma_f32_16x16x32_bf16 v[26:29], v[142:145], v[184:187], v[26:29]
	v_mfma_f32_16x16x32_bf16 v[14:17], v[134:137], v[198:201], v[14:17]
	v_mfma_f32_16x16x32_bf16 v[10:13], v[142:145], v[198:201], v[10:13]
	s_setprio 0
	s_barrier
	s_add_u32 s0, s30, 0x20000
	s_mov_b32 m0, s46
	s_addc_u32 s1, s31, 0
	global_load_lds_dwordx4 v1, s[0:1]
	s_add_u32 s0, s30, 0x30000
	s_mov_b32 m0, s47
	s_addc_u32 s1, s31, 0
	global_load_lds_dwordx4 v1, s[0:1]
	s_waitcnt vmcnt(6)
	s_barrier
; #define PG8_STAGE(bufoff, gbase, voff) do { _Pragma("unroll") for (int _i = 0; _i < 2; ++_i) glds16_s((const void*)((const char*)(gbase) + _i * r64), (voff), ldsb + (unsigned)(bufoff) + ldsw + _i * 8192u); } while (0)
; #define PG8_LDA(b, h) do { _Pragma("unroll") for (int m = 0; m < 4; ++m) { const int o_ = PG8_SA(b, h) + aoff + m * 2048; \
;         if constexpr (FP8) A8[m] = PG8_CAT8(o_); else { At[m][0] = PG8_LD16(o_); At[m][1] = PG8_LD16(o_ + 1024); } } } while (0)
; #define PG8_LDB(X, X8, b, h) do { _Pragma("unroll") for (int n = 0; n < 2; ++n) { const int o_ = PG8_SB(b, h) + boff + n * 2048; \
;         if constexpr (FP8) X8[n] = PG8_CAT8(o_); else { X[n][0] = PG8_LD16(o_); X[n][1] = PG8_LD16(o_ + 1024); } } } while (0)
; #define PG8_WAIT_V(n) asm volatile("s_waitcnt vmcnt(" #n ")" ::: "memory")
; #define PG8_WAIT_L(n) asm volatile("s_waitcnt lgkmcnt(" #n ")" ::: "memory")
; #define PG8_BAR __builtin_amdgcn_s_barrier()
; #define PG8_SCHED __builtin_amdgcn_sched_barrier(0)
; #define PG8_HI do { if constexpr (FP8) asm volatile("s_setprio 1"); } while (0)
; #define PG8_LO do { if constexpr (FP8) asm volatile("s_setprio 0"); } while (0)
; template <class Epi, class Sched, bool FP8 = false>
; __device__ __forceinline__ void gemm_phase(LAS unsigned char* lds, const int Kb, const int nt  , const Sched& S, const Epi& E) {
;     ...
;             PG8_WAIT_V(6); PG8_BAR; PG8_HI; PG8_MMA(1, 1, B1, B18); PG8_BAR; PG8_LO;
;             PG8_LDB(B0, B08, 1, 0); PG8_SCHED; PG8_LDA(1, 0); PG8_STAGE(PG8_SA(0, 1), a2 + hstep, voffA);
;             PG8_WAIT_L(8); PG8_BAR; PG8_HI; PG8_WAIT_L(0); PG8_MMA(0, 0, B0, B08); PG8_BAR; PG8_LO; PG8_SCHED;
;             PG8_LDB(B1, B18, 1, 1); PG8_STAGE(PG8_SB(1, 0), b3, voffB);
;             PG8_BAR; PG8_HI; PG8_WAIT_L(0); PG8_MMA(0, 1, B1, B18); PG8_BAR; PG8_LO;
;             PG8_LDA(1, 1); PG8_STAGE(PG8_SA(1, 0), a3, voffA);
;             PG8_BAR; PG8_HI; PG8_WAIT_L(0); PG8_MMA(1, 0, B0, B08); PG8_BAR; PG8_LO; PG8_SCHED;
	s_setprio 1
	v_mfma_f32_16x16x32_bf16 v[54:57], v[202:205], v[146:149], v[54:57]
	v_mfma_f32_16x16x32_bf16 v[50:53], v[210:213], v[146:149], v[50:53]
	v_mfma_f32_16x16x32_bf16 v[38:41], v[202:205], v[172:175], v[38:41]
	v_mfma_f32_16x16x32_bf16 v[34:37], v[210:213], v[172:175], v[34:37]
	v_mfma_f32_16x16x32_bf16 v[22:25], v[202:205], v[180:183], v[22:25]
	v_mfma_f32_16x16x32_bf16 v[18:21], v[210:213], v[180:183], v[18:21]
	v_mfma_f32_16x16x32_bf16 v[6:9], v[202:205], v[194:197], v[6:9]
	v_mfma_f32_16x16x32_bf16 v[2:5], v[210:213], v[194:197], v[2:5]
	v_mfma_f32_16x16x32_bf16 v[54:57], v[206:209], v[168:171], v[54:57]
	v_mfma_f32_16x16x32_bf16 v[50:53], v[214:217], v[168:171], v[50:53]
	v_mfma_f32_16x16x32_bf16 v[38:41], v[206:209], v[176:179], v[38:41]
	v_mfma_f32_16x16x32_bf16 v[34:37], v[214:217], v[176:179], v[34:37]
	v_mfma_f32_16x16x32_bf16 v[22:25], v[206:209], v[184:187], v[22:25]
	v_mfma_f32_16x16x32_bf16 v[18:21], v[214:217], v[184:187], v[18:21]
	v_mfma_f32_16x16x32_bf16 v[6:9], v[206:209], v[198:201], v[6:9]
	v_mfma_f32_16x16x32_bf16 v[2:5], v[214:217], v[198:201], v[2:5]
	s_setprio 0
	s_barrier
	ds_read_b128 v[130:133], v158
	ds_read_b128 v[134:137], v159
	ds_read_b128 v[138:141], v160
	ds_read_b128 v[142:145], v161
	ds_read_b128 v[146:149], v166 offset:32768
	ds_read_b128 v[168:171], v166 offset:33792
	ds_read_b128 v[172:175], v166 offset:34816
	ds_read_b128 v[176:179], v166 offset:35840
	ds_read_b128 v[180:183], v166 offset:36864
	ds_read_b128 v[184:187], v166 offset:37888
	ds_read_b128 v[194:197], v166 offset:38912
	ds_read_b128 v[198:201], v166 offset:39936
	s_add_u32 s0, s34, 0x20000
	s_mov_b32 m0, s48
	s_addc_u32 s1, s35, 0
	global_load_lds_dwordx4 v1, s[0:1]
	s_add_u32 s0, s34, 0x30000
	s_mov_b32 m0, s49
	s_addc_u32 s1, s35, 0
	global_load_lds_dwordx4 v1, s[0:1]
	s_waitcnt lgkmcnt(8)
	s_barrier
	s_waitcnt lgkmcnt(0)
	s_setprio 1
	v_mfma_f32_16x16x32_bf16 v[126:129], v[130:133], v[146:149], v[126:129]
	v_mfma_f32_16x16x32_bf16 v[122:125], v[138:141], v[146:149], v[122:125]
	v_mfma_f32_16x16x32_bf16 v[110:113], v[130:133], v[172:175], v[110:113]
	v_mfma_f32_16x16x32_bf16 v[106:109], v[138:141], v[172:175], v[106:109]
	v_mfma_f32_16x16x32_bf16 v[94:97], v[130:133], v[180:183], v[94:97]
	v_mfma_f32_16x16x32_bf16 v[90:93], v[138:141], v[180:183], v[90:93]
	v_mfma_f32_16x16x32_bf16 v[78:81], v[130:133], v[194:197], v[78:81]
	v_mfma_f32_16x16x32_bf16 v[74:77], v[138:141], v[194:197], v[74:77]
	v_mfma_f32_16x16x32_bf16 v[126:129], v[134:137], v[168:171], v[126:129]
	v_mfma_f32_16x16x32_bf16 v[122:125], v[142:145], v[168:171], v[122:125]
	v_mfma_f32_16x16x32_bf16 v[110:113], v[134:137], v[176:179], v[110:113]
	v_mfma_f32_16x16x32_bf16 v[106:109], v[142:145], v[176:179], v[106:109]
	v_mfma_f32_16x16x32_bf16 v[94:97], v[134:137], v[184:187], v[94:97]
	v_mfma_f32_16x16x32_bf16 v[90:93], v[142:145], v[184:187], v[90:93]
	v_mfma_f32_16x16x32_bf16 v[78:81], v[134:137], v[198:201], v[78:81]
	v_mfma_f32_16x16x32_bf16 v[74:77], v[142:145], v[198:201], v[74:77]
	s_setprio 0
	s_barrier
	ds_read_b128 v[202:205], v162
	ds_read_b128 v[206:209], v163
	ds_read_b128 v[210:213], v164
	ds_read_b128 v[214:217], v165
	s_add_u32 s0, s30, 0x80
	s_mov_b32 m0, s52
	s_addc_u32 s1, s31, 0
	global_load_lds_dwordx4 v1, s[0:1]
	s_add_u32 s0, s30, 0x10080
	s_mov_b32 m0, s53
	s_addc_u32 s1, s31, 0
	global_load_lds_dwordx4 v1, s[0:1]
	s_barrier
	s_waitcnt lgkmcnt(0)
	s_setprio 1
	v_mfma_f32_16x16x32_bf16 v[118:121], v[202:205], v[146:149], v[118:121]
	v_mfma_f32_16x16x32_bf16 v[114:117], v[210:213], v[146:149], v[114:117]
	v_mfma_f32_16x16x32_bf16 v[102:105], v[202:205], v[172:175], v[102:105]
	v_mfma_f32_16x16x32_bf16 v[98:101], v[210:213], v[172:175], v[98:101]
	v_mfma_f32_16x16x32_bf16 v[86:89], v[202:205], v[180:183], v[86:89]
	v_mfma_f32_16x16x32_bf16 v[82:85], v[210:213], v[180:183], v[82:85]
	v_mfma_f32_16x16x32_bf16 v[70:73], v[202:205], v[194:197], v[70:73]
	v_mfma_f32_16x16x32_bf16 v[66:69], v[210:213], v[194:197], v[66:69]
	v_mfma_f32_16x16x32_bf16 v[118:121], v[206:209], v[168:171], v[118:121]
	v_mfma_f32_16x16x32_bf16 v[114:117], v[214:217], v[168:171], v[114:117]
	v_mfma_f32_16x16x32_bf16 v[102:105], v[206:209], v[176:179], v[102:105]
	v_mfma_f32_16x16x32_bf16 v[98:101], v[214:217], v[176:179], v[98:101]
	v_mfma_f32_16x16x32_bf16 v[86:89], v[206:209], v[184:187], v[86:89]
	v_mfma_f32_16x16x32_bf16 v[82:85], v[214:217], v[184:187], v[82:85]
	v_mfma_f32_16x16x32_bf16 v[70:73], v[206:209], v[198:201], v[70:73]
	v_mfma_f32_16x16x32_bf16 v[66:69], v[214:217], v[198:201], v[66:69]
	s_setprio 0
	s_barrier
; #define PG8_STAGE(bufoff, gbase, voff) do { _Pragma("unroll") for (int _i = 0; _i < 2; ++_i) glds16_s((const void*)((const char*)(gbase) + _i * r64), (voff), ldsb + (unsigned)(bufoff) + ldsw + _i * 8192u); } while (0)
; #define PG8_WAIT_V(n) asm volatile("s_waitcnt vmcnt(" #n ")" ::: "memory")
; #define PG8_WAIT_L(n) asm volatile("s_waitcnt lgkmcnt(" #n ")" ::: "memory")
; #define PG8_BAR __builtin_amdgcn_s_barrier()
; #define PG8_SCHED __builtin_amdgcn_sched_barrier(0)
; #define PG8_HI do { if constexpr (FP8) asm volatile("s_setprio 1"); } while (0)
; #define PG8_LO do { if constexpr (FP8) asm volatile("s_setprio 0"); } while (0)
;     __device__ __forceinline__ void operator()(const f32x4 (&acc)[2][2][4][2], const Unit& u, int wr, int wc, int fr, int fq) const {
;         const int row0 = u.pm * BM + wr * 64 + fr, col0 = u.pn * BM + wc * 32 + 4 * fq;
;         f32x4 cs[2][2];
; #pragma unroll
;         for (int bj = 0; bj < 2; ++bj)
; #pragma unroll
;             for (int n = 0; n < 2; ++n) cs[bj][n] = (cscale ? *(const f32x4*)(cscale + col0 + bj * HALF + n * 16) : (f32x4){1.f, 1.f, 1.f, 1.f}) * ascale;
; template <class Epi, class Sched, bool FP8 = false>
; __device__ __forceinline__ void gemm_phase(LAS unsigned char* lds, const int Kb, const int nt  , const Sched& S, const Epi& E) {
;     ...
;             PG8_BAR; PG8_HI; PG8_WAIT_L(0); PG8_MMA(1, 0, B0, B08); PG8_BAR; PG8_LO; PG8_SCHED;
;             PG8_STAGE(PG8_SB(1, 1), b3 + hstep, voffB);
;             PG8_WAIT_V(6); PG8_BAR; PG8_HI; PG8_MMA(1, 1, B1, B18); PG8_BAR; PG8_LO;
;         }
;         { int l_; asm volatile("v_mbcnt_lo_u32_b32 %0, -1, 0\n\tv_mbcnt_hi_u32_b32 %0, -1, %0" : "=v"(l_));
;           E(acc, cur, wr, wc, l_ & 15, l_ >> 4); }
	ds_read_b128 v[146:149], v166 offset:49152
	ds_read_b128 v[168:171], v166 offset:50176
	ds_read_b128 v[172:175], v166 offset:51200
	ds_read_b128 v[176:179], v166 offset:52224
	ds_read_b128 v[180:183], v166 offset:53248
	ds_read_b128 v[184:187], v166 offset:54272
	ds_read_b128 v[194:197], v166 offset:55296
	s_mov_b32 m0, s54
	ds_read_b128 v[198:201], v166 offset:56320
	global_load_lds_dwordx4 v1, s[36:37]
	s_add_u32 s0, s34, 0x10080
	s_mov_b32 m0, s55
	s_addc_u32 s1, s35, 0
	global_load_lds_dwordx4 v1, s[0:1]
	s_barrier
	s_waitcnt lgkmcnt(0)
	s_setprio 1
	v_mfma_f32_16x16x32_bf16 v[62:65], v[130:133], v[146:149], v[62:65]
	v_mfma_f32_16x16x32_bf16 v[58:61], v[138:141], v[146:149], v[58:61]
	v_mfma_f32_16x16x32_bf16 v[46:49], v[130:133], v[172:175], v[46:49]
	v_mfma_f32_16x16x32_bf16 v[42:45], v[138:141], v[172:175], v[42:45]
	v_mfma_f32_16x16x32_bf16 v[30:33], v[130:133], v[180:183], v[30:33]
	v_mfma_f32_16x16x32_bf16 v[26:29], v[138:141], v[180:183], v[26:29]
	v_mfma_f32_16x16x32_bf16 v[14:17], v[130:133], v[194:197], v[14:17]
	v_mfma_f32_16x16x32_bf16 v[10:13], v[138:141], v[194:197], v[10:13]
	v_mfma_f32_16x16x32_bf16 v[62:65], v[134:137], v[168:171], v[62:65]
	v_mfma_f32_16x16x32_bf16 v[58:61], v[142:145], v[168:171], v[58:61]
	v_mfma_f32_16x16x32_bf16 v[46:49], v[134:137], v[176:179], v[46:49]
	v_mfma_f32_16x16x32_bf16 v[42:45], v[142:145], v[176:179], v[42:45]
	v_mfma_f32_16x16x32_bf16 v[30:33], v[134:137], v[184:187], v[30:33]
	v_mfma_f32_16x16x32_bf16 v[26:29], v[142:145], v[184:187], v[26:29]
	v_mfma_f32_16x16x32_bf16 v[14:17], v[134:137], v[198:201], v[14:17]
	v_mfma_f32_16x16x32_bf16 v[10:13], v[142:145], v[198:201], v[10:13]
	s_setprio 0
	s_barrier
	s_add_u32 s0, s30, 0x20080
	s_mov_b32 m0, s56
	s_addc_u32 s1, s31, 0
	global_load_lds_dwordx4 v1, s[0:1]
	s_add_u32 s0, s30, 0x30080
	s_mov_b32 m0, s57
	s_addc_u32 s1, s31, 0
	global_load_lds_dwordx4 v1, s[0:1]
	s_waitcnt vmcnt(6)
	s_barrier
	s_setprio 1
	v_mfma_f32_16x16x32_bf16 v[54:57], v[202:205], v[146:149], v[54:57]
	v_mfma_f32_16x16x32_bf16 v[50:53], v[210:213], v[146:149], v[50:53]
	v_mfma_f32_16x16x32_bf16 v[38:41], v[202:205], v[172:175], v[38:41]
	v_mfma_f32_16x16x32_bf16 v[34:37], v[210:213], v[172:175], v[34:37]
	v_mfma_f32_16x16x32_bf16 v[22:25], v[202:205], v[180:183], v[22:25]
	v_mfma_f32_16x16x32_bf16 v[18:21], v[210:213], v[180:183], v[18:21]
	v_mfma_f32_16x16x32_bf16 v[6:9], v[202:205], v[194:197], v[6:9]
	v_mfma_f32_16x16x32_bf16 v[2:5], v[210:213], v[194:197], v[2:5]
	v_mfma_f32_16x16x32_bf16 v[54:57], v[206:209], v[168:171], v[54:57]
	v_mfma_f32_16x16x32_bf16 v[50:53], v[214:217], v[168:171], v[50:53]
	v_mfma_f32_16x16x32_bf16 v[38:41], v[206:209], v[176:179], v[38:41]
	v_mfma_f32_16x16x32_bf16 v[34:37], v[214:217], v[176:179], v[34:37]
	v_mfma_f32_16x16x32_bf16 v[22:25], v[206:209], v[184:187], v[22:25]
	v_mfma_f32_16x16x32_bf16 v[18:21], v[214:217], v[184:187], v[18:21]
	v_mfma_f32_16x16x32_bf16 v[6:9], v[206:209], v[198:201], v[6:9]
	v_mfma_f32_16x16x32_bf16 v[2:5], v[214:217], v[198:201], v[2:5]
	s_setprio 0
	s_add_i32 s63, s63, 2
	s_add_u32 s21, s21, 0x100
	s_addc_u32 s62, s62, 0
	s_cmp_gt_u32 s63, 5
	s_mov_b64 s[0:1], s[28:29]
	s_barrier
	s_cbranch_scc0 .LBB0_2332
	v_mbcnt_lo_u32_b32 v167, -1, 0
	v_mbcnt_hi_u32_b32 v167, -1, v167
	s_lshl_b32 s0, s61, 8
	v_ashrrev_i32_e32 v130, 2, v167
	s_or_b32 s0, s0, s51
	v_and_b32_e32 v130, -4, v130
	v_add_u32_e32 v148, s0, v130
	v_readlane_b32 s80, v241, 26
	v_ashrrev_i32_e32 v149, 31, v148
	v_readlane_b32 s94, v241, 40
	v_readlane_b32 s95, v241, 41
	v_cndmask_b32_e64 v131, 0, 1, s[8:9]
	v_mov_b32_e32 v130, 1.0
	v_lshl_add_u64 v[146:147], v[148:149], 2, s[94:95]
	v_cmp_ne_u32_e64 s[0:1], 1, v131
	s_andn2_b64 vcc, exec, s[8:9]
	v_mov_b32_e32 v134, 1.0
	v_mov_b32_e32 v135, 1.0
	v_mov_b32_e32 v136, 1.0
	v_mov_b32_e32 v137, 1.0
	v_readlane_b32 s81, v241, 27
	v_readlane_b32 s82, v241, 28
	v_readlane_b32 s83, v241, 29
	v_readlane_b32 s84, v241, 30
	v_readlane_b32 s85, v241, 31
	v_readlane_b32 s86, v241, 32
	v_readlane_b32 s87, v241, 33
	v_readlane_b32 s88, v241, 34
	v_readlane_b32 s89, v241, 35
	v_readlane_b32 s90, v241, 36
	v_readlane_b32 s91, v241, 37
	v_readlane_b32 s92, v241, 38
	v_readlane_b32 s93, v241, 39
	s_cbranch_vccnz .LBB0_2335
	global_load_dwordx4 v[134:137], v[146:147], off

;     __device__ __forceinline__ bool next(int i, Unit& u) const { if (!order_tile(i, G, c, nM, nN, u.pm, u.pn)) return false; u.A = A0 + (size_t)u.pm * tstep; u.B = B0 + (size_t)u.pn * tstep; return true; }
;     __device__ __forceinline__ bool next(int i, Unit& u) const { if (!order_tile(i, G, c, nM, nN, u.pm, u.pn)) return false; u.A = A0 + (size_t)(u.pn >> 1) * groupA + (size_t)u.pm * tstep; u.B = B0 + (size_t)u.pn * tstep; return true; }
; #define PG8_STAGE(bufoff, gbase, voff) do { _Pragma("unroll") for (int _i = 0; _i < 2; ++_i) glds16_s((const void*)((const char*)(gbase) + _i * r64), (voff), ldsb + (unsigned)(bufoff) + ldsw + _i * 8192u); } while (0)
; #define PG8_WAIT_V(n) asm volatile("s_waitcnt vmcnt(" #n ")" ::: "memory")
; #define PG8_BAR __builtin_amdgcn_s_barrier()
; template <class Epi, class Sched, bool FP8 = false>
; __device__ __forceinline__ void gemm_phase(LAS unsigned char* lds, const int Kb, const int nt  , const Sched& S, const Epi& E) {
;     ...
;         const bool has_next = S.next(ui + 1, nxt);
;         const char* nA = has_next ? nxt.A : cA; const char* nB = has_next ? nxt.B : cB;
;         for (int t = 0; t < nt; t += 2) {
;             const bool last = (t == nt - 2);
;             const char* a1 = cA + (size_t)(t + 1) * kstep;
;             const char* a2 = last ? nA : cA + (size_t)(t + 2) * kstep; const char* b2 = last ? nB : cB + (size_t)(t + 2) * kstep;
;             const char* a3 = a2 + kstep; const char* b3 = b2 + kstep;
;             PG8_LDB(B0, B08, 0, 0); PG8_SCHED; PG8_LDA(0, 0); PG8_STAGE(PG8_SA(1, 1), a1 + hstep, voffA);
;             PG8_WAIT_L(8); PG8_BAR; PG8_HI; PG8_WAIT_L(0); PG8_MMA(0, 0, B0, B08); PG8_BAR; PG8_LO; PG8_SCHED;
;             PG8_LDB(B1, B18, 0, 1); PG8_STAGE(PG8_SB(0, 0), b2, voffB);
;             PG8_BAR; PG8_HI; PG8_WAIT_L(0); PG8_MMA(0, 1, B1, B18); PG8_BAR; PG8_LO;
;             PG8_LDA(0, 1); PG8_STAGE(PG8_SA(0, 0), a2, voffA);
;             PG8_BAR; PG8_HI; PG8_WAIT_L(0); PG8_MMA(1, 0, B0, B08); PG8_BAR; PG8_LO; PG8_SCHED;
;             PG8_STAGE(PG8_SB(0, 1), b2 + hstep, voffB);
;             PG8_WAIT_V(6); PG8_BAR; PG8_HI; PG8_MMA(1, 1, B1, B18); PG8_BAR; PG8_LO;
;             PG8_LDB(B0, B08, 1, 0); PG8_SCHED; PG8_LDA(1, 0); PG8_STAGE(PG8_SA(0, 1), a2 + hstep, voffA);
;             PG8_WAIT_L(8); PG8_BAR; PG8_HI; PG8_WAIT_L(0); PG8_MMA(0, 0, B0, B08); PG8_BAR; PG8_LO; PG8_SCHED;
.LBB0_2752:
	ds_read_b128 v[158:161], v139
	ds_read_b128 v[162:165], v140
	ds_read_b128 v[166:169], v141
	ds_read_b128 v[170:173], v142
	s_add_u32 s24, s22, 0x100
	s_addc_u32 s25, s23, 0
	s_cmp_eq_u32 s67, 12
	s_cselect_b32 s28, s14, s24
	s_cselect_b32 s29, s15, s25
	s_cselect_b32 s26, s16, s11
	s_cselect_b32 s27, s17, s13
	s_add_u32 s30, s28, 0x80
	s_addc_u32 s31, s29, 0
	ds_read_b128 v[174:177], v155
	ds_read_b128 v[178:181], v155 offset:1024
	ds_read_b128 v[182:185], v155 offset:2048
	ds_read_b128 v[186:189], v155 offset:3072
	ds_read_b128 v[194:197], v155 offset:4096
	ds_read_b128 v[198:201], v155 offset:5120
	ds_read_b128 v[202:205], v155 offset:6144
	ds_read_b128 v[206:209], v155 offset:7168
	s_add_u32 s68, s22, 0x40080
	s_mov_b32 m0, s63
	s_addc_u32 s69, s23, 0
	global_load_lds_dwordx4 v1, s[68:69]
	s_add_u32 s22, s22, 0x60080
	s_mov_b32 m0, s64
	s_addc_u32 s23, s23, 0
	global_load_lds_dwordx4 v1, s[22:23]
	s_waitcnt lgkmcnt(8)
	s_barrier
	s_waitcnt lgkmcnt(0)
	s_setprio 1
	v_mfma_f32_16x16x128_f8f6f4 v[130:133], v[158:165], v[174:181], v[130:133]
	v_mfma_f32_16x16x128_f8f6f4 v[122:125], v[166:173], v[174:181], v[122:125]
	v_mfma_f32_16x16x128_f8f6f4 v[114:117], v[158:165], v[182:189], v[114:117]
	v_mfma_f32_16x16x128_f8f6f4 v[106:109], v[166:173], v[182:189], v[106:109]
	v_mfma_f32_16x16x128_f8f6f4 v[98:101], v[158:165], v[194:201], v[98:101]
	v_mfma_f32_16x16x128_f8f6f4 v[90:93], v[166:173], v[194:201], v[90:93]
	v_mfma_f32_16x16x128_f8f6f4 v[82:85], v[158:165], v[202:209], v[82:85]
	v_mfma_f32_16x16x128_f8f6f4 v[74:77], v[166:173], v[202:209], v[74:77]
	s_setprio 0
	s_barrier
	ds_read_b128 v[210:213], v143
	ds_read_b128 v[214:217], v144
	ds_read_b128 v[218:221], v145
	s_mov_b32 m0, s21
	ds_read_b128 v[222:225], v146
	global_load_lds_dwordx4 v138, s[26:27]
	s_add_u32 s22, s26, 0x20000
	s_mov_b32 m0, s48
	s_addc_u32 s23, s27, 0
	global_load_lds_dwordx4 v138, s[22:23]
	s_barrier
	s_waitcnt lgkmcnt(0)
	s_setprio 1
	v_mfma_f32_16x16x128_f8f6f4 v[126:129], v[210:217], v[174:181], v[126:129]
	v_mfma_f32_16x16x128_f8f6f4 v[118:121], v[218:225], v[174:181], v[118:121]
	v_mfma_f32_16x16x128_f8f6f4 v[110:113], v[210:217], v[182:189], v[110:113]
	v_mfma_f32_16x16x128_f8f6f4 v[102:105], v[218:225], v[182:189], v[102:105]
	v_mfma_f32_16x16x128_f8f6f4 v[94:97], v[210:217], v[194:201], v[94:97]
	v_mfma_f32_16x16x128_f8f6f4 v[86:89], v[218:225], v[194:201], v[86:89]
	v_mfma_f32_16x16x128_f8f6f4 v[78:81], v[210:217], v[202:209], v[78:81]
	v_mfma_f32_16x16x128_f8f6f4 v[70:73], v[218:225], v[202:209], v[70:73]
	s_setprio 0
	s_barrier
	ds_read_b128 v[174:177], v155 offset:16384
	ds_read_b128 v[178:181], v155 offset:17408
	ds_read_b128 v[182:185], v155 offset:18432
	ds_read_b128 v[186:189], v155 offset:19456
	ds_read_b128 v[194:197], v155 offset:20480
	ds_read_b128 v[198:201], v155 offset:21504
	ds_read_b128 v[202:205], v155 offset:22528
	s_mov_b32 m0, s19
	ds_read_b128 v[206:209], v155 offset:23552
	global_load_lds_dwordx4 v1, s[28:29]
	s_add_u32 s22, s28, 0x20000
	s_mov_b32 m0, s49
	s_addc_u32 s23, s29, 0
	global_load_lds_dwordx4 v1, s[22:23]
	s_barrier
	s_waitcnt lgkmcnt(0)
	s_setprio 1
	v_mfma_f32_16x16x128_f8f6f4 v[66:69], v[158:165], v[174:181], v[66:69]
	v_mfma_f32_16x16x128_f8f6f4 v[58:61], v[166:173], v[174:181], v[58:61]
	v_mfma_f32_16x16x128_f8f6f4 v[50:53], v[158:165], v[182:189], v[50:53]
	v_mfma_f32_16x16x128_f8f6f4 v[42:45], v[166:173], v[182:189], v[42:45]
	v_mfma_f32_16x16x128_f8f6f4 v[34:37], v[158:165], v[194:201], v[34:37]
	v_mfma_f32_16x16x128_f8f6f4 v[26:29], v[166:173], v[194:201], v[26:29]
	v_mfma_f32_16x16x128_f8f6f4 v[18:21], v[158:165], v[202:209], v[18:21]
	v_mfma_f32_16x16x128_f8f6f4 v[10:13], v[166:173], v[202:209], v[10:13]
	s_setprio 0
	s_barrier
	s_add_u32 s22, s26, 0x40000
	s_mov_b32 m0, s50
	s_addc_u32 s23, s27, 0
	global_load_lds_dwordx4 v138, s[22:23]
	s_add_u32 s22, s26, 0x60000
	s_mov_b32 m0, s51
	s_addc_u32 s23, s27, 0
	global_load_lds_dwordx4 v138, s[22:23]
	s_waitcnt vmcnt(6)
	s_barrier
	s_setprio 1
	v_mfma_f32_16x16x128_f8f6f4 v[62:65], v[210:217], v[174:181], v[62:65]
	v_mfma_f32_16x16x128_f8f6f4 v[54:57], v[218:225], v[174:181], v[54:57]
	v_mfma_f32_16x16x128_f8f6f4 v[46:49], v[210:217], v[182:189], v[46:49]
	v_mfma_f32_16x16x128_f8f6f4 v[38:41], v[218:225], v[182:189], v[38:41]
	v_mfma_f32_16x16x128_f8f6f4 v[30:33], v[210:217], v[194:201], v[30:33]
	v_mfma_f32_16x16x128_f8f6f4 v[22:25], v[218:225], v[194:201], v[22:25]
	v_mfma_f32_16x16x128_f8f6f4 v[14:17], v[210:217], v[202:209], v[14:17]
	v_mfma_f32_16x16x128_f8f6f4 v[2:5], v[218:225], v[202:209], v[2:5]
	s_setprio 0
	s_barrier
	ds_read_b128 v[158:161], v147
	ds_read_b128 v[162:165], v148
	ds_read_b128 v[166:169], v149
	ds_read_b128 v[170:173], v150
	ds_read_b128 v[174:177], v155 offset:32768
	ds_read_b128 v[178:181], v155 offset:33792
	ds_read_b128 v[182:185], v155 offset:34816
	ds_read_b128 v[186:189], v155 offset:35840
	ds_read_b128 v[194:197], v155 offset:36864
	ds_read_b128 v[198:201], v155 offset:37888
	ds_read_b128 v[202:205], v155 offset:38912
	ds_read_b128 v[206:209], v155 offset:39936
	s_add_u32 s22, s28, 0x40000
	s_mov_b32 m0, s52
	s_addc_u32 s23, s29, 0
	global_load_lds_dwordx4 v1, s[22:23]
	s_add_u32 s22, s28, 0x60000
	s_mov_b32 m0, s53
	s_addc_u32 s23, s29, 0
	global_load_lds_dwordx4 v1, s[22:23]
	s_waitcnt lgkmcnt(8)
	s_barrier
; #define PG8_STAGE(bufoff, gbase, voff) do { _Pragma("unroll") for (int _i = 0; _i < 2; ++_i) glds16_s((const void*)((const char*)(gbase) + _i * r64), (voff), ldsb + (unsigned)(bufoff) + ldsw + _i * 8192u); } while (0)
; #define PG8_LDA(b, h) do { _Pragma("unroll") for (int m = 0; m < 4; ++m) { const int o_ = PG8_SA(b, h) + aoff + m * 2048; \
;         if constexpr (FP8) A8[m] = PG8_CAT8(o_); else { At[m][0] = PG8_LD16(o_); At[m][1] = PG8_LD16(o_ + 1024); } } } while (0)
; #define PG8_LDB(X, X8, b, h) do { _Pragma("unroll") for (int n = 0; n < 2; ++n) { const int o_ = PG8_SB(b, h) + boff + n * 2048; \
;         if constexpr (FP8) X8[n] = PG8_CAT8(o_); else { X[n][0] = PG8_LD16(o_); X[n][1] = PG8_LD16(o_ + 1024); } } } while (0)
; #define PG8_WAIT_V(n) asm volatile("s_waitcnt vmcnt(" #n ")" ::: "memory")
;     __device__ __forceinline__ void operator()(const f32x4 (&acc)[2][2][4][2], const Unit& u, int wr, int wc, int fr, int fq) const {
;         const int row0 = u.pm * BM + wr * 64 + fr, col0 = u.pn * HALF + wc * 32 + 8 * fq;
; #pragma unroll
;         for (int ai = 0; ai < 2; ++ai)
; #pragma unroll
;             for (int m = 0; m < 4; ++m) { unsigned char* rowp = O + (size_t)(row0 + ai * HALF + m * 16) * ldc + col0;
;                 f32x4 v[2];
; #pragma unroll
;                 for (int n = 0; n < 2; ++n) { const f32x4 g = acc[ai][0][m][n] * sin_, up = acc[ai][1][m][n] * (sin_ * sout);
; #pragma unroll
;                     for (int j = 0; j < 4; ++j) { const float e = __builtin_amdgcn_exp2f(-1.4426950408889634f * g[j]); v[n][j] = g[j] * __builtin_amdgcn_rcpf(1.f + e) * up[j]; } }
; template <class Epi, class Sched, bool FP8 = false>
; __device__ __forceinline__ void gemm_phase(LAS unsigned char* lds, const int Kb, const int nt  , const Sched& S, const Epi& E) {
;     ...
;             PG8_WAIT_L(8); PG8_BAR; PG8_HI; PG8_WAIT_L(0); PG8_MMA(0, 0, B0, B08); PG8_BAR; PG8_LO; PG8_SCHED;
;             PG8_LDB(B1, B18, 1, 1); PG8_STAGE(PG8_SB(1, 0), b3, voffB);
;             PG8_BAR; PG8_HI; PG8_WAIT_L(0); PG8_MMA(0, 1, B1, B18); PG8_BAR; PG8_LO;
;             PG8_LDA(1, 1); PG8_STAGE(PG8_SA(1, 0), a3, voffA);
;             PG8_BAR; PG8_HI; PG8_WAIT_L(0); PG8_MMA(1, 0, B0, B08); PG8_BAR; PG8_LO; PG8_SCHED;
;             PG8_STAGE(PG8_SB(1, 1), b3 + hstep, voffB);
;             PG8_WAIT_V(6); PG8_BAR; PG8_HI; PG8_MMA(1, 1, B1, B18); PG8_BAR; PG8_LO;
	s_waitcnt lgkmcnt(0)
	s_setprio 1
	v_mfma_f32_16x16x128_f8f6f4 v[130:133], v[158:165], v[174:181], v[130:133]
	v_mfma_f32_16x16x128_f8f6f4 v[122:125], v[166:173], v[174:181], v[122:125]
	v_mfma_f32_16x16x128_f8f6f4 v[114:117], v[158:165], v[182:189], v[114:117]
	v_mfma_f32_16x16x128_f8f6f4 v[106:109], v[166:173], v[182:189], v[106:109]
	v_mfma_f32_16x16x128_f8f6f4 v[98:101], v[158:165], v[194:201], v[98:101]
	v_mfma_f32_16x16x128_f8f6f4 v[90:93], v[166:173], v[194:201], v[90:93]
	v_mfma_f32_16x16x128_f8f6f4 v[82:85], v[158:165], v[202:209], v[82:85]
	v_mfma_f32_16x16x128_f8f6f4 v[74:77], v[166:173], v[202:209], v[74:77]
	s_setprio 0
	s_barrier
	ds_read_b128 v[210:213], v151
	ds_read_b128 v[214:217], v152
	s_add_u32 s22, s26, 0x80
	s_addc_u32 s23, s27, 0
	ds_read_b128 v[218:221], v153
	s_mov_b32 m0, s57
	ds_read_b128 v[222:225], v154
	global_load_lds_dwordx4 v138, s[22:23]
	s_add_u32 s22, s26, 0x20080
	s_mov_b32 m0, s58
	s_addc_u32 s23, s27, 0
	global_load_lds_dwordx4 v138, s[22:23]
	s_barrier
	s_waitcnt lgkmcnt(0)
	s_setprio 1
	v_mfma_f32_16x16x128_f8f6f4 v[126:129], v[210:217], v[174:181], v[126:129]
	v_mfma_f32_16x16x128_f8f6f4 v[118:121], v[218:225], v[174:181], v[118:121]
	v_mfma_f32_16x16x128_f8f6f4 v[110:113], v[210:217], v[182:189], v[110:113]
	v_mfma_f32_16x16x128_f8f6f4 v[102:105], v[218:225], v[182:189], v[102:105]
	v_mfma_f32_16x16x128_f8f6f4 v[94:97], v[210:217], v[194:201], v[94:97]
	v_mfma_f32_16x16x128_f8f6f4 v[86:89], v[218:225], v[194:201], v[86:89]
	v_mfma_f32_16x16x128_f8f6f4 v[78:81], v[210:217], v[202:209], v[78:81]
	v_mfma_f32_16x16x128_f8f6f4 v[70:73], v[218:225], v[202:209], v[70:73]
	s_setprio 0
	s_barrier
	ds_read_b128 v[174:177], v155 offset:49152
	ds_read_b128 v[178:181], v155 offset:50176
	ds_read_b128 v[182:185], v155 offset:51200
	ds_read_b128 v[186:189], v155 offset:52224
	ds_read_b128 v[194:197], v155 offset:53248
	ds_read_b128 v[198:201], v155 offset:54272
	ds_read_b128 v[202:205], v155 offset:55296
	s_mov_b32 m0, s59
	ds_read_b128 v[206:209], v155 offset:56320
	global_load_lds_dwordx4 v1, s[30:31]
	s_add_u32 s22, s28, 0x20080
	s_mov_b32 m0, s60
	s_addc_u32 s23, s29, 0
	global_load_lds_dwordx4 v1, s[22:23]
	s_barrier
	s_waitcnt lgkmcnt(0)
	s_setprio 1
	v_mfma_f32_16x16x128_f8f6f4 v[66:69], v[158:165], v[174:181], v[66:69]
	v_mfma_f32_16x16x128_f8f6f4 v[58:61], v[166:173], v[174:181], v[58:61]
	v_mfma_f32_16x16x128_f8f6f4 v[50:53], v[158:165], v[182:189], v[50:53]
	v_mfma_f32_16x16x128_f8f6f4 v[42:45], v[166:173], v[182:189], v[42:45]
	v_mfma_f32_16x16x128_f8f6f4 v[34:37], v[158:165], v[194:201], v[34:37]
	v_mfma_f32_16x16x128_f8f6f4 v[26:29], v[166:173], v[194:201], v[26:29]
	v_mfma_f32_16x16x128_f8f6f4 v[18:21], v[158:165], v[202:209], v[18:21]
	v_mfma_f32_16x16x128_f8f6f4 v[10:13], v[166:173], v[202:209], v[10:13]
	s_setprio 0
	s_barrier
	s_add_u32 s22, s26, 0x40080
	s_mov_b32 m0, s61
	s_addc_u32 s23, s27, 0
	global_load_lds_dwordx4 v138, s[22:23]
	s_add_u32 s22, s26, 0x60080
	s_mov_b32 m0, s62
	s_addc_u32 s23, s27, 0
	global_load_lds_dwordx4 v138, s[22:23]
	s_add_i32 s67, s67, 2
	s_add_u32 s11, s11, 0x100
	s_addc_u32 s13, s13, 0
	s_cmp_gt_u32 s67, 13
	s_mov_b64 s[22:23], s[24:25]
	s_waitcnt vmcnt(6)
	s_barrier
	s_setprio 1
	v_mfma_f32_16x16x128_f8f6f4 v[62:65], v[210:217], v[174:181], v[62:65]
	v_mfma_f32_16x16x128_f8f6f4 v[54:57], v[218:225], v[174:181], v[54:57]
	v_mfma_f32_16x16x128_f8f6f4 v[46:49], v[210:217], v[182:189], v[46:49]
	v_mfma_f32_16x16x128_f8f6f4 v[38:41], v[218:225], v[182:189], v[38:41]
	v_mfma_f32_16x16x128_f8f6f4 v[30:33], v[210:217], v[194:201], v[30:33]
	v_mfma_f32_16x16x128_f8f6f4 v[22:25], v[218:225], v[194:201], v[22:25]
	v_mfma_f32_16x16x128_f8f6f4 v[14:17], v[210:217], v[202:209], v[14:17]
	v_mfma_f32_16x16x128_f8f6f4 v[2:5], v[218:225], v[202:209], v[2:5]
	s_setprio 0
	s_barrier
	s_cbranch_scc0 .LBB0_2752
	v_mov_b32_e32 v8, v130
	v_mov_b32_e32 v9, v126
	s_nop 3
	v_pk_mul_f32 v[136:137], v[8:9], s[6:7]
	v_mov_b32_e32 v126, v131
	v_mul_f32_e32 v8, 0xbfb8aa3b, v136
	v_exp_f32_e32 v130, v8
	v_pk_mul_f32 v[126:127], v[126:127], s[6:7]
	s_lshl_b32 s11, s20, 8
	v_mul_f32_e32 v8, 0xbfb8aa3b, v126
	v_add_f32_e32 v130, 1.0, v130
	v_rcp_f32_e32 v135, v130
	v_exp_f32_e32 v131, v8
	v_mbcnt_lo_u32_b32 v6, -1, 0
	v_mbcnt_hi_u32_b32 v6, -1, v6
	s_add_i32 s11, s11, s54
	v_mul_f32_e32 v135, v136, v135
	v_mul_f32_e32 v135, v135, v137
	v_mov_b32_e32 v136, v132
	v_mov_b32_e32 v137, v128
	v_pk_mul_f32 v[136:137], v[136:137], s[6:7]
	v_add_f32_e32 v130, 1.0, v131
	v_mul_f32_e32 v128, 0xbfb8aa3b, v136
	v_exp_f32_e32 v132, v128
	v_mov_b32_e32 v128, v133
	v_rcp_f32_e32 v158, v130
	v_pk_mul_f32 v[128:129], v[128:129], s[6:7]
	v_and_or_b32 v134, v6, 15, s11
	v_mul_f32_e32 v133, 0xbfb8aa3b, v128
	v_exp_f32_e32 v133, v133
	v_mul_f32_e32 v126, v126, v158
	v_mul_f32_e32 v158, v126, v127
	v_add_f32_e32 v126, 1.0, v132
	v_rcp_f32_e32 v132, v126
	v_add_f32_e32 v126, 1.0, v133
	v_rcp_f32_e32 v133, v126
	v_mov_b32_e32 v126, v122
	v_mov_b32_e32 v127, v118
	v_pk_mul_f32 v[126:127], v[126:127], s[6:7]
	v_mul_f32_e32 v122, v136, v132
	v_mul_f32_e32 v118, 0xbfb8aa3b, v126
	v_exp_f32_e32 v118, v118
	v_mul_f32_e32 v132, v122, v137
	v_mul_f32_e32 v122, v128, v133
	v_mul_f32_e32 v129, v122, v129
	v_add_f32_e32 v118, 1.0, v118
	v_rcp_f32_e32 v128, v118
	v_mov_b32_e32 v118, v123
	v_pk_mul_f32 v[118:119], v[118:119], s[6:7]
	s_lshl_b32 s11, s18, 7
	v_mul_f32_e32 v123, 0xbfb8aa3b, v118
	v_exp_f32_e32 v123, v123
	v_mul_f32_e32 v122, v126, v128
	v_mul_f32_e32 v126, v122, v127
	v_ashrrev_i32_e32 v6, 1, v6
	v_add_f32_e32 v122, 1.0, v123
	v_rcp_f32_e32 v127, v122
	v_mov_b32_e32 v122, v124
	v_mov_b32_e32 v123, v120
;     __device__ __forceinline__ void operator()(const f32x4 (&acc)[2][2][4][2], const Unit& u, int wr, int wc, int fr, int fq) const {
;         const int row0 = u.pm * BM + wr * 64 + fr, col0 = u.pn * HALF + wc * 32 + 8 * fq;
; #pragma unroll
;         for (int ai = 0; ai < 2; ++ai)
; #pragma unroll
;             for (int m = 0; m < 4; ++m) { unsigned char* rowp = O + (size_t)(row0 + ai * HALF + m * 16) * ldc + col0;
;                 f32x4 v[2];
; #pragma unroll
;                 for (int n = 0; n < 2; ++n) { const f32x4 g = acc[ai][0][m][n] * sin_, up = acc[ai][1][m][n] * (sin_ * sout);
; #pragma unroll
;                     for (int j = 0; j < 4; ++j) { const float e = __builtin_amdgcn_exp2f(-1.4426950408889634f * g[j]); v[n][j] = g[j] * __builtin_amdgcn_rcpf(1.f + e) * up[j]; } }
;                 u32x2 w; w.x = pk4_fp8(v[0][0], v[0][1], v[0][2], v[0][3]); w.y = pk4_fp8(v[1][0], v[1][1], v[1][2], v[1][3]);
;                 *(u32x2*)rowp = w; }
	v_pk_mul_f32 v[122:123], v[122:123], s[6:7]
	v_mul_f32_e32 v118, v118, v127
	v_mul_f32_e32 v120, 0xbfb8aa3b, v122
	v_exp_f32_e32 v124, v120
	v_mov_b32_e32 v120, v125
	v_pk_mul_f32 v[120:121], v[120:121], s[6:7]
	v_mul_f32_e32 v127, v118, v119
	v_mul_f32_e32 v125, 0xbfb8aa3b, v120
	v_exp_f32_e32 v125, v125
	v_add_f32_e32 v124, 1.0, v124
	v_rcp_f32_e32 v124, v124
	v_med3_f32 v128, v129, s66, v157
	v_add_f32_e32 v125, 1.0, v125
	v_rcp_f32_e32 v125, v125
	v_mul_f32_e32 v118, v122, v124
	v_mul_f32_e32 v122, v118, v123
	v_med3_f32 v124, v158, s66, v157
	v_mul_f32_e32 v118, v120, v125
	v_mul_f32_e32 v123, v118, v121
	v_med3_f32 v121, v135, s66, v157
	v_mov_b32_e32 v120, 0
	v_cvt_pk_fp8_f32 v120, v121, v124
	v_med3_f32 v124, v126, s66, v157
	v_med3_f32 v126, v127, s66, v157
	v_mov_b32_e32 v121, 0
	v_cvt_pk_fp8_f32 v121, v124, v126
	v_med3_f32 v122, v122, s66, v157
	v_med3_f32 v123, v123, s66, v157
	v_med3_f32 v125, v132, s66, v157
	v_cvt_pk_fp8_f32 v121, v122, v123 op_sel:[0,0,1]
	v_mov_b32_e32 v122, v114
	v_mov_b32_e32 v123, v110
	v_pk_mul_f32 v[122:123], v[122:123], s[6:7]
	s_or_b32 s11, s11, s55
	v_mul_f32_e32 v110, 0xbfb8aa3b, v122
	v_exp_f32_e32 v114, v110
	v_mov_b32_e32 v110, v115
	v_pk_mul_f32 v[110:111], v[110:111], s[6:7]
	v_and_b32_e32 v6, -8, v6
	v_mul_f32_e32 v115, 0xbfb8aa3b, v110
	v_exp_f32_e32 v115, v115
	v_add_f32_e32 v114, 1.0, v114
	v_rcp_f32_e32 v114, v114
	v_cvt_pk_fp8_f32 v120, v125, v128 op_sel:[0,0,1]
	v_add_f32_e32 v115, 1.0, v115
	v_rcp_f32_e32 v115, v115
	v_add_u32_e32 v6, s11, v6
	v_mov_b64_e32 v[8:9], s[2:3]
	v_ashrrev_i32_e32 v7, 31, v6
	v_mad_i64_i32 v[130:131], s[22:23], v134, s65, v[8:9]
	v_lshl_add_u64 v[118:119], v[130:131], 0, v[6:7]
	v_mul_f32_e32 v114, v122, v114
	global_store_dwordx2 v[118:119], v[120:121], off
	v_mul_f32_e32 v119, v114, v123
	v_mul_f32_e32 v110, v110, v115
	v_mov_b32_e32 v114, v116
	v_mov_b32_e32 v115, v112
	v_pk_mul_f32 v[114:115], v[114:115], s[6:7]
	v_mul_f32_e32 v120, v110, v111
	v_mul_f32_e32 v112, 0xbfb8aa3b, v114
	v_exp_f32_e32 v116, v112
	v_mov_b32_e32 v112, v117
	v_pk_mul_f32 v[112:113], v[112:113], s[6:7]
	v_mov_b32_e32 v111, v102
	v_mul_f32_e32 v117, 0xbfb8aa3b, v112
	v_exp_f32_e32 v117, v117
	v_add_f32_e32 v110, 1.0, v116
	v_rcp_f32_e32 v116, v110
	v_or_b32_e32 v118, 16, v134
	v_add_f32_e32 v110, 1.0, v117
	v_rcp_f32_e32 v117, v110
	v_mov_b32_e32 v110, v106
	v_pk_mul_f32 v[110:111], v[110:111], s[6:7]
	v_mul_f32_e32 v106, v114, v116
	v_mul_f32_e32 v102, 0xbfb8aa3b, v110
	v_exp_f32_e32 v102, v102
	v_mul_f32_e32 v114, v106, v115
	v_mul_f32_e32 v106, v112, v117
	v_mul_f32_e32 v113, v106, v113
	v_add_f32_e32 v102, 1.0, v102
	v_rcp_f32_e32 v112, v102
	v_mov_b32_e32 v102, v107
	v_pk_mul_f32 v[102:103], v[102:103], s[6:7]
	s_and_b64 vcc, exec, s[8:9]
	v_mul_f32_e32 v107, 0xbfb8aa3b, v102
	v_exp_f32_e32 v107, v107
	v_mul_f32_e32 v106, v110, v112
	v_mul_f32_e32 v110, v106, v111
	s_mov_b32 s18, s10
	v_add_f32_e32 v106, 1.0, v107
	v_rcp_f32_e32 v111, v106
	v_mov_b32_e32 v106, v108
	v_mov_b32_e32 v107, v104
	v_pk_mul_f32 v[106:107], v[106:107], s[6:7]
	v_mul_f32_e32 v102, v102, v111
	v_mul_f32_e32 v104, 0xbfb8aa3b, v106
	v_exp_f32_e32 v108, v104
	v_mov_b32_e32 v104, v109
	v_pk_mul_f32 v[104:105], v[104:105], s[6:7]
	v_mul_f32_e32 v103, v102, v103
	v_mul_f32_e32 v109, 0xbfb8aa3b, v104
	v_exp_f32_e32 v109, v109
	v_add_f32_e32 v108, 1.0, v108
	v_rcp_f32_e32 v108, v108
	s_mov_b32 s20, s12
	v_add_f32_e32 v109, 1.0, v109
	v_rcp_f32_e32 v109, v109
	v_mul_f32_e32 v102, v106, v108
	v_mul_f32_e32 v106, v102, v107
	v_med3_f32 v107, v120, s66, v157
	v_mul_f32_e32 v102, v104, v109
	v_mul_f32_e32 v104, v102, v105
	v_med3_f32 v105, v119, s66, v157
	v_mov_b32_e32 v102, 0
	v_cvt_pk_fp8_f32 v102, v105, v107
	v_med3_f32 v105, v110, s66, v157
	v_med3_f32 v107, v103, s66, v157
	v_mov_b32_e32 v103, 0
	v_cvt_pk_fp8_f32 v103, v105, v107
	v_med3_f32 v108, v114, s66, v157
	v_med3_f32 v109, v113, s66, v157
	v_med3_f32 v105, v106, s66, v157
	v_med3_f32 v104, v104, s66, v157
	v_cvt_pk_fp8_f32 v102, v108, v109 op_sel:[0,0,1]
	v_cvt_pk_fp8_f32 v103, v105, v104 op_sel:[0,0,1]
	v_mad_i64_i32 v[104:105], s[22:23], v118, s65, v[8:9]
	v_lshl_add_u64 v[104:105], v[104:105], 0, v[6:7]
	global_store_dwordx2 v[104:105], v[102:103], off
	v_mov_b32_e32 v102, v98
	v_mov_b32_e32 v103, v94
	v_pk_mul_f32 v[102:103], v[102:103], s[6:7]
	v_or_b32_e32 v104, 32, v134
	v_mul_f32_e32 v94, 0xbfb8aa3b, v102
	v_exp_f32_e32 v98, v94
	v_mov_b32_e32 v94, v99
	v_pk_mul_f32 v[94:95], v[94:95], s[6:7]
	s_mov_b64 s[24:25], s[16:17]
	v_mul_f32_e32 v99, 0xbfb8aa3b, v94
	v_add_f32_e32 v98, 1.0, v98
	v_exp_f32_e32 v99, v99
	v_rcp_f32_e32 v105, v98
	v_add_f32_e32 v98, 1.0, v99
	v_mul_f32_e32 v102, v102, v105
	v_rcp_f32_e32 v106, v98
	v_mad_i64_i32 v[98:99], s[22:23], v104, s65, v[8:9]
	v_mul_f32_e32 v104, v102, v103
	v_mov_b32_e32 v102, v100
	v_mov_b32_e32 v103, v96
	v_pk_mul_f32 v[102:103], v[102:103], s[6:7]
	v_mul_f32_e32 v94, v94, v106
	v_mul_f32_e32 v96, 0xbfb8aa3b, v102
	v_exp_f32_e32 v100, v96
	v_mov_b32_e32 v96, v101
	v_pk_mul_f32 v[96:97], v[96:97], s[6:7]
	v_mul_f32_e32 v105, v94, v95
	v_mul_f32_e32 v101, 0xbfb8aa3b, v96
	v_exp_f32_e32 v101, v101
	v_add_f32_e32 v94, 1.0, v100
	v_rcp_f32_e32 v100, v94
	v_mov_b32_e32 v95, v86
	v_add_f32_e32 v94, 1.0, v101
	v_rcp_f32_e32 v101, v94
	v_mov_b32_e32 v94, v90
	v_pk_mul_f32 v[94:95], v[94:95], s[6:7]
	v_mul_f32_e32 v90, v102, v100
	v_mul_f32_e32 v86, 0xbfb8aa3b, v94
	v_exp_f32_e32 v86, v86
	v_mul_f32_e32 v100, v90, v103
	v_mul_f32_e32 v90, v96, v101
	v_mul_f32_e32 v97, v90, v97
	v_add_f32_e32 v86, 1.0, v86
	v_rcp_f32_e32 v96, v86
	v_mov_b32_e32 v86, v91
	v_pk_mul_f32 v[86:87], v[86:87], s[6:7]
;     __device__ __forceinline__ void operator()(const f32x4 (&acc)[2][2][4][2], const Unit& u, int wr, int wc, int fr, int fq) const {
;         const int row0 = u.pm * BM + wr * 64 + fr, col0 = u.pn * HALF + wc * 32 + 8 * fq;
; #pragma unroll
;         for (int ai = 0; ai < 2; ++ai)
; #pragma unroll
;             for (int m = 0; m < 4; ++m) { unsigned char* rowp = O + (size_t)(row0 + ai * HALF + m * 16) * ldc + col0;
;                 f32x4 v[2];
; #pragma unroll
;                 for (int n = 0; n < 2; ++n) { const f32x4 g = acc[ai][0][m][n] * sin_, up = acc[ai][1][m][n] * (sin_ * sout);
; #pragma unroll
;                     for (int j = 0; j < 4; ++j) { const float e = __builtin_amdgcn_exp2f(-1.4426950408889634f * g[j]); v[n][j] = g[j] * __builtin_amdgcn_rcpf(1.f + e) * up[j]; } }
;                 u32x2 w; w.x = pk4_fp8(v[0][0], v[0][1], v[0][2], v[0][3]); w.y = pk4_fp8(v[1][0], v[1][1], v[1][2], v[1][3]);
;                 *(u32x2*)rowp = w; }
	v_mul_f32_e32 v90, v94, v96
	v_mul_f32_e32 v91, 0xbfb8aa3b, v86
	v_exp_f32_e32 v91, v91
	v_mul_f32_e32 v94, v90, v95
	v_med3_f32 v96, v97, s66, v157
	v_add_f32_e32 v90, 1.0, v91
	v_rcp_f32_e32 v95, v90
	v_mov_b32_e32 v90, v92
	v_mov_b32_e32 v91, v88
	v_pk_mul_f32 v[90:91], v[90:91], s[6:7]
	v_mul_f32_e32 v86, v86, v95
	v_mul_f32_e32 v88, 0xbfb8aa3b, v90
	v_exp_f32_e32 v92, v88
	v_mov_b32_e32 v88, v93
	v_pk_mul_f32 v[88:89], v[88:89], s[6:7]
	v_mul_f32_e32 v95, v86, v87
	v_mul_f32_e32 v93, 0xbfb8aa3b, v88
	v_exp_f32_e32 v93, v93
	v_add_f32_e32 v92, 1.0, v92
	v_rcp_f32_e32 v92, v92
	v_add_f32_e32 v93, 1.0, v93
	v_rcp_f32_e32 v93, v93
	v_mul_f32_e32 v86, v90, v92
	v_mul_f32_e32 v90, v86, v91
	v_med3_f32 v92, v105, s66, v157
	v_mul_f32_e32 v86, v88, v93
	v_mul_f32_e32 v91, v86, v89
	v_med3_f32 v89, v104, s66, v157
	v_mov_b32_e32 v88, 0
	v_cvt_pk_fp8_f32 v88, v89, v92
	v_med3_f32 v92, v94, s66, v157
	v_med3_f32 v94, v95, s66, v157
	v_mov_b32_e32 v89, 0
	v_cvt_pk_fp8_f32 v89, v92, v94
	v_med3_f32 v90, v90, s66, v157
	v_med3_f32 v91, v91, s66, v157
	v_med3_f32 v93, v100, s66, v157
	v_cvt_pk_fp8_f32 v89, v90, v91 op_sel:[0,0,1]
	v_mov_b32_e32 v90, v82
	v_mov_b32_e32 v91, v78
	v_pk_mul_f32 v[90:91], v[90:91], s[6:7]
	v_cvt_pk_fp8_f32 v88, v93, v96 op_sel:[0,0,1]
	v_mul_f32_e32 v78, 0xbfb8aa3b, v90
	v_exp_f32_e32 v82, v78
	v_mov_b32_e32 v78, v83
	v_pk_mul_f32 v[78:79], v[78:79], s[6:7]
	v_lshl_add_u64 v[86:87], v[98:99], 0, v[6:7]
	v_mul_f32_e32 v83, 0xbfb8aa3b, v78
	v_exp_f32_e32 v83, v83
	v_add_f32_e32 v82, 1.0, v82
	v_rcp_f32_e32 v82, v82
	global_store_dwordx2 v[86:87], v[88:89], off
	v_add_f32_e32 v83, 1.0, v83
	v_rcp_f32_e32 v83, v83
	v_mul_f32_e32 v82, v90, v82
	v_mul_f32_e32 v87, v82, v91
	v_mov_b32_e32 v82, v84
	v_mul_f32_e32 v78, v78, v83
	v_mov_b32_e32 v83, v80
	v_pk_mul_f32 v[82:83], v[82:83], s[6:7]
	v_mul_f32_e32 v88, v78, v79
	v_mul_f32_e32 v80, 0xbfb8aa3b, v82
	v_exp_f32_e32 v84, v80
	v_mov_b32_e32 v80, v85
	v_pk_mul_f32 v[80:81], v[80:81], s[6:7]
	v_mov_b32_e32 v79, v70
	v_mul_f32_e32 v85, 0xbfb8aa3b, v80
	v_exp_f32_e32 v85, v85
	v_add_f32_e32 v78, 1.0, v84
	v_rcp_f32_e32 v84, v78
	v_or_b32_e32 v86, 48, v134
	v_add_f32_e32 v78, 1.0, v85
	v_rcp_f32_e32 v85, v78
	v_mov_b32_e32 v78, v74
	v_pk_mul_f32 v[78:79], v[78:79], s[6:7]
	v_mul_f32_e32 v74, v82, v84
	v_mul_f32_e32 v70, 0xbfb8aa3b, v78
	v_exp_f32_e32 v70, v70
	v_mul_f32_e32 v82, v74, v83
	v_mul_f32_e32 v74, v80, v85
	v_mul_f32_e32 v81, v74, v81
	v_add_f32_e32 v70, 1.0, v70
	v_rcp_f32_e32 v80, v70
	v_mov_b32_e32 v70, v75
	v_pk_mul_f32 v[70:71], v[70:71], s[6:7]
	v_mul_f32_e32 v74, v78, v80
	v_mul_f32_e32 v75, 0xbfb8aa3b, v70
	v_exp_f32_e32 v75, v75
	v_mul_f32_e32 v78, v74, v79
	v_add_f32_e32 v74, 1.0, v75
	v_rcp_f32_e32 v79, v74
	v_mov_b32_e32 v74, v76
	v_mov_b32_e32 v75, v72
	v_pk_mul_f32 v[74:75], v[74:75], s[6:7]
	v_mul_f32_e32 v70, v70, v79
	v_mul_f32_e32 v72, 0xbfb8aa3b, v74
	v_exp_f32_e32 v76, v72
	v_mov_b32_e32 v72, v77
	v_pk_mul_f32 v[72:73], v[72:73], s[6:7]
	v_mul_f32_e32 v71, v70, v71
	v_mul_f32_e32 v77, 0xbfb8aa3b, v72
	v_exp_f32_e32 v77, v77
	v_add_f32_e32 v76, 1.0, v76
	v_rcp_f32_e32 v76, v76
	v_add_f32_e32 v77, 1.0, v77
	v_rcp_f32_e32 v77, v77
	v_mul_f32_e32 v70, v74, v76
	v_mul_f32_e32 v74, v70, v75
	v_med3_f32 v75, v88, s66, v157
	v_mul_f32_e32 v70, v72, v77
	v_mul_f32_e32 v72, v70, v73
	v_med3_f32 v73, v87, s66, v157
	v_mov_b32_e32 v70, 0
	v_cvt_pk_fp8_f32 v70, v73, v75
	v_med3_f32 v73, v78, s66, v157
	v_med3_f32 v75, v71, s66, v157
	v_mov_b32_e32 v71, 0
	v_cvt_pk_fp8_f32 v71, v73, v75
	v_med3_f32 v76, v82, s66, v157
	v_med3_f32 v77, v81, s66, v157
	v_med3_f32 v73, v74, s66, v157
	v_med3_f32 v72, v72, s66, v157
	v_cvt_pk_fp8_f32 v70, v76, v77 op_sel:[0,0,1]
	v_cvt_pk_fp8_f32 v71, v73, v72 op_sel:[0,0,1]
	v_mad_i64_i32 v[72:73], s[22:23], v86, s65, v[8:9]
	v_lshl_add_u64 v[72:73], v[72:73], 0, v[6:7]
	global_store_dwordx2 v[72:73], v[70:71], off
	v_mov_b32_e32 v70, v66
	v_mov_b32_e32 v71, v62
	v_pk_mul_f32 v[70:71], v[70:71], s[6:7]
	v_add_u32_e32 v72, 0x80, v134
	v_mul_f32_e32 v62, 0xbfb8aa3b, v70
	v_exp_f32_e32 v66, v62
	v_mov_b32_e32 v62, v67
	v_pk_mul_f32 v[62:63], v[62:63], s[6:7]
	v_add_f32_e32 v66, 1.0, v66
	v_mul_f32_e32 v67, 0xbfb8aa3b, v62
	v_exp_f32_e32 v67, v67
	v_rcp_f32_e32 v73, v66
	v_add_f32_e32 v66, 1.0, v67
	v_mul_f32_e32 v70, v70, v73
	v_rcp_f32_e32 v74, v66
	v_mad_i64_i32 v[66:67], s[22:23], v72, s65, v[8:9]
	v_mul_f32_e32 v72, v70, v71
	v_mov_b32_e32 v70, v68
	v_mov_b32_e32 v71, v64
	v_pk_mul_f32 v[70:71], v[70:71], s[6:7]
	v_mul_f32_e32 v62, v62, v74
	v_mul_f32_e32 v64, 0xbfb8aa3b, v70
	v_exp_f32_e32 v68, v64
	v_mov_b32_e32 v64, v69
	v_pk_mul_f32 v[64:65], v[64:65], s[6:7]
	v_mul_f32_e32 v73, v62, v63
	v_mul_f32_e32 v69, 0xbfb8aa3b, v64
	v_exp_f32_e32 v69, v69
	v_add_f32_e32 v62, 1.0, v68
	v_rcp_f32_e32 v68, v62
	v_mov_b32_e32 v63, v54
	v_add_f32_e32 v62, 1.0, v69
	v_rcp_f32_e32 v69, v62
	v_mov_b32_e32 v62, v58
	v_pk_mul_f32 v[62:63], v[62:63], s[6:7]
	v_mul_f32_e32 v58, v70, v68
	v_mul_f32_e32 v54, 0xbfb8aa3b, v62
	v_exp_f32_e32 v54, v54
	v_mul_f32_e32 v68, v58, v71
	v_mul_f32_e32 v58, v64, v69
	v_mul_f32_e32 v65, v58, v65
	v_add_f32_e32 v54, 1.0, v54
	v_rcp_f32_e32 v64, v54
	v_mov_b32_e32 v54, v59
	v_pk_mul_f32 v[54:55], v[54:55], s[6:7]
	v_mul_f32_e32 v58, v62, v64
	v_mul_f32_e32 v59, 0xbfb8aa3b, v54
	v_exp_f32_e32 v59, v59
	v_mul_f32_e32 v62, v58, v63
	v_med3_f32 v64, v65, s66, v157
	v_add_f32_e32 v58, 1.0, v59
	v_rcp_f32_e32 v63, v58
	v_mov_b32_e32 v58, v60
	v_mov_b32_e32 v59, v56
	v_pk_mul_f32 v[58:59], v[58:59], s[6:7]
	v_mul_f32_e32 v54, v54, v63
	v_mul_f32_e32 v56, 0xbfb8aa3b, v58
	v_exp_f32_e32 v60, v56
	v_mov_b32_e32 v56, v61
;     __device__ __forceinline__ void operator()(const f32x4 (&acc)[2][2][4][2], const Unit& u, int wr, int wc, int fr, int fq) const {
;         const int row0 = u.pm * BM + wr * 64 + fr, col0 = u.pn * HALF + wc * 32 + 8 * fq;
; #pragma unroll
;         for (int ai = 0; ai < 2; ++ai)
; #pragma unroll
;             for (int m = 0; m < 4; ++m) { unsigned char* rowp = O + (size_t)(row0 + ai * HALF + m * 16) * ldc + col0;
;                 f32x4 v[2];
; #pragma unroll
;                 for (int n = 0; n < 2; ++n) { const f32x4 g = acc[ai][0][m][n] * sin_, up = acc[ai][1][m][n] * (sin_ * sout);
; #pragma unroll
;                     for (int j = 0; j < 4; ++j) { const float e = __builtin_amdgcn_exp2f(-1.4426950408889634f * g[j]); v[n][j] = g[j] * __builtin_amdgcn_rcpf(1.f + e) * up[j]; } }
;                 u32x2 w; w.x = pk4_fp8(v[0][0], v[0][1], v[0][2], v[0][3]); w.y = pk4_fp8(v[1][0], v[1][1], v[1][2], v[1][3]);
;                 *(u32x2*)rowp = w; }
	v_pk_mul_f32 v[56:57], v[56:57], s[6:7]
	v_mul_f32_e32 v63, v54, v55
	v_mul_f32_e32 v61, 0xbfb8aa3b, v56
	v_exp_f32_e32 v61, v61
	v_add_f32_e32 v60, 1.0, v60
	v_rcp_f32_e32 v60, v60
	v_add_f32_e32 v61, 1.0, v61
	v_rcp_f32_e32 v61, v61
	v_mul_f32_e32 v54, v58, v60
	v_mul_f32_e32 v58, v54, v59
	v_med3_f32 v60, v73, s66, v157
	v_mul_f32_e32 v54, v56, v61
	v_mul_f32_e32 v59, v54, v57
	v_med3_f32 v57, v72, s66, v157
	v_mov_b32_e32 v56, 0
	v_cvt_pk_fp8_f32 v56, v57, v60
	v_med3_f32 v60, v62, s66, v157
	v_med3_f32 v62, v63, s66, v157
	v_mov_b32_e32 v57, 0
	v_cvt_pk_fp8_f32 v57, v60, v62
	v_med3_f32 v58, v58, s66, v157
	v_med3_f32 v59, v59, s66, v157
	v_med3_f32 v61, v68, s66, v157
	v_cvt_pk_fp8_f32 v57, v58, v59 op_sel:[0,0,1]
	v_mov_b32_e32 v58, v50
	v_mov_b32_e32 v59, v46
	v_pk_mul_f32 v[58:59], v[58:59], s[6:7]
	v_cvt_pk_fp8_f32 v56, v61, v64 op_sel:[0,0,1]
	v_mul_f32_e32 v46, 0xbfb8aa3b, v58
	v_exp_f32_e32 v50, v46
	v_mov_b32_e32 v46, v51
	v_pk_mul_f32 v[46:47], v[46:47], s[6:7]
	v_lshl_add_u64 v[54:55], v[66:67], 0, v[6:7]
	v_mul_f32_e32 v51, 0xbfb8aa3b, v46
	v_exp_f32_e32 v51, v51
	v_add_f32_e32 v50, 1.0, v50
	v_rcp_f32_e32 v50, v50
	global_store_dwordx2 v[54:55], v[56:57], off
	v_add_f32_e32 v51, 1.0, v51
	v_rcp_f32_e32 v51, v51
	v_mul_f32_e32 v50, v58, v50
	v_mul_f32_e32 v55, v50, v59
	v_mov_b32_e32 v50, v52
	v_mul_f32_e32 v46, v46, v51
	v_mov_b32_e32 v51, v48
	v_pk_mul_f32 v[50:51], v[50:51], s[6:7]
	v_mul_f32_e32 v56, v46, v47
	v_mul_f32_e32 v48, 0xbfb8aa3b, v50
	v_exp_f32_e32 v52, v48
	v_mov_b32_e32 v48, v53
	v_pk_mul_f32 v[48:49], v[48:49], s[6:7]
	v_mov_b32_e32 v47, v38
	v_mul_f32_e32 v53, 0xbfb8aa3b, v48
	v_exp_f32_e32 v53, v53
	v_add_f32_e32 v46, 1.0, v52
	v_rcp_f32_e32 v52, v46
	v_add_u32_e32 v54, 0x90, v134
	v_add_f32_e32 v46, 1.0, v53
	v_rcp_f32_e32 v53, v46
	v_mov_b32_e32 v46, v42
	v_pk_mul_f32 v[46:47], v[46:47], s[6:7]
	v_mul_f32_e32 v42, v50, v52
	v_mul_f32_e32 v38, 0xbfb8aa3b, v46
	v_exp_f32_e32 v38, v38
	v_mul_f32_e32 v50, v42, v51
	v_mul_f32_e32 v42, v48, v53
	v_mul_f32_e32 v49, v42, v49
	v_add_f32_e32 v38, 1.0, v38
	v_rcp_f32_e32 v48, v38
	v_mov_b32_e32 v38, v43
	v_pk_mul_f32 v[38:39], v[38:39], s[6:7]
	v_mul_f32_e32 v42, v46, v48
	v_mul_f32_e32 v43, 0xbfb8aa3b, v38
	v_exp_f32_e32 v43, v43
	v_mul_f32_e32 v46, v42, v47
	v_add_f32_e32 v42, 1.0, v43
	v_rcp_f32_e32 v47, v42
	v_mov_b32_e32 v42, v44
	v_mov_b32_e32 v43, v40
	v_pk_mul_f32 v[42:43], v[42:43], s[6:7]
	v_mul_f32_e32 v38, v38, v47
	v_mul_f32_e32 v40, 0xbfb8aa3b, v42
	v_exp_f32_e32 v44, v40
	v_mov_b32_e32 v40, v45
	v_pk_mul_f32 v[40:41], v[40:41], s[6:7]
	v_mul_f32_e32 v39, v38, v39
	v_mul_f32_e32 v45, 0xbfb8aa3b, v40
	v_exp_f32_e32 v45, v45
	v_add_f32_e32 v44, 1.0, v44
	v_rcp_f32_e32 v44, v44
	v_add_f32_e32 v45, 1.0, v45
	v_rcp_f32_e32 v45, v45
	v_mul_f32_e32 v38, v42, v44
	v_mul_f32_e32 v42, v38, v43
	v_med3_f32 v43, v56, s66, v157
	v_mul_f32_e32 v38, v40, v45
	v_mul_f32_e32 v40, v38, v41
	v_med3_f32 v41, v55, s66, v157
	v_mov_b32_e32 v38, 0
	v_cvt_pk_fp8_f32 v38, v41, v43
	v_med3_f32 v41, v46, s66, v157
	v_med3_f32 v43, v39, s66, v157
	v_mov_b32_e32 v39, 0
	v_cvt_pk_fp8_f32 v39, v41, v43
	v_med3_f32 v44, v50, s66, v157
	v_med3_f32 v45, v49, s66, v157
	v_med3_f32 v41, v42, s66, v157
	v_med3_f32 v40, v40, s66, v157
	v_cvt_pk_fp8_f32 v38, v44, v45 op_sel:[0,0,1]
	v_cvt_pk_fp8_f32 v39, v41, v40 op_sel:[0,0,1]
	v_mad_i64_i32 v[40:41], s[22:23], v54, s65, v[8:9]
	v_lshl_add_u64 v[40:41], v[40:41], 0, v[6:7]
	global_store_dwordx2 v[40:41], v[38:39], off
	v_mov_b32_e32 v38, v34
	v_mov_b32_e32 v39, v30
	v_pk_mul_f32 v[38:39], v[38:39], s[6:7]
	v_add_u32_e32 v40, 0xa0, v134
	v_mul_f32_e32 v30, 0xbfb8aa3b, v38
	v_exp_f32_e32 v34, v30
	v_mov_b32_e32 v30, v35
	v_pk_mul_f32 v[30:31], v[30:31], s[6:7]
	v_add_f32_e32 v34, 1.0, v34
	v_mul_f32_e32 v35, 0xbfb8aa3b, v30
	v_exp_f32_e32 v35, v35
	v_rcp_f32_e32 v41, v34
	v_add_f32_e32 v34, 1.0, v35
	v_mul_f32_e32 v38, v38, v41
	v_rcp_f32_e32 v42, v34
	v_mad_i64_i32 v[34:35], s[22:23], v40, s65, v[8:9]
	v_mul_f32_e32 v40, v38, v39
	v_mov_b32_e32 v38, v36
	v_mov_b32_e32 v39, v32
	v_pk_mul_f32 v[38:39], v[38:39], s[6:7]
	v_mul_f32_e32 v30, v30, v42
	v_mul_f32_e32 v32, 0xbfb8aa3b, v38
	v_exp_f32_e32 v36, v32
	v_mov_b32_e32 v32, v37
	v_pk_mul_f32 v[32:33], v[32:33], s[6:7]
	v_mul_f32_e32 v41, v30, v31
	v_mul_f32_e32 v37, 0xbfb8aa3b, v32
	v_exp_f32_e32 v37, v37
	v_add_f32_e32 v30, 1.0, v36
	v_rcp_f32_e32 v36, v30
; #define PG8_WAIT_V(n) asm volatile("s_waitcnt vmcnt(" #n ")" ::: "memory")
; #define PG8_BAR __builtin_amdgcn_s_barrier()
;     __device__ __forceinline__ void operator()(const f32x4 (&acc)[2][2][4][2], const Unit& u, int wr, int wc, int fr, int fq) const {
;         const int row0 = u.pm * BM + wr * 64 + fr, col0 = u.pn * HALF + wc * 32 + 8 * fq;
; #pragma unroll
;         for (int ai = 0; ai < 2; ++ai)
; #pragma unroll
;             for (int m = 0; m < 4; ++m) { unsigned char* rowp = O + (size_t)(row0 + ai * HALF + m * 16) * ldc + col0;
;                 f32x4 v[2];
; #pragma unroll
;                 for (int n = 0; n < 2; ++n) { const f32x4 g = acc[ai][0][m][n] * sin_, up = acc[ai][1][m][n] * (sin_ * sout);
; #pragma unroll
;                     for (int j = 0; j < 4; ++j) { const float e = __builtin_amdgcn_exp2f(-1.4426950408889634f * g[j]); v[n][j] = g[j] * __builtin_amdgcn_rcpf(1.f + e) * up[j]; } }
;                 u32x2 w; w.x = pk4_fp8(v[0][0], v[0][1], v[0][2], v[0][3]); w.y = pk4_fp8(v[1][0], v[1][1], v[1][2], v[1][3]);
;                 *(u32x2*)rowp = w; }
; template <class Epi, class Sched, bool FP8 = false>
; __device__ __forceinline__ void gemm_phase(LAS unsigned char* lds, const int Kb, const int nt  , const Sched& S, const Epi& E) {
;     ...
;         if (!has_next) break;
; #pragma unroll
;         for (int a = 0; a < 2; ++a)
; #pragma unroll
;             for (int b = 0; b < 2; ++b)
; #pragma unroll
;                 for (int m = 0; m < 4; ++m)
; #pragma unroll
;                     for (int n = 0; n < 2; ++n) acc[a][b][m][n] = (f32x4){0.f, 0.f, 0.f, 0.f};
;         cur = nxt; cA = nA; cB = nB; ++ui;
;     }
;     PG8_WAIT_V(0);
;     if (wr == 0) PG8_BAR;
;     PG8_BAR;
	v_mov_b32_e32 v31, v22
	v_add_f32_e32 v30, 1.0, v37
	v_rcp_f32_e32 v37, v30
	v_mov_b32_e32 v30, v26
	v_pk_mul_f32 v[30:31], v[30:31], s[6:7]
	v_mul_f32_e32 v26, v38, v36
	v_mul_f32_e32 v22, 0xbfb8aa3b, v30
	v_exp_f32_e32 v22, v22
	v_mul_f32_e32 v36, v26, v39
	v_mul_f32_e32 v26, v32, v37
	v_mul_f32_e32 v33, v26, v33
	v_add_f32_e32 v22, 1.0, v22
	v_rcp_f32_e32 v32, v22
	v_mov_b32_e32 v22, v27
	v_pk_mul_f32 v[22:23], v[22:23], s[6:7]
	v_mul_f32_e32 v26, v30, v32
	v_mul_f32_e32 v27, 0xbfb8aa3b, v22
	v_exp_f32_e32 v27, v27
	v_mul_f32_e32 v30, v26, v31
	v_med3_f32 v32, v33, s66, v157
	v_add_f32_e32 v26, 1.0, v27
	v_rcp_f32_e32 v31, v26
	v_mov_b32_e32 v26, v28
	v_mov_b32_e32 v27, v24
	v_pk_mul_f32 v[26:27], v[26:27], s[6:7]
	v_mul_f32_e32 v22, v22, v31
	v_mul_f32_e32 v24, 0xbfb8aa3b, v26
	v_exp_f32_e32 v28, v24
	v_mov_b32_e32 v24, v29
	v_pk_mul_f32 v[24:25], v[24:25], s[6:7]
	v_mul_f32_e32 v31, v22, v23
	v_mul_f32_e32 v29, 0xbfb8aa3b, v24
	v_exp_f32_e32 v29, v29
	v_add_f32_e32 v28, 1.0, v28
	v_rcp_f32_e32 v28, v28
	v_add_f32_e32 v29, 1.0, v29
	v_rcp_f32_e32 v29, v29
	v_mul_f32_e32 v22, v26, v28
	v_mul_f32_e32 v26, v22, v27
	v_med3_f32 v28, v41, s66, v157
	v_mul_f32_e32 v22, v24, v29
	v_mul_f32_e32 v27, v22, v25
	v_med3_f32 v25, v40, s66, v157
	v_mov_b32_e32 v24, 0
	v_cvt_pk_fp8_f32 v24, v25, v28
	v_med3_f32 v28, v30, s66, v157
	v_med3_f32 v30, v31, s66, v157
	v_mov_b32_e32 v25, 0
	v_cvt_pk_fp8_f32 v25, v28, v30
	v_med3_f32 v26, v26, s66, v157
	v_med3_f32 v27, v27, s66, v157
	v_med3_f32 v29, v36, s66, v157
	v_cvt_pk_fp8_f32 v25, v26, v27 op_sel:[0,0,1]
	v_mov_b32_e32 v26, v18
	v_mov_b32_e32 v27, v14
	v_pk_mul_f32 v[26:27], v[26:27], s[6:7]
	v_cvt_pk_fp8_f32 v24, v29, v32 op_sel:[0,0,1]
	v_mul_f32_e32 v14, 0xbfb8aa3b, v26
	v_exp_f32_e32 v18, v14
	v_mov_b32_e32 v14, v19
	v_pk_mul_f32 v[14:15], v[14:15], s[6:7]
	v_lshl_add_u64 v[22:23], v[34:35], 0, v[6:7]
	v_mul_f32_e32 v19, 0xbfb8aa3b, v14
	v_exp_f32_e32 v19, v19
	v_add_f32_e32 v18, 1.0, v18
	v_rcp_f32_e32 v18, v18
	global_store_dwordx2 v[22:23], v[24:25], off
	v_add_f32_e32 v19, 1.0, v19
	v_rcp_f32_e32 v19, v19
	v_mul_f32_e32 v18, v26, v18
	v_mul_f32_e32 v23, v18, v27
	v_mov_b32_e32 v18, v20
	v_mul_f32_e32 v14, v14, v19
	v_mov_b32_e32 v19, v16
	v_pk_mul_f32 v[18:19], v[18:19], s[6:7]
	v_mul_f32_e32 v24, v14, v15
	v_mul_f32_e32 v16, 0xbfb8aa3b, v18
	v_exp_f32_e32 v20, v16
	v_mov_b32_e32 v16, v21
	v_pk_mul_f32 v[16:17], v[16:17], s[6:7]
	v_mov_b32_e32 v15, v2
	v_mul_f32_e32 v21, 0xbfb8aa3b, v16
	v_exp_f32_e32 v21, v21
	v_add_f32_e32 v14, 1.0, v20
	v_rcp_f32_e32 v20, v14
	v_add_u32_e32 v22, 0xb0, v134
	v_add_f32_e32 v14, 1.0, v21
	v_rcp_f32_e32 v21, v14
	v_mov_b32_e32 v14, v10
	v_pk_mul_f32 v[14:15], v[14:15], s[6:7]
	v_mul_f32_e32 v10, v18, v20
	v_mul_f32_e32 v2, 0xbfb8aa3b, v14
	v_exp_f32_e32 v2, v2
	v_mul_f32_e32 v18, v10, v19
	v_mul_f32_e32 v10, v16, v21
	v_mul_f32_e32 v17, v10, v17
	v_add_f32_e32 v2, 1.0, v2
	v_rcp_f32_e32 v16, v2
	v_mov_b32_e32 v2, v11
	v_pk_mul_f32 v[2:3], v[2:3], s[6:7]
	v_mul_f32_e32 v10, v14, v16
	v_mul_f32_e32 v11, 0xbfb8aa3b, v2
	v_exp_f32_e32 v11, v11
	v_mul_f32_e32 v14, v10, v15
	v_add_f32_e32 v10, 1.0, v11
	v_rcp_f32_e32 v15, v10
	v_mov_b32_e32 v10, v12
	v_mov_b32_e32 v11, v4
	v_pk_mul_f32 v[10:11], v[10:11], s[6:7]
	v_mul_f32_e32 v2, v2, v15
	v_mul_f32_e32 v4, 0xbfb8aa3b, v10
	v_exp_f32_e32 v12, v4
	v_mov_b32_e32 v4, v13
	v_pk_mul_f32 v[4:5], v[4:5], s[6:7]
	v_mul_f32_e32 v3, v2, v3
	v_mul_f32_e32 v13, 0xbfb8aa3b, v4
	v_exp_f32_e32 v13, v13
	v_add_f32_e32 v12, 1.0, v12
	v_rcp_f32_e32 v12, v12
	v_add_f32_e32 v13, 1.0, v13
	v_rcp_f32_e32 v13, v13
	v_mul_f32_e32 v2, v10, v12
	v_mul_f32_e32 v10, v2, v11
	v_med3_f32 v11, v24, s66, v157
	v_mul_f32_e32 v2, v4, v13
	v_mul_f32_e32 v4, v2, v5
	v_med3_f32 v5, v23, s66, v157
	v_mov_b32_e32 v2, 0
	v_cvt_pk_fp8_f32 v2, v5, v11
	v_med3_f32 v5, v14, s66, v157
	v_med3_f32 v11, v3, s66, v157
	v_mov_b32_e32 v3, 0
	v_cvt_pk_fp8_f32 v3, v5, v11
	v_med3_f32 v12, v18, s66, v157
	v_med3_f32 v13, v17, s66, v157
	v_med3_f32 v5, v10, s66, v157
	v_med3_f32 v4, v4, s66, v157
	v_cvt_pk_fp8_f32 v2, v12, v13 op_sel:[0,0,1]
	v_cvt_pk_fp8_f32 v3, v5, v4 op_sel:[0,0,1]
	v_mad_i64_i32 v[4:5], s[22:23], v22, s65, v[8:9]
	v_lshl_add_u64 v[4:5], v[4:5], 0, v[6:7]
	s_mov_b64 s[22:23], s[14:15]
	global_store_dwordx2 v[4:5], v[2:3], off
	s_cbranch_vccz .LBB0_2749
	s_waitcnt vmcnt(0)
	s_cmpk_gt_u32 s42, 0xff
	s_cbranch_scc1 .LBB0_2756
	s_barrier

;     __device__ __forceinline__ bool next(int i, Unit& u) const { if (!order_tile(i, G, c, nM, nN, u.pm, u.pn)) return false; u.A = A0 + (size_t)u.pm * tstep; u.B = B0 + (size_t)u.pn * tstep; return true; }
;     __device__ __forceinline__ bool next(int i, Unit& u) const { if (!order_tile(i, G, c, nM, nN, u.pm, u.pn)) return false; u.A = A0 + (size_t)(u.pn >> 1) * groupA + (size_t)u.pm * tstep; u.B = B0 + (size_t)u.pn * tstep; return true; }
; #define PG8_STAGE(bufoff, gbase, voff) do { _Pragma("unroll") for (int _i = 0; _i < 2; ++_i) glds16_s((const void*)((const char*)(gbase) + _i * r64), (voff), ldsb + (unsigned)(bufoff) + ldsw + _i * 8192u); } while (0)
; #define PG8_WAIT_V(n) asm volatile("s_waitcnt vmcnt(" #n ")" ::: "memory")
; #define PG8_BAR __builtin_amdgcn_s_barrier()
; template <class Epi, class Sched, bool FP8 = false>
; __device__ __forceinline__ void gemm_phase(LAS unsigned char* lds, const int Kb, const int nt  , const Sched& S, const Epi& E) {
;     ...
;         const bool has_next = S.next(ui + 1, nxt);
;         const char* nA = has_next ? nxt.A : cA; const char* nB = has_next ? nxt.B : cB;
;         for (int t = 0; t < nt; t += 2) {
;             const bool last = (t == nt - 2);
;             const char* a1 = cA + (size_t)(t + 1) * kstep;
;             const char* a2 = last ? nA : cA + (size_t)(t + 2) * kstep; const char* b2 = last ? nB : cB + (size_t)(t + 2) * kstep;
;             const char* a3 = a2 + kstep; const char* b3 = b2 + kstep;
;             PG8_LDB(B0, B08, 0, 0); PG8_SCHED; PG8_LDA(0, 0); PG8_STAGE(PG8_SA(1, 1), a1 + hstep, voffA);
;             PG8_WAIT_L(8); PG8_BAR; PG8_HI; PG8_WAIT_L(0); PG8_MMA(0, 0, B0, B08); PG8_BAR; PG8_LO; PG8_SCHED;
;             PG8_LDB(B1, B18, 0, 1); PG8_STAGE(PG8_SB(0, 0), b2, voffB);
;             PG8_BAR; PG8_HI; PG8_WAIT_L(0); PG8_MMA(0, 1, B1, B18); PG8_BAR; PG8_LO;
;             PG8_LDA(0, 1); PG8_STAGE(PG8_SA(0, 0), a2, voffA);
;             PG8_BAR; PG8_HI; PG8_WAIT_L(0); PG8_MMA(1, 0, B0, B08); PG8_BAR; PG8_LO; PG8_SCHED;
;             PG8_STAGE(PG8_SB(0, 1), b2 + hstep, voffB);
;             PG8_WAIT_V(6); PG8_BAR; PG8_HI; PG8_MMA(1, 1, B1, B18); PG8_BAR; PG8_LO;
;             PG8_LDB(B0, B08, 1, 0); PG8_SCHED; PG8_LDA(1, 0); PG8_STAGE(PG8_SA(0, 1), a2 + hstep, voffA);
;             PG8_WAIT_L(8); PG8_BAR; PG8_HI; PG8_WAIT_L(0); PG8_MMA(0, 0, B0, B08); PG8_BAR; PG8_LO; PG8_SCHED;
.LBB0_2837:
	ds_read_b128 v[162:165], v143
	ds_read_b128 v[166:169], v144
	ds_read_b128 v[170:173], v145
	ds_read_b128 v[174:177], v146
	s_add_u32 s24, s22, 0x100
	s_addc_u32 s25, s23, 0
	s_cmp_eq_u32 s75, 52
	s_cselect_b32 s28, s18, s24
	s_cselect_b32 s29, s19, s25
	s_cselect_b32 s26, s20, s73
	s_cselect_b32 s27, s21, s74
	s_add_u32 s30, s28, 0x80
	s_addc_u32 s31, s29, 0
	ds_read_b128 v[178:181], v159
	ds_read_b128 v[182:185], v159 offset:1024
	ds_read_b128 v[192:195], v159 offset:2048
	ds_read_b128 v[196:199], v159 offset:3072
	ds_read_b128 v[200:203], v159 offset:4096
	ds_read_b128 v[204:207], v159 offset:5120
	ds_read_b128 v[208:211], v159 offset:6144
	ds_read_b128 v[212:215], v159 offset:7168
	s_add_u32 s76, s22, 0xe0080
	s_mov_b32 m0, s63
	s_addc_u32 s77, s23, 0
	global_load_lds_dwordx4 v138, s[76:77]
	s_add_u32 s22, s22, 0x150080
	s_mov_b32 m0, s64
	s_addc_u32 s23, s23, 0
	global_load_lds_dwordx4 v138, s[22:23]
	s_waitcnt lgkmcnt(8)
	s_barrier
	s_waitcnt lgkmcnt(0)
	s_setprio 1
	v_mfma_f32_16x16x128_f8f6f4 v[130:133], v[162:169], v[178:185], v[130:133]
	v_mfma_f32_16x16x128_f8f6f4 v[126:129], v[170:177], v[178:185], v[126:129]
	v_mfma_f32_16x16x128_f8f6f4 v[114:117], v[162:169], v[192:199], v[114:117]
	v_mfma_f32_16x16x128_f8f6f4 v[110:113], v[170:177], v[192:199], v[110:113]
	v_mfma_f32_16x16x128_f8f6f4 v[98:101], v[162:169], v[200:207], v[98:101]
	v_mfma_f32_16x16x128_f8f6f4 v[94:97], v[170:177], v[200:207], v[94:97]
	v_mfma_f32_16x16x128_f8f6f4 v[82:85], v[162:169], v[208:215], v[82:85]
	v_mfma_f32_16x16x128_f8f6f4 v[78:81], v[170:177], v[208:215], v[78:81]
	s_setprio 0
	s_barrier
	ds_read_b128 v[216:219], v147
	ds_read_b128 v[220:223], v148
	ds_read_b128 v[224:227], v149
	s_mov_b32 m0, s47
	ds_read_b128 v[228:231], v150
	global_load_lds_dwordx4 v142, s[26:27]
	s_add_u32 s22, s26, 0x70000
	s_mov_b32 m0, s48
	s_addc_u32 s23, s27, 0
	global_load_lds_dwordx4 v142, s[22:23]
	s_barrier
	s_waitcnt lgkmcnt(0)
	s_setprio 1
	v_mfma_f32_16x16x128_f8f6f4 v[122:125], v[216:223], v[178:185], v[122:125]
	v_mfma_f32_16x16x128_f8f6f4 v[118:121], v[224:231], v[178:185], v[118:121]
	v_mfma_f32_16x16x128_f8f6f4 v[106:109], v[216:223], v[192:199], v[106:109]
	v_mfma_f32_16x16x128_f8f6f4 v[102:105], v[224:231], v[192:199], v[102:105]
	v_mfma_f32_16x16x128_f8f6f4 v[90:93], v[216:223], v[200:207], v[90:93]
	v_mfma_f32_16x16x128_f8f6f4 v[86:89], v[224:231], v[200:207], v[86:89]
	v_mfma_f32_16x16x128_f8f6f4 v[74:77], v[216:223], v[208:215], v[74:77]
	v_mfma_f32_16x16x128_f8f6f4 v[70:73], v[224:231], v[208:215], v[70:73]
	s_setprio 0
	s_barrier
	ds_read_b128 v[178:181], v159 offset:16384
	ds_read_b128 v[182:185], v159 offset:17408
	ds_read_b128 v[192:195], v159 offset:18432
	ds_read_b128 v[196:199], v159 offset:19456
	ds_read_b128 v[200:203], v159 offset:20480
	ds_read_b128 v[204:207], v159 offset:21504
	ds_read_b128 v[208:211], v159 offset:22528
	s_mov_b32 m0, s46
	ds_read_b128 v[212:215], v159 offset:23552
	global_load_lds_dwordx4 v138, s[28:29]
	s_add_u32 s22, s28, 0x70000
	s_mov_b32 m0, s49
	s_addc_u32 s23, s29, 0
	global_load_lds_dwordx4 v138, s[22:23]
	s_barrier
	s_waitcnt lgkmcnt(0)
	s_setprio 1
	v_mfma_f32_16x16x128_f8f6f4 v[66:69], v[162:169], v[178:185], v[66:69]
	v_mfma_f32_16x16x128_f8f6f4 v[62:65], v[170:177], v[178:185], v[62:65]
	v_mfma_f32_16x16x128_f8f6f4 v[54:57], v[162:169], v[192:199], v[54:57]
	v_mfma_f32_16x16x128_f8f6f4 v[46:49], v[170:177], v[192:199], v[46:49]
	v_mfma_f32_16x16x128_f8f6f4 v[38:41], v[162:169], v[200:207], v[38:41]
	v_mfma_f32_16x16x128_f8f6f4 v[30:33], v[170:177], v[200:207], v[30:33]
	v_mfma_f32_16x16x128_f8f6f4 v[22:25], v[162:169], v[208:215], v[22:25]
	v_mfma_f32_16x16x128_f8f6f4 v[14:17], v[170:177], v[208:215], v[14:17]
	s_setprio 0
	s_barrier
	s_add_u32 s22, s26, 0xe0000
	s_mov_b32 m0, s50
	s_addc_u32 s23, s27, 0
	global_load_lds_dwordx4 v142, s[22:23]
	s_add_u32 s22, s26, 0x150000
	s_mov_b32 m0, s51
	s_addc_u32 s23, s27, 0
	global_load_lds_dwordx4 v142, s[22:23]
	s_waitcnt vmcnt(6)
	s_barrier
	s_setprio 1
	v_mfma_f32_16x16x128_f8f6f4 v[58:61], v[216:223], v[178:185], v[58:61]
	v_mfma_f32_16x16x128_f8f6f4 v[50:53], v[224:231], v[178:185], v[50:53]
	v_mfma_f32_16x16x128_f8f6f4 v[42:45], v[216:223], v[192:199], v[42:45]
	v_mfma_f32_16x16x128_f8f6f4 v[34:37], v[224:231], v[192:199], v[34:37]
	v_mfma_f32_16x16x128_f8f6f4 v[26:29], v[216:223], v[200:207], v[26:29]
	v_mfma_f32_16x16x128_f8f6f4 v[18:21], v[224:231], v[200:207], v[18:21]
	v_mfma_f32_16x16x128_f8f6f4 v[10:13], v[216:223], v[208:215], v[10:13]
	v_mfma_f32_16x16x128_f8f6f4 v[2:5], v[224:231], v[208:215], v[2:5]
	s_setprio 0
	s_barrier
	ds_read_b128 v[162:165], v151
	ds_read_b128 v[166:169], v152
	ds_read_b128 v[170:173], v153
	ds_read_b128 v[174:177], v154
	ds_read_b128 v[178:181], v159 offset:32768
	ds_read_b128 v[182:185], v159 offset:33792
	ds_read_b128 v[192:195], v159 offset:34816
	ds_read_b128 v[196:199], v159 offset:35840
	ds_read_b128 v[200:203], v159 offset:36864
	ds_read_b128 v[204:207], v159 offset:37888
	ds_read_b128 v[208:211], v159 offset:38912
	ds_read_b128 v[212:215], v159 offset:39936
	s_add_u32 s22, s28, 0xe0000
	s_mov_b32 m0, s52
	s_addc_u32 s23, s29, 0
	global_load_lds_dwordx4 v138, s[22:23]
	s_add_u32 s22, s28, 0x150000
	s_mov_b32 m0, s53
	s_addc_u32 s23, s29, 0
	global_load_lds_dwordx4 v138, s[22:23]
	s_waitcnt lgkmcnt(8)
	s_barrier
; __device__ __forceinline__ unsigned cvt_pk_bf16(float lo, float hi) { unsigned r; asm volatile("v_cvt_pk_bf16_f32 %0, %1, %2" : "=v"(r) : "v"(lo), "v"(hi)); return r; }
; #define PG8_STAGE(bufoff, gbase, voff) do { _Pragma("unroll") for (int _i = 0; _i < 2; ++_i) glds16_s((const void*)((const char*)(gbase) + _i * r64), (voff), ldsb + (unsigned)(bufoff) + ldsw + _i * 8192u); } while (0)
; #define PG8_LDA(b, h) do { _Pragma("unroll") for (int m = 0; m < 4; ++m) { const int o_ = PG8_SA(b, h) + aoff + m * 2048; \
;         if constexpr (FP8) A8[m] = PG8_CAT8(o_); else { At[m][0] = PG8_LD16(o_); At[m][1] = PG8_LD16(o_ + 1024); } } } while (0)
; #define PG8_WAIT_V(n) asm volatile("s_waitcnt vmcnt(" #n ")" ::: "memory")
; #define PG8_WAIT_L(n) asm volatile("s_waitcnt lgkmcnt(" #n ")" ::: "memory")
; #define PG8_BAR __builtin_amdgcn_s_barrier()
;     __device__ __forceinline__ void operator()(const f32x4 (&acc)[2][2][4][2], const Unit& u, int wr, int wc, int fr, int fq) const {
;         const int row0 = u.pm * BM + wr * 64 + fr, col0 = u.pn * BM + wc * 32 + 8 * fq;
; #pragma unroll
;         for (int ai = 0; ai < 2; ++ai)
; #pragma unroll
;             for (int m = 0; m < 4; ++m) { bf16_t* rowp = O + (size_t)(row0 + ai * HALF + m * 16) * ldc + col0;
; #pragma unroll
;                 for (int bj = 0; bj < 2; ++bj) { const f32x4 v0 = acc[ai][bj][m][0] * scale, v1 = acc[ai][bj][m][1] * scale;
;                     u32x4 w; w.x = cvt_pk_bf16(v0[0], v0[1]); w.y = cvt_pk_bf16(v0[2], v0[3]); w.z = cvt_pk_bf16(v1[0], v1[1]); w.w = cvt_pk_bf16(v1[2], v1[3]);
;                     *(u32x4*)(rowp + bj * HALF) = w; } }
; template <class Epi, class Sched, bool FP8 = false>
; __device__ __forceinline__ void gemm_phase(LAS unsigned char* lds, const int Kb, const int nt  , const Sched& S, const Epi& E) {
;     ...
;             PG8_WAIT_L(8); PG8_BAR; PG8_HI; PG8_WAIT_L(0); PG8_MMA(0, 0, B0, B08); PG8_BAR; PG8_LO; PG8_SCHED;
;             PG8_LDB(B1, B18, 1, 1); PG8_STAGE(PG8_SB(1, 0), b3, voffB);
;             PG8_BAR; PG8_HI; PG8_WAIT_L(0); PG8_MMA(0, 1, B1, B18); PG8_BAR; PG8_LO;
;             PG8_LDA(1, 1); PG8_STAGE(PG8_SA(1, 0), a3, voffA);
;             PG8_BAR; PG8_HI; PG8_WAIT_L(0); PG8_MMA(1, 0, B0, B08); PG8_BAR; PG8_LO; PG8_SCHED;
;             PG8_STAGE(PG8_SB(1, 1), b3 + hstep, voffB);
;             PG8_WAIT_V(6); PG8_BAR; PG8_HI; PG8_MMA(1, 1, B1, B18); PG8_BAR; PG8_LO;
	s_waitcnt lgkmcnt(0)
	s_setprio 1
	v_mfma_f32_16x16x128_f8f6f4 v[130:133], v[162:169], v[178:185], v[130:133]
	v_mfma_f32_16x16x128_f8f6f4 v[126:129], v[170:177], v[178:185], v[126:129]
	v_mfma_f32_16x16x128_f8f6f4 v[114:117], v[162:169], v[192:199], v[114:117]
	v_mfma_f32_16x16x128_f8f6f4 v[110:113], v[170:177], v[192:199], v[110:113]
	v_mfma_f32_16x16x128_f8f6f4 v[98:101], v[162:169], v[200:207], v[98:101]
	v_mfma_f32_16x16x128_f8f6f4 v[94:97], v[170:177], v[200:207], v[94:97]
	v_mfma_f32_16x16x128_f8f6f4 v[82:85], v[162:169], v[208:215], v[82:85]
	v_mfma_f32_16x16x128_f8f6f4 v[78:81], v[170:177], v[208:215], v[78:81]
	s_setprio 0
	s_barrier
	ds_read_b128 v[216:219], v155
	ds_read_b128 v[220:223], v156
	s_add_u32 s22, s26, 0x80
	s_addc_u32 s23, s27, 0
	ds_read_b128 v[224:227], v157
	s_mov_b32 m0, s57
	ds_read_b128 v[228:231], v158
	global_load_lds_dwordx4 v142, s[22:23]
	s_add_u32 s22, s26, 0x70080
	s_mov_b32 m0, s58
	s_addc_u32 s23, s27, 0
	global_load_lds_dwordx4 v142, s[22:23]
	s_barrier
	s_waitcnt lgkmcnt(0)
	s_setprio 1
	v_mfma_f32_16x16x128_f8f6f4 v[122:125], v[216:223], v[178:185], v[122:125]
	v_mfma_f32_16x16x128_f8f6f4 v[118:121], v[224:231], v[178:185], v[118:121]
	v_mfma_f32_16x16x128_f8f6f4 v[106:109], v[216:223], v[192:199], v[106:109]
	v_mfma_f32_16x16x128_f8f6f4 v[102:105], v[224:231], v[192:199], v[102:105]
	v_mfma_f32_16x16x128_f8f6f4 v[90:93], v[216:223], v[200:207], v[90:93]
	v_mfma_f32_16x16x128_f8f6f4 v[86:89], v[224:231], v[200:207], v[86:89]
	v_mfma_f32_16x16x128_f8f6f4 v[74:77], v[216:223], v[208:215], v[74:77]
	v_mfma_f32_16x16x128_f8f6f4 v[70:73], v[224:231], v[208:215], v[70:73]
	s_setprio 0
	s_barrier
	ds_read_b128 v[178:181], v159 offset:49152
	ds_read_b128 v[182:185], v159 offset:50176
	ds_read_b128 v[192:195], v159 offset:51200
	ds_read_b128 v[196:199], v159 offset:52224
	ds_read_b128 v[200:203], v159 offset:53248
	ds_read_b128 v[204:207], v159 offset:54272
	ds_read_b128 v[208:211], v159 offset:55296
	s_mov_b32 m0, s59
	ds_read_b128 v[212:215], v159 offset:56320
	global_load_lds_dwordx4 v138, s[30:31]
	s_add_u32 s22, s28, 0x70080
	s_mov_b32 m0, s60
	s_addc_u32 s23, s29, 0
	global_load_lds_dwordx4 v138, s[22:23]
	s_barrier
	s_waitcnt lgkmcnt(0)
	s_setprio 1
	v_mfma_f32_16x16x128_f8f6f4 v[66:69], v[162:169], v[178:185], v[66:69]
	v_mfma_f32_16x16x128_f8f6f4 v[62:65], v[170:177], v[178:185], v[62:65]
	v_mfma_f32_16x16x128_f8f6f4 v[54:57], v[162:169], v[192:199], v[54:57]
	v_mfma_f32_16x16x128_f8f6f4 v[46:49], v[170:177], v[192:199], v[46:49]
	v_mfma_f32_16x16x128_f8f6f4 v[38:41], v[162:169], v[200:207], v[38:41]
	v_mfma_f32_16x16x128_f8f6f4 v[30:33], v[170:177], v[200:207], v[30:33]
	v_mfma_f32_16x16x128_f8f6f4 v[22:25], v[162:169], v[208:215], v[22:25]
	v_mfma_f32_16x16x128_f8f6f4 v[14:17], v[170:177], v[208:215], v[14:17]
	s_setprio 0
	s_barrier
	s_add_u32 s22, s26, 0xe0080
	s_mov_b32 m0, s61
	s_addc_u32 s23, s27, 0
	global_load_lds_dwordx4 v142, s[22:23]
	s_add_u32 s22, s26, 0x150080
	s_mov_b32 m0, s62
	s_addc_u32 s23, s27, 0
	global_load_lds_dwordx4 v142, s[22:23]
	s_add_i32 s75, s75, 2
	s_add_u32 s73, s73, 0x100
	s_addc_u32 s74, s74, 0
	s_cmp_gt_u32 s75, 53
	s_mov_b64 s[22:23], s[24:25]
	s_waitcnt vmcnt(6)
	s_barrier
	s_setprio 1
	v_mfma_f32_16x16x128_f8f6f4 v[58:61], v[216:223], v[178:185], v[58:61]
	v_mfma_f32_16x16x128_f8f6f4 v[50:53], v[224:231], v[178:185], v[50:53]
	v_mfma_f32_16x16x128_f8f6f4 v[42:45], v[216:223], v[192:199], v[42:45]
	v_mfma_f32_16x16x128_f8f6f4 v[34:37], v[224:231], v[192:199], v[34:37]
	v_mfma_f32_16x16x128_f8f6f4 v[26:29], v[216:223], v[200:207], v[26:29]
	v_mfma_f32_16x16x128_f8f6f4 v[18:21], v[224:231], v[200:207], v[18:21]
	v_mfma_f32_16x16x128_f8f6f4 v[10:13], v[216:223], v[208:215], v[10:13]
	v_mfma_f32_16x16x128_f8f6f4 v[2:5], v[224:231], v[208:215], v[2:5]
	s_setprio 0
	s_barrier
	s_cbranch_scc0 .LBB0_2837
	s_lshl_b32 s22, s72, 8
	v_mbcnt_lo_u32_b32 v6, -1, 0
	v_mbcnt_hi_u32_b32 v6, -1, v6
	s_add_i32 s22, s22, s54
	v_and_or_b32 v8, v6, 15, s22
	s_lshl_b32 s22, s71, 8
	v_ashrrev_i32_e32 v6, 1, v6
	s_or_b32 s22, s22, s55
	v_and_b32_e32 v6, -8, v6
	v_add_u32_e32 v6, s22, v6
	v_ashrrev_i32_e32 v9, 31, v8
	v_ashrrev_i32_e32 v7, 31, v6
	v_lshlrev_b64 v[134:135], 12, v[8:9]
	v_lshl_add_u64 v[134:135], s[4:5], 0, v[134:135]
	v_lshlrev_b64 v[136:137], 1, v[6:7]
	v_lshl_add_u64 v[6:7], v[134:135], 0, v[136:137]
	v_pk_mul_f32 v[132:133], v[132:133], s[6:7] op_sel_hi:[1,0]
	v_pk_mul_f32 v[130:131], v[130:131], s[6:7] op_sel_hi:[1,0]
	v_pk_mul_f32 v[134:135], v[128:129], s[6:7] op_sel_hi:[1,0]
	v_pk_mul_f32 v[128:129], v[126:127], s[6:7] op_sel_hi:[1,0]
	v_cvt_pk_bf16_f32 v126, v130, v131
	v_cvt_pk_bf16_f32 v127, v132, v133
	v_pk_mul_f32 v[122:123], v[122:123], s[6:7] op_sel_hi:[1,0]
	v_cvt_pk_bf16_f32 v128, v128, v129
	v_cvt_pk_bf16_f32 v129, v134, v135
	global_store_dwordx4 v[6:7], v[126:129], off
	v_pk_mul_f32 v[124:125], v[124:125], s[6:7] op_sel_hi:[1,0]
	v_pk_mul_f32 v[116:117], v[116:117], s[6:7] op_sel_hi:[1,0]
	v_pk_mul_f32 v[126:127], v[120:121], s[6:7] op_sel_hi:[1,0]
	v_pk_mul_f32 v[120:121], v[118:119], s[6:7] op_sel_hi:[1,0]
	v_cvt_pk_bf16_f32 v118, v122, v123
	v_cvt_pk_bf16_f32 v119, v124, v125
	v_pk_mul_f32 v[114:115], v[114:115], s[6:7] op_sel_hi:[1,0]
	v_cvt_pk_bf16_f32 v120, v120, v121
	v_cvt_pk_bf16_f32 v121, v126, v127
	global_store_dwordx4 v[6:7], v[118:121], off offset:256
	v_pk_mul_f32 v[106:107], v[106:107], s[6:7] op_sel_hi:[1,0]
	v_pk_mul_f32 v[108:109], v[108:109], s[6:7] op_sel_hi:[1,0]
	v_or_b32_e32 v118, 16, v8
	v_ashrrev_i32_e32 v119, 31, v118
	v_lshlrev_b64 v[118:119], 12, v[118:119]
	v_lshl_add_u64 v[118:119], s[4:5], 0, v[118:119]
; __device__ __forceinline__ unsigned cvt_pk_bf16(float lo, float hi) { unsigned r; asm volatile("v_cvt_pk_bf16_f32 %0, %1, %2" : "=v"(r) : "v"(lo), "v"(hi)); return r; }
; #define PG8_WAIT_V(n) asm volatile("s_waitcnt vmcnt(" #n ")" ::: "memory")
; #define PG8_BAR __builtin_amdgcn_s_barrier()
;     __device__ __forceinline__ void operator()(const f32x4 (&acc)[2][2][4][2], const Unit& u, int wr, int wc, int fr, int fq) const {
;         const int row0 = u.pm * BM + wr * 64 + fr, col0 = u.pn * BM + wc * 32 + 8 * fq;
; #pragma unroll
;         for (int ai = 0; ai < 2; ++ai)
; #pragma unroll
;             for (int m = 0; m < 4; ++m) { bf16_t* rowp = O + (size_t)(row0 + ai * HALF + m * 16) * ldc + col0;
; #pragma unroll
;                 for (int bj = 0; bj < 2; ++bj) { const f32x4 v0 = acc[ai][bj][m][0] * scale, v1 = acc[ai][bj][m][1] * scale;
;                     u32x4 w; w.x = cvt_pk_bf16(v0[0], v0[1]); w.y = cvt_pk_bf16(v0[2], v0[3]); w.z = cvt_pk_bf16(v1[0], v1[1]); w.w = cvt_pk_bf16(v1[2], v1[3]);
;                     *(u32x4*)(rowp + bj * HALF) = w; } }
; template <class Epi, class Sched, bool FP8 = false>
; __device__ __forceinline__ void gemm_phase(LAS unsigned char* lds, const int Kb, const int nt  , const Sched& S, const Epi& E) {
;     ...
;         if (!has_next) break;
; #pragma unroll
;         for (int a = 0; a < 2; ++a)
; #pragma unroll
;             for (int b = 0; b < 2; ++b)
; #pragma unroll
;                 for (int m = 0; m < 4; ++m)
; #pragma unroll
;                     for (int n = 0; n < 2; ++n) acc[a][b][m][n] = (f32x4){0.f, 0.f, 0.f, 0.f};
;         cur = nxt; cA = nA; cB = nB; ++ui;
;     }
;     PG8_WAIT_V(0);
;     if (wr == 0) PG8_BAR;
;     PG8_BAR;
	v_lshl_add_u64 v[118:119], v[118:119], 0, v[136:137]
	v_pk_mul_f32 v[120:121], v[112:113], s[6:7] op_sel_hi:[1,0]
	v_pk_mul_f32 v[112:113], v[110:111], s[6:7] op_sel_hi:[1,0]
	v_cvt_pk_bf16_f32 v110, v114, v115
	v_cvt_pk_bf16_f32 v111, v116, v117
	v_pk_mul_f32 v[100:101], v[100:101], s[6:7] op_sel_hi:[1,0]
	v_cvt_pk_bf16_f32 v112, v112, v113
	v_cvt_pk_bf16_f32 v113, v120, v121
	global_store_dwordx4 v[118:119], v[110:113], off
	v_pk_mul_f32 v[98:99], v[98:99], s[6:7] op_sel_hi:[1,0]
	v_pk_mul_f32 v[92:93], v[92:93], s[6:7] op_sel_hi:[1,0]
	v_pk_mul_f32 v[110:111], v[104:105], s[6:7] op_sel_hi:[1,0]
	v_pk_mul_f32 v[104:105], v[102:103], s[6:7] op_sel_hi:[1,0]
	v_cvt_pk_bf16_f32 v102, v106, v107
	v_cvt_pk_bf16_f32 v103, v108, v109
	v_pk_mul_f32 v[90:91], v[90:91], s[6:7] op_sel_hi:[1,0]
	v_cvt_pk_bf16_f32 v104, v104, v105
	v_cvt_pk_bf16_f32 v105, v110, v111
	global_store_dwordx4 v[118:119], v[102:105], off offset:256
	v_pk_mul_f32 v[84:85], v[84:85], s[6:7] op_sel_hi:[1,0]
	v_pk_mul_f32 v[82:83], v[82:83], s[6:7] op_sel_hi:[1,0]
	v_or_b32_e32 v102, 32, v8
	v_ashrrev_i32_e32 v103, 31, v102
	v_lshlrev_b64 v[102:103], 12, v[102:103]
	v_or_b32_e32 v8, 48, v8
	v_lshl_add_u64 v[102:103], s[4:5], 0, v[102:103]
	v_ashrrev_i32_e32 v9, 31, v8
	v_lshl_add_u64 v[102:103], v[102:103], 0, v[136:137]
	v_pk_mul_f32 v[104:105], v[96:97], s[6:7] op_sel_hi:[1,0]
	v_pk_mul_f32 v[96:97], v[94:95], s[6:7] op_sel_hi:[1,0]
	v_cvt_pk_bf16_f32 v94, v98, v99
	v_cvt_pk_bf16_f32 v95, v100, v101
	v_lshlrev_b64 v[8:9], 12, v[8:9]
	v_cvt_pk_bf16_f32 v96, v96, v97
	v_cvt_pk_bf16_f32 v97, v104, v105
	global_store_dwordx4 v[102:103], v[94:97], off
	v_lshl_add_u64 v[8:9], s[4:5], 0, v[8:9]
	v_lshl_add_u64 v[8:9], v[8:9], 0, v[136:137]
	v_pk_mul_f32 v[94:95], v[88:89], s[6:7] op_sel_hi:[1,0]
	v_pk_mul_f32 v[88:89], v[86:87], s[6:7] op_sel_hi:[1,0]
	v_cvt_pk_bf16_f32 v86, v90, v91
	v_cvt_pk_bf16_f32 v87, v92, v93
	v_pk_mul_f32 v[76:77], v[76:77], s[6:7] op_sel_hi:[1,0]
	v_cvt_pk_bf16_f32 v88, v88, v89
	v_cvt_pk_bf16_f32 v89, v94, v95
	global_store_dwordx4 v[102:103], v[86:89], off offset:256
	v_pk_mul_f32 v[74:75], v[74:75], s[6:7] op_sel_hi:[1,0]
	v_pk_mul_f32 v[66:67], v[66:67], s[6:7] op_sel_hi:[1,0]
	v_pk_mul_f32 v[86:87], v[80:81], s[6:7] op_sel_hi:[1,0]
	v_pk_mul_f32 v[80:81], v[78:79], s[6:7] op_sel_hi:[1,0]
	v_cvt_pk_bf16_f32 v78, v82, v83
	v_cvt_pk_bf16_f32 v79, v84, v85
	v_pk_mul_f32 v[68:69], v[68:69], s[6:7] op_sel_hi:[1,0]
	v_cvt_pk_bf16_f32 v80, v80, v81
	v_cvt_pk_bf16_f32 v81, v86, v87
	global_store_dwordx4 v[8:9], v[78:81], off
	v_pk_mul_f32 v[60:61], v[60:61], s[6:7] op_sel_hi:[1,0]
	v_pk_mul_f32 v[58:59], v[58:59], s[6:7] op_sel_hi:[1,0]
	v_pk_mul_f32 v[78:79], v[72:73], s[6:7] op_sel_hi:[1,0]
	v_pk_mul_f32 v[72:73], v[70:71], s[6:7] op_sel_hi:[1,0]
	v_cvt_pk_bf16_f32 v70, v74, v75
	v_cvt_pk_bf16_f32 v71, v76, v77
	v_pk_mul_f32 v[44:45], v[44:45], s[6:7] op_sel_hi:[1,0]
	v_cvt_pk_bf16_f32 v72, v72, v73
	v_cvt_pk_bf16_f32 v73, v78, v79
	global_store_dwordx4 v[8:9], v[70:73], off offset:256
	v_lshl_add_u64 v[8:9], v[6:7], 0, s[8:9]
	v_pk_mul_f32 v[42:43], v[42:43], s[6:7] op_sel_hi:[1,0]
	v_pk_mul_f32 v[70:71], v[64:65], s[6:7] op_sel_hi:[1,0]
	v_pk_mul_f32 v[64:65], v[62:63], s[6:7] op_sel_hi:[1,0]
	v_cvt_pk_bf16_f32 v62, v66, v67
	v_add_co_u32_e32 v66, vcc, s65, v6
	v_cvt_pk_bf16_f32 v63, v68, v69
	v_cvt_pk_bf16_f32 v64, v64, v65
	v_cvt_pk_bf16_f32 v65, v70, v71
	v_pk_mul_f32 v[28:29], v[28:29], s[6:7] op_sel_hi:[1,0]
	s_nop 0
	v_addc_co_u32_e32 v67, vcc, 0, v7, vcc
	global_store_dwordx4 v[66:67], v[62:65], off
	v_pk_mul_f32 v[26:27], v[26:27], s[6:7] op_sel_hi:[1,0]
	s_mov_b32 s71, s69
	v_pk_mul_f32 v[62:63], v[52:53], s[6:7] op_sel_hi:[1,0]
	v_pk_mul_f32 v[52:53], v[50:51], s[6:7] op_sel_hi:[1,0]
	v_cvt_pk_bf16_f32 v50, v58, v59
	v_cvt_pk_bf16_f32 v51, v60, v61
	s_mov_b32 s72, s70
	v_cvt_pk_bf16_f32 v52, v52, v53
	v_cvt_pk_bf16_f32 v53, v62, v63
	global_store_dwordx4 v[8:9], v[50:53], off offset:256
	v_lshl_add_u64 v[8:9], v[6:7], 0, s[10:11]
	s_mov_b64 s[24:25], s[20:21]
	v_pk_mul_f32 v[50:51], v[56:57], s[6:7] op_sel_hi:[1,0]
	v_pk_mul_f32 v[52:53], v[54:55], s[6:7] op_sel_hi:[1,0]
	v_pk_mul_f32 v[54:55], v[48:49], s[6:7] op_sel_hi:[1,0]
	v_pk_mul_f32 v[48:49], v[46:47], s[6:7] op_sel_hi:[1,0]
	v_cvt_pk_bf16_f32 v46, v52, v53
	v_cvt_pk_bf16_f32 v47, v50, v51
	v_add_co_u32_e32 v50, vcc, s66, v6
	v_cvt_pk_bf16_f32 v48, v48, v49
	v_cvt_pk_bf16_f32 v49, v54, v55
	s_mov_b64 s[22:23], s[18:19]
	s_nop 0
	v_addc_co_u32_e32 v51, vcc, 0, v7, vcc
	global_store_dwordx4 v[50:51], v[46:49], off
	v_pk_mul_f32 v[10:11], v[10:11], s[6:7] op_sel_hi:[1,0]
	s_nop 0
	v_pk_mul_f32 v[46:47], v[36:37], s[6:7] op_sel_hi:[1,0]
	v_pk_mul_f32 v[36:37], v[34:35], s[6:7] op_sel_hi:[1,0]
	v_cvt_pk_bf16_f32 v34, v42, v43
	v_cvt_pk_bf16_f32 v35, v44, v45
	s_nop 0
	v_cvt_pk_bf16_f32 v36, v36, v37
	v_cvt_pk_bf16_f32 v37, v46, v47
	global_store_dwordx4 v[8:9], v[34:37], off offset:256
	v_lshl_add_u64 v[8:9], v[6:7], 0, s[12:13]
	s_nop 0
	v_pk_mul_f32 v[34:35], v[40:41], s[6:7] op_sel_hi:[1,0]
	v_pk_mul_f32 v[36:37], v[38:39], s[6:7] op_sel_hi:[1,0]
	v_pk_mul_f32 v[38:39], v[32:33], s[6:7] op_sel_hi:[1,0]
	v_pk_mul_f32 v[32:33], v[30:31], s[6:7] op_sel_hi:[1,0]
	v_cvt_pk_bf16_f32 v30, v36, v37
	v_cvt_pk_bf16_f32 v31, v34, v35
	v_add_co_u32_e32 v34, vcc, s67, v6
	v_cvt_pk_bf16_f32 v32, v32, v33
	v_cvt_pk_bf16_f32 v33, v38, v39
	s_nop 1
	v_addc_co_u32_e32 v35, vcc, 0, v7, vcc
	global_store_dwordx4 v[34:35], v[30:33], off
	s_nop 1
	v_pk_mul_f32 v[30:31], v[20:21], s[6:7] op_sel_hi:[1,0]
	v_pk_mul_f32 v[20:21], v[18:19], s[6:7] op_sel_hi:[1,0]
	v_cvt_pk_bf16_f32 v18, v26, v27
	v_cvt_pk_bf16_f32 v19, v28, v29
	s_nop 0
	v_cvt_pk_bf16_f32 v20, v20, v21
	v_cvt_pk_bf16_f32 v21, v30, v31
	global_store_dwordx4 v[8:9], v[18:21], off offset:256
	v_lshl_add_u64 v[8:9], v[6:7], 0, s[14:15]
	v_add_co_u32_e32 v6, vcc, s68, v6
	v_pk_mul_f32 v[20:21], v[22:23], s[6:7] op_sel_hi:[1,0]
	v_pk_mul_f32 v[22:23], v[16:17], s[6:7] op_sel_hi:[1,0]
	v_pk_mul_f32 v[16:17], v[14:15], s[6:7] op_sel_hi:[1,0]
	v_addc_co_u32_e32 v7, vcc, 0, v7, vcc
	v_pk_mul_f32 v[18:19], v[24:25], s[6:7] op_sel_hi:[1,0]
	v_cvt_pk_bf16_f32 v14, v20, v21
	s_and_b64 vcc, exec, s[16:17]
	v_cvt_pk_bf16_f32 v15, v18, v19
	v_cvt_pk_bf16_f32 v16, v16, v17
	v_cvt_pk_bf16_f32 v17, v22, v23
	global_store_dwordx4 v[6:7], v[14:17], off
	v_pk_mul_f32 v[6:7], v[12:13], s[6:7] op_sel_hi:[1,0]
	v_pk_mul_f32 v[12:13], v[4:5], s[6:7] op_sel_hi:[1,0]
	v_pk_mul_f32 v[4:5], v[2:3], s[6:7] op_sel_hi:[1,0]
	v_cvt_pk_bf16_f32 v2, v10, v11
	v_cvt_pk_bf16_f32 v3, v6, v7
	s_nop 0
	v_cvt_pk_bf16_f32 v4, v4, v5
	v_cvt_pk_bf16_f32 v5, v12, v13
	global_store_dwordx4 v[8:9], v[2:5], off offset:256
	s_cbranch_vccz .LBB0_2834
	s_waitcnt vmcnt(0)
	s_cmpk_gt_u32 s3, 0xff
	s_cbranch_scc1 .LBB0_2841
	s_barrier

;     __device__ __forceinline__ bool next(int i, Unit& u) const { if (!order_tile(i, G, c, nM, nN, u.pm, u.pn)) return false; u.A = A0 + (size_t)u.pm * tstep; u.B = B0 + (size_t)u.pn * tstep; return true; }
;     __device__ __forceinline__ bool next(int i, Unit& u) const { if (!order_tile(i, G, c, nM, nN, u.pm, u.pn)) return false; u.A = A0 + (size_t)(u.pn >> 1) * groupA + (size_t)u.pm * tstep; u.B = B0 + (size_t)u.pn * tstep; return true; }
; #define PG8_STAGE(bufoff, gbase, voff) do { _Pragma("unroll") for (int _i = 0; _i < 2; ++_i) glds16_s((const void*)((const char*)(gbase) + _i * r64), (voff), ldsb + (unsigned)(bufoff) + ldsw + _i * 8192u); } while (0)
; #define PG8_WAIT_V(n) asm volatile("s_waitcnt vmcnt(" #n ")" ::: "memory")
; #define PG8_BAR __builtin_amdgcn_s_barrier()
; template <class Epi, class Sched, bool FP8 = false>
; __device__ __forceinline__ void gemm_phase(LAS unsigned char* lds, const int Kb, const int nt  , const Sched& S, const Epi& E) {
;     ...
;         const bool has_next = S.next(ui + 1, nxt);
;         const char* nA = has_next ? nxt.A : cA; const char* nB = has_next ? nxt.B : cB;
;         for (int t = 0; t < nt; t += 2) {
;             const bool last = (t == nt - 2);
;             const char* a1 = cA + (size_t)(t + 1) * kstep;
;             const char* a2 = last ? nA : cA + (size_t)(t + 2) * kstep; const char* b2 = last ? nB : cB + (size_t)(t + 2) * kstep;
;             const char* a3 = a2 + kstep; const char* b3 = b2 + kstep;
;             PG8_LDB(B0, B08, 0, 0); PG8_SCHED; PG8_LDA(0, 0); PG8_STAGE(PG8_SA(1, 1), a1 + hstep, voffA);
;             PG8_WAIT_L(8); PG8_BAR; PG8_HI; PG8_WAIT_L(0); PG8_MMA(0, 0, B0, B08); PG8_BAR; PG8_LO; PG8_SCHED;
;             PG8_LDB(B1, B18, 0, 1); PG8_STAGE(PG8_SB(0, 0), b2, voffB);
;             PG8_BAR; PG8_HI; PG8_WAIT_L(0); PG8_MMA(0, 1, B1, B18); PG8_BAR; PG8_LO;
;             PG8_LDA(0, 1); PG8_STAGE(PG8_SA(0, 0), a2, voffA);
;             PG8_BAR; PG8_HI; PG8_WAIT_L(0); PG8_MMA(1, 0, B0, B08); PG8_BAR; PG8_LO; PG8_SCHED;
;             PG8_STAGE(PG8_SB(0, 1), b2 + hstep, voffB);
;             PG8_WAIT_V(6); PG8_BAR; PG8_HI; PG8_MMA(1, 1, B1, B18); PG8_BAR; PG8_LO;
;             PG8_LDB(B0, B08, 1, 0); PG8_SCHED; PG8_LDA(1, 0); PG8_STAGE(PG8_SA(0, 1), a2 + hstep, voffA);
;             PG8_WAIT_L(8); PG8_BAR; PG8_HI; PG8_WAIT_L(0); PG8_MMA(0, 0, B0, B08); PG8_BAR; PG8_LO; PG8_SCHED;
.LBB0_2851:
	ds_read_b128 v[162:165], v143
	ds_read_b128 v[166:169], v144
	ds_read_b128 v[170:173], v145
	ds_read_b128 v[174:177], v146
	s_add_u32 s24, s22, 0x100
	s_addc_u32 s25, s23, 0
	s_cmp_eq_u32 s77, 52
	s_cselect_b32 s28, s18, s24
	s_cselect_b32 s29, s19, s25
	s_cselect_b32 s26, s20, s75
	s_cselect_b32 s27, s21, s76
	s_add_u32 s30, s28, 0x80
	s_addc_u32 s31, s29, 0
	ds_read_b128 v[178:181], v159
	ds_read_b128 v[182:185], v159 offset:1024
	ds_read_b128 v[192:195], v159 offset:2048
	ds_read_b128 v[196:199], v159 offset:3072
	ds_read_b128 v[200:203], v159 offset:4096
	ds_read_b128 v[204:207], v159 offset:5120
	ds_read_b128 v[208:211], v159 offset:6144
	ds_read_b128 v[212:215], v159 offset:7168
	s_add_u32 s78, s22, 0xe0080
	s_mov_b32 m0, s65
	s_addc_u32 s79, s23, 0
	global_load_lds_dwordx4 v138, s[78:79]
	s_add_u32 s22, s22, 0x150080
	s_mov_b32 m0, s66
	s_addc_u32 s23, s23, 0
	global_load_lds_dwordx4 v138, s[22:23]
	s_waitcnt lgkmcnt(8)
	s_barrier
	s_waitcnt lgkmcnt(0)
	s_setprio 1
	v_mfma_f32_16x16x128_f8f6f4 v[130:133], v[162:169], v[178:185], v[130:133]
	v_mfma_f32_16x16x128_f8f6f4 v[126:129], v[170:177], v[178:185], v[126:129]
	v_mfma_f32_16x16x128_f8f6f4 v[114:117], v[162:169], v[192:199], v[114:117]
	v_mfma_f32_16x16x128_f8f6f4 v[110:113], v[170:177], v[192:199], v[110:113]
	v_mfma_f32_16x16x128_f8f6f4 v[98:101], v[162:169], v[200:207], v[98:101]
	v_mfma_f32_16x16x128_f8f6f4 v[94:97], v[170:177], v[200:207], v[94:97]
	v_mfma_f32_16x16x128_f8f6f4 v[82:85], v[162:169], v[208:215], v[82:85]
	v_mfma_f32_16x16x128_f8f6f4 v[78:81], v[170:177], v[208:215], v[78:81]
	s_setprio 0
	s_barrier
	ds_read_b128 v[216:219], v147
	ds_read_b128 v[220:223], v148
	ds_read_b128 v[224:227], v149
	s_mov_b32 m0, s51
	ds_read_b128 v[228:231], v150
	global_load_lds_dwordx4 v142, s[26:27]
	s_add_u32 s22, s26, 0x70000
	s_mov_b32 m0, s52
	s_addc_u32 s23, s27, 0
	global_load_lds_dwordx4 v142, s[22:23]
	s_barrier
	s_waitcnt lgkmcnt(0)
	s_setprio 1
	v_mfma_f32_16x16x128_f8f6f4 v[122:125], v[216:223], v[178:185], v[122:125]
	v_mfma_f32_16x16x128_f8f6f4 v[118:121], v[224:231], v[178:185], v[118:121]
	v_mfma_f32_16x16x128_f8f6f4 v[106:109], v[216:223], v[192:199], v[106:109]
	v_mfma_f32_16x16x128_f8f6f4 v[102:105], v[224:231], v[192:199], v[102:105]
	v_mfma_f32_16x16x128_f8f6f4 v[90:93], v[216:223], v[200:207], v[90:93]
	v_mfma_f32_16x16x128_f8f6f4 v[86:89], v[224:231], v[200:207], v[86:89]
	v_mfma_f32_16x16x128_f8f6f4 v[74:77], v[216:223], v[208:215], v[74:77]
	v_mfma_f32_16x16x128_f8f6f4 v[70:73], v[224:231], v[208:215], v[70:73]
	s_setprio 0
	s_barrier
	ds_read_b128 v[178:181], v159 offset:16384
	ds_read_b128 v[182:185], v159 offset:17408
	ds_read_b128 v[192:195], v159 offset:18432
	ds_read_b128 v[196:199], v159 offset:19456
	ds_read_b128 v[200:203], v159 offset:20480
	ds_read_b128 v[204:207], v159 offset:21504
	ds_read_b128 v[208:211], v159 offset:22528
	s_mov_b32 m0, s50
	ds_read_b128 v[212:215], v159 offset:23552
	global_load_lds_dwordx4 v138, s[28:29]
	s_add_u32 s22, s28, 0x70000
	s_mov_b32 m0, s53
	s_addc_u32 s23, s29, 0
	global_load_lds_dwordx4 v138, s[22:23]
	s_barrier
	s_waitcnt lgkmcnt(0)
	s_setprio 1
	v_mfma_f32_16x16x128_f8f6f4 v[66:69], v[162:169], v[178:185], v[66:69]
	v_mfma_f32_16x16x128_f8f6f4 v[62:65], v[170:177], v[178:185], v[62:65]
	v_mfma_f32_16x16x128_f8f6f4 v[54:57], v[162:169], v[192:199], v[54:57]
	v_mfma_f32_16x16x128_f8f6f4 v[46:49], v[170:177], v[192:199], v[46:49]
	v_mfma_f32_16x16x128_f8f6f4 v[38:41], v[162:169], v[200:207], v[38:41]
	v_mfma_f32_16x16x128_f8f6f4 v[30:33], v[170:177], v[200:207], v[30:33]
	v_mfma_f32_16x16x128_f8f6f4 v[22:25], v[162:169], v[208:215], v[22:25]
	v_mfma_f32_16x16x128_f8f6f4 v[14:17], v[170:177], v[208:215], v[14:17]
	s_setprio 0
	s_barrier
	s_add_u32 s22, s26, 0xe0000
	s_mov_b32 m0, s54
	s_addc_u32 s23, s27, 0
	global_load_lds_dwordx4 v142, s[22:23]
	s_add_u32 s22, s26, 0x150000
	s_mov_b32 m0, s55
	s_addc_u32 s23, s27, 0
	global_load_lds_dwordx4 v142, s[22:23]
	s_waitcnt vmcnt(6)
	s_barrier
	s_setprio 1
	v_mfma_f32_16x16x128_f8f6f4 v[58:61], v[216:223], v[178:185], v[58:61]
	v_mfma_f32_16x16x128_f8f6f4 v[50:53], v[224:231], v[178:185], v[50:53]
	v_mfma_f32_16x16x128_f8f6f4 v[42:45], v[216:223], v[192:199], v[42:45]
	v_mfma_f32_16x16x128_f8f6f4 v[34:37], v[224:231], v[192:199], v[34:37]
	v_mfma_f32_16x16x128_f8f6f4 v[26:29], v[216:223], v[200:207], v[26:29]
	v_mfma_f32_16x16x128_f8f6f4 v[18:21], v[224:231], v[200:207], v[18:21]
	v_mfma_f32_16x16x128_f8f6f4 v[10:13], v[216:223], v[208:215], v[10:13]
	v_mfma_f32_16x16x128_f8f6f4 v[2:5], v[224:231], v[208:215], v[2:5]
	s_setprio 0
	s_barrier
	ds_read_b128 v[162:165], v151
	ds_read_b128 v[166:169], v152
	ds_read_b128 v[170:173], v153
	ds_read_b128 v[174:177], v154
	ds_read_b128 v[178:181], v159 offset:32768
	ds_read_b128 v[182:185], v159 offset:33792
	ds_read_b128 v[192:195], v159 offset:34816
	ds_read_b128 v[196:199], v159 offset:35840
	ds_read_b128 v[200:203], v159 offset:36864
	ds_read_b128 v[204:207], v159 offset:37888
	ds_read_b128 v[208:211], v159 offset:38912
	ds_read_b128 v[212:215], v159 offset:39936
	s_add_u32 s22, s28, 0xe0000
	s_mov_b32 m0, s56
	s_addc_u32 s23, s29, 0
	global_load_lds_dwordx4 v138, s[22:23]
	s_add_u32 s22, s28, 0x150000
	s_mov_b32 m0, s57
	s_addc_u32 s23, s29, 0
	global_load_lds_dwordx4 v138, s[22:23]
	s_waitcnt lgkmcnt(8)
	s_barrier
; __device__ __forceinline__ unsigned cvt_pk_bf16(float lo, float hi) { unsigned r; asm volatile("v_cvt_pk_bf16_f32 %0, %1, %2" : "=v"(r) : "v"(lo), "v"(hi)); return r; }
; #define PG8_STAGE(bufoff, gbase, voff) do { _Pragma("unroll") for (int _i = 0; _i < 2; ++_i) glds16_s((const void*)((const char*)(gbase) + _i * r64), (voff), ldsb + (unsigned)(bufoff) + ldsw + _i * 8192u); } while (0)
; #define PG8_LDA(b, h) do { _Pragma("unroll") for (int m = 0; m < 4; ++m) { const int o_ = PG8_SA(b, h) + aoff + m * 2048; \
;         if constexpr (FP8) A8[m] = PG8_CAT8(o_); else { At[m][0] = PG8_LD16(o_); At[m][1] = PG8_LD16(o_ + 1024); } } } while (0)
; #define PG8_WAIT_V(n) asm volatile("s_waitcnt vmcnt(" #n ")" ::: "memory")
; #define PG8_WAIT_L(n) asm volatile("s_waitcnt lgkmcnt(" #n ")" ::: "memory")
; #define PG8_BAR __builtin_amdgcn_s_barrier()
;     __device__ __forceinline__ void operator()(const f32x4 (&acc)[2][2][4][2], const Unit& u, int wr, int wc, int fr, int fq) const {
;         const int row0 = u.pm * BM + wr * 64 + fr, col0 = u.pn * BM + wc * 32 + 8 * fq;
; #pragma unroll
;         for (int ai = 0; ai < 2; ++ai)
; #pragma unroll
;             for (int m = 0; m < 4; ++m) { bf16_t* rowp = O + (size_t)(row0 + ai * HALF + m * 16) * ldc + col0;
; #pragma unroll
;                 for (int bj = 0; bj < 2; ++bj) { const f32x4 v0 = acc[ai][bj][m][0] * scale, v1 = acc[ai][bj][m][1] * scale;
;                     u32x4 w; w.x = cvt_pk_bf16(v0[0], v0[1]); w.y = cvt_pk_bf16(v0[2], v0[3]); w.z = cvt_pk_bf16(v1[0], v1[1]); w.w = cvt_pk_bf16(v1[2], v1[3]);
;                     *(u32x4*)(rowp + bj * HALF) = w; } }
; template <class Epi, class Sched, bool FP8 = false>
; __device__ __forceinline__ void gemm_phase(LAS unsigned char* lds, const int Kb, const int nt  , const Sched& S, const Epi& E) {
;     ...
;             PG8_WAIT_L(8); PG8_BAR; PG8_HI; PG8_WAIT_L(0); PG8_MMA(0, 0, B0, B08); PG8_BAR; PG8_LO; PG8_SCHED;
;             PG8_LDB(B1, B18, 1, 1); PG8_STAGE(PG8_SB(1, 0), b3, voffB);
;             PG8_BAR; PG8_HI; PG8_WAIT_L(0); PG8_MMA(0, 1, B1, B18); PG8_BAR; PG8_LO;
;             PG8_LDA(1, 1); PG8_STAGE(PG8_SA(1, 0), a3, voffA);
;             PG8_BAR; PG8_HI; PG8_WAIT_L(0); PG8_MMA(1, 0, B0, B08); PG8_BAR; PG8_LO; PG8_SCHED;
;             PG8_STAGE(PG8_SB(1, 1), b3 + hstep, voffB);
;             PG8_WAIT_V(6); PG8_BAR; PG8_HI; PG8_MMA(1, 1, B1, B18); PG8_BAR; PG8_LO;
	s_waitcnt lgkmcnt(0)
	s_setprio 1
	v_mfma_f32_16x16x128_f8f6f4 v[130:133], v[162:169], v[178:185], v[130:133]
	v_mfma_f32_16x16x128_f8f6f4 v[126:129], v[170:177], v[178:185], v[126:129]
	v_mfma_f32_16x16x128_f8f6f4 v[114:117], v[162:169], v[192:199], v[114:117]
	v_mfma_f32_16x16x128_f8f6f4 v[110:113], v[170:177], v[192:199], v[110:113]
	v_mfma_f32_16x16x128_f8f6f4 v[98:101], v[162:169], v[200:207], v[98:101]
	v_mfma_f32_16x16x128_f8f6f4 v[94:97], v[170:177], v[200:207], v[94:97]
	v_mfma_f32_16x16x128_f8f6f4 v[82:85], v[162:169], v[208:215], v[82:85]
	v_mfma_f32_16x16x128_f8f6f4 v[78:81], v[170:177], v[208:215], v[78:81]
	s_setprio 0
	s_barrier
	ds_read_b128 v[216:219], v155
	ds_read_b128 v[220:223], v156
	s_add_u32 s22, s26, 0x80
	s_addc_u32 s23, s27, 0
	ds_read_b128 v[224:227], v157
	s_mov_b32 m0, s59
	ds_read_b128 v[228:231], v158
	global_load_lds_dwordx4 v142, s[22:23]
	s_add_u32 s22, s26, 0x70080
	s_mov_b32 m0, s60
	s_addc_u32 s23, s27, 0
	global_load_lds_dwordx4 v142, s[22:23]
	s_barrier
	s_waitcnt lgkmcnt(0)
	s_setprio 1
	v_mfma_f32_16x16x128_f8f6f4 v[122:125], v[216:223], v[178:185], v[122:125]
	v_mfma_f32_16x16x128_f8f6f4 v[118:121], v[224:231], v[178:185], v[118:121]
	v_mfma_f32_16x16x128_f8f6f4 v[106:109], v[216:223], v[192:199], v[106:109]
	v_mfma_f32_16x16x128_f8f6f4 v[102:105], v[224:231], v[192:199], v[102:105]
	v_mfma_f32_16x16x128_f8f6f4 v[90:93], v[216:223], v[200:207], v[90:93]
	v_mfma_f32_16x16x128_f8f6f4 v[86:89], v[224:231], v[200:207], v[86:89]
	v_mfma_f32_16x16x128_f8f6f4 v[74:77], v[216:223], v[208:215], v[74:77]
	v_mfma_f32_16x16x128_f8f6f4 v[70:73], v[224:231], v[208:215], v[70:73]
	s_setprio 0
	s_barrier
	ds_read_b128 v[178:181], v159 offset:49152
	ds_read_b128 v[182:185], v159 offset:50176
	ds_read_b128 v[192:195], v159 offset:51200
	ds_read_b128 v[196:199], v159 offset:52224
	ds_read_b128 v[200:203], v159 offset:53248
	ds_read_b128 v[204:207], v159 offset:54272
	ds_read_b128 v[208:211], v159 offset:55296
	s_mov_b32 m0, s61
	ds_read_b128 v[212:215], v159 offset:56320
	global_load_lds_dwordx4 v138, s[30:31]
	s_add_u32 s22, s28, 0x70080
	s_mov_b32 m0, s62
	s_addc_u32 s23, s29, 0
	global_load_lds_dwordx4 v138, s[22:23]
	s_barrier
	s_waitcnt lgkmcnt(0)
	s_setprio 1
	v_mfma_f32_16x16x128_f8f6f4 v[66:69], v[162:169], v[178:185], v[66:69]
	v_mfma_f32_16x16x128_f8f6f4 v[62:65], v[170:177], v[178:185], v[62:65]
	v_mfma_f32_16x16x128_f8f6f4 v[54:57], v[162:169], v[192:199], v[54:57]
	v_mfma_f32_16x16x128_f8f6f4 v[46:49], v[170:177], v[192:199], v[46:49]
	v_mfma_f32_16x16x128_f8f6f4 v[38:41], v[162:169], v[200:207], v[38:41]
	v_mfma_f32_16x16x128_f8f6f4 v[30:33], v[170:177], v[200:207], v[30:33]
	v_mfma_f32_16x16x128_f8f6f4 v[22:25], v[162:169], v[208:215], v[22:25]
	v_mfma_f32_16x16x128_f8f6f4 v[14:17], v[170:177], v[208:215], v[14:17]
	s_setprio 0
	s_barrier
	s_add_u32 s22, s26, 0xe0080
	s_mov_b32 m0, s63
	s_addc_u32 s23, s27, 0
	global_load_lds_dwordx4 v142, s[22:23]
	s_add_u32 s22, s26, 0x150080
	s_mov_b32 m0, s64
	s_addc_u32 s23, s27, 0
	global_load_lds_dwordx4 v142, s[22:23]
	s_add_i32 s77, s77, 2
	s_add_u32 s75, s75, 0x100
	s_addc_u32 s76, s76, 0
	s_cmp_gt_u32 s77, 53
	s_mov_b64 s[22:23], s[24:25]
	s_waitcnt vmcnt(6)
	s_barrier
	s_setprio 1
	v_mfma_f32_16x16x128_f8f6f4 v[58:61], v[216:223], v[178:185], v[58:61]
	v_mfma_f32_16x16x128_f8f6f4 v[50:53], v[224:231], v[178:185], v[50:53]
	v_mfma_f32_16x16x128_f8f6f4 v[42:45], v[216:223], v[192:199], v[42:45]
	v_mfma_f32_16x16x128_f8f6f4 v[34:37], v[224:231], v[192:199], v[34:37]
	v_mfma_f32_16x16x128_f8f6f4 v[26:29], v[216:223], v[200:207], v[26:29]
	v_mfma_f32_16x16x128_f8f6f4 v[18:21], v[224:231], v[200:207], v[18:21]
	v_mfma_f32_16x16x128_f8f6f4 v[10:13], v[216:223], v[208:215], v[10:13]
	v_mfma_f32_16x16x128_f8f6f4 v[2:5], v[224:231], v[208:215], v[2:5]
	s_setprio 0
	s_barrier
	s_cbranch_scc0 .LBB0_2851
	s_lshl_b32 s22, s74, 8
	v_mbcnt_lo_u32_b32 v6, -1, 0
	v_mbcnt_hi_u32_b32 v6, -1, v6
	s_add_i32 s22, s22, s3
	v_and_or_b32 v8, v6, 15, s22
	s_lshl_b32 s22, s73, 8
	v_ashrrev_i32_e32 v6, 1, v6
	s_or_b32 s22, s22, s58
	v_and_b32_e32 v6, -8, v6
	v_add_u32_e32 v6, s22, v6
	v_ashrrev_i32_e32 v9, 31, v8
	v_ashrrev_i32_e32 v7, 31, v6
	v_lshlrev_b64 v[134:135], 12, v[8:9]
	v_lshl_add_u64 v[134:135], s[4:5], 0, v[134:135]
	v_lshlrev_b64 v[136:137], 1, v[6:7]
	v_lshl_add_u64 v[6:7], v[134:135], 0, v[136:137]
	v_pk_mul_f32 v[132:133], v[132:133], s[6:7] op_sel_hi:[1,0]
	v_pk_mul_f32 v[130:131], v[130:131], s[6:7] op_sel_hi:[1,0]
	v_pk_mul_f32 v[134:135], v[128:129], s[6:7] op_sel_hi:[1,0]
	v_pk_mul_f32 v[128:129], v[126:127], s[6:7] op_sel_hi:[1,0]
	v_cvt_pk_bf16_f32 v126, v130, v131
	v_cvt_pk_bf16_f32 v127, v132, v133
	v_pk_mul_f32 v[122:123], v[122:123], s[6:7] op_sel_hi:[1,0]
	v_cvt_pk_bf16_f32 v128, v128, v129
	v_cvt_pk_bf16_f32 v129, v134, v135
	global_store_dwordx4 v[6:7], v[126:129], off
	v_pk_mul_f32 v[124:125], v[124:125], s[6:7] op_sel_hi:[1,0]
	v_pk_mul_f32 v[116:117], v[116:117], s[6:7] op_sel_hi:[1,0]
	v_pk_mul_f32 v[126:127], v[120:121], s[6:7] op_sel_hi:[1,0]
	v_pk_mul_f32 v[120:121], v[118:119], s[6:7] op_sel_hi:[1,0]
	v_cvt_pk_bf16_f32 v118, v122, v123
	v_cvt_pk_bf16_f32 v119, v124, v125
	v_pk_mul_f32 v[114:115], v[114:115], s[6:7] op_sel_hi:[1,0]
	v_cvt_pk_bf16_f32 v120, v120, v121
	v_cvt_pk_bf16_f32 v121, v126, v127
	global_store_dwordx4 v[6:7], v[118:121], off offset:256
	v_pk_mul_f32 v[106:107], v[106:107], s[6:7] op_sel_hi:[1,0]
	v_pk_mul_f32 v[108:109], v[108:109], s[6:7] op_sel_hi:[1,0]
	v_or_b32_e32 v118, 16, v8
	v_ashrrev_i32_e32 v119, 31, v118
	v_lshlrev_b64 v[118:119], 12, v[118:119]
	v_lshl_add_u64 v[118:119], s[4:5], 0, v[118:119]
; __device__ __forceinline__ unsigned cvt_pk_bf16(float lo, float hi) { unsigned r; asm volatile("v_cvt_pk_bf16_f32 %0, %1, %2" : "=v"(r) : "v"(lo), "v"(hi)); return r; }
; #define PG8_WAIT_V(n) asm volatile("s_waitcnt vmcnt(" #n ")" ::: "memory")
; #define PG8_BAR __builtin_amdgcn_s_barrier()
;     __device__ __forceinline__ void operator()(const f32x4 (&acc)[2][2][4][2], const Unit& u, int wr, int wc, int fr, int fq) const {
;         const int row0 = u.pm * BM + wr * 64 + fr, col0 = u.pn * BM + wc * 32 + 8 * fq;
; #pragma unroll
;         for (int ai = 0; ai < 2; ++ai)
; #pragma unroll
;             for (int m = 0; m < 4; ++m) { bf16_t* rowp = O + (size_t)(row0 + ai * HALF + m * 16) * ldc + col0;
; #pragma unroll
;                 for (int bj = 0; bj < 2; ++bj) { const f32x4 v0 = acc[ai][bj][m][0] * scale, v1 = acc[ai][bj][m][1] * scale;
;                     u32x4 w; w.x = cvt_pk_bf16(v0[0], v0[1]); w.y = cvt_pk_bf16(v0[2], v0[3]); w.z = cvt_pk_bf16(v1[0], v1[1]); w.w = cvt_pk_bf16(v1[2], v1[3]);
;                     *(u32x4*)(rowp + bj * HALF) = w; } }
; template <class Epi, class Sched, bool FP8 = false>
; __device__ __forceinline__ void gemm_phase(LAS unsigned char* lds, const int Kb, const int nt  , const Sched& S, const Epi& E) {
;     ...
;         if (!has_next) break;
; #pragma unroll
;         for (int a = 0; a < 2; ++a)
; #pragma unroll
;             for (int b = 0; b < 2; ++b)
; #pragma unroll
;                 for (int m = 0; m < 4; ++m)
; #pragma unroll
;                     for (int n = 0; n < 2; ++n) acc[a][b][m][n] = (f32x4){0.f, 0.f, 0.f, 0.f};
;         cur = nxt; cA = nA; cB = nB; ++ui;
;     }
;     PG8_WAIT_V(0);
;     if (wr == 0) PG8_BAR;
;     PG8_BAR;
	v_lshl_add_u64 v[118:119], v[118:119], 0, v[136:137]
	v_pk_mul_f32 v[120:121], v[112:113], s[6:7] op_sel_hi:[1,0]
	v_pk_mul_f32 v[112:113], v[110:111], s[6:7] op_sel_hi:[1,0]
	v_cvt_pk_bf16_f32 v110, v114, v115
	v_cvt_pk_bf16_f32 v111, v116, v117
	v_pk_mul_f32 v[100:101], v[100:101], s[6:7] op_sel_hi:[1,0]
	v_cvt_pk_bf16_f32 v112, v112, v113
	v_cvt_pk_bf16_f32 v113, v120, v121
	global_store_dwordx4 v[118:119], v[110:113], off
	v_pk_mul_f32 v[98:99], v[98:99], s[6:7] op_sel_hi:[1,0]
	v_pk_mul_f32 v[92:93], v[92:93], s[6:7] op_sel_hi:[1,0]
	v_pk_mul_f32 v[110:111], v[104:105], s[6:7] op_sel_hi:[1,0]
	v_pk_mul_f32 v[104:105], v[102:103], s[6:7] op_sel_hi:[1,0]
	v_cvt_pk_bf16_f32 v102, v106, v107
	v_cvt_pk_bf16_f32 v103, v108, v109
	v_pk_mul_f32 v[90:91], v[90:91], s[6:7] op_sel_hi:[1,0]
	v_cvt_pk_bf16_f32 v104, v104, v105
	v_cvt_pk_bf16_f32 v105, v110, v111
	global_store_dwordx4 v[118:119], v[102:105], off offset:256
	v_pk_mul_f32 v[84:85], v[84:85], s[6:7] op_sel_hi:[1,0]
	v_pk_mul_f32 v[82:83], v[82:83], s[6:7] op_sel_hi:[1,0]
	v_or_b32_e32 v102, 32, v8
	v_ashrrev_i32_e32 v103, 31, v102
	v_lshlrev_b64 v[102:103], 12, v[102:103]
	v_or_b32_e32 v8, 48, v8
	v_lshl_add_u64 v[102:103], s[4:5], 0, v[102:103]
	v_ashrrev_i32_e32 v9, 31, v8
	v_lshl_add_u64 v[102:103], v[102:103], 0, v[136:137]
	v_pk_mul_f32 v[104:105], v[96:97], s[6:7] op_sel_hi:[1,0]
	v_pk_mul_f32 v[96:97], v[94:95], s[6:7] op_sel_hi:[1,0]
	v_cvt_pk_bf16_f32 v94, v98, v99
	v_cvt_pk_bf16_f32 v95, v100, v101
	v_lshlrev_b64 v[8:9], 12, v[8:9]
	v_cvt_pk_bf16_f32 v96, v96, v97
	v_cvt_pk_bf16_f32 v97, v104, v105
	global_store_dwordx4 v[102:103], v[94:97], off
	v_lshl_add_u64 v[8:9], s[4:5], 0, v[8:9]
	v_lshl_add_u64 v[8:9], v[8:9], 0, v[136:137]
	v_pk_mul_f32 v[94:95], v[88:89], s[6:7] op_sel_hi:[1,0]
	v_pk_mul_f32 v[88:89], v[86:87], s[6:7] op_sel_hi:[1,0]
	v_cvt_pk_bf16_f32 v86, v90, v91
	v_cvt_pk_bf16_f32 v87, v92, v93
	v_pk_mul_f32 v[76:77], v[76:77], s[6:7] op_sel_hi:[1,0]
	v_cvt_pk_bf16_f32 v88, v88, v89
	v_cvt_pk_bf16_f32 v89, v94, v95
	global_store_dwordx4 v[102:103], v[86:89], off offset:256
	v_pk_mul_f32 v[74:75], v[74:75], s[6:7] op_sel_hi:[1,0]
	v_pk_mul_f32 v[66:67], v[66:67], s[6:7] op_sel_hi:[1,0]
	v_pk_mul_f32 v[86:87], v[80:81], s[6:7] op_sel_hi:[1,0]
	v_pk_mul_f32 v[80:81], v[78:79], s[6:7] op_sel_hi:[1,0]
	v_cvt_pk_bf16_f32 v78, v82, v83
	v_cvt_pk_bf16_f32 v79, v84, v85
	v_pk_mul_f32 v[68:69], v[68:69], s[6:7] op_sel_hi:[1,0]
	v_cvt_pk_bf16_f32 v80, v80, v81
	v_cvt_pk_bf16_f32 v81, v86, v87
	global_store_dwordx4 v[8:9], v[78:81], off
	v_pk_mul_f32 v[60:61], v[60:61], s[6:7] op_sel_hi:[1,0]
	v_pk_mul_f32 v[58:59], v[58:59], s[6:7] op_sel_hi:[1,0]
	v_pk_mul_f32 v[78:79], v[72:73], s[6:7] op_sel_hi:[1,0]
	v_pk_mul_f32 v[72:73], v[70:71], s[6:7] op_sel_hi:[1,0]
	v_cvt_pk_bf16_f32 v70, v74, v75
	v_cvt_pk_bf16_f32 v71, v76, v77
	v_pk_mul_f32 v[44:45], v[44:45], s[6:7] op_sel_hi:[1,0]
	v_cvt_pk_bf16_f32 v72, v72, v73
	v_cvt_pk_bf16_f32 v73, v78, v79
	global_store_dwordx4 v[8:9], v[70:73], off offset:256
	v_lshl_add_u64 v[8:9], v[6:7], 0, s[8:9]
	v_pk_mul_f32 v[42:43], v[42:43], s[6:7] op_sel_hi:[1,0]
	v_pk_mul_f32 v[70:71], v[64:65], s[6:7] op_sel_hi:[1,0]
	v_pk_mul_f32 v[64:65], v[62:63], s[6:7] op_sel_hi:[1,0]
	v_cvt_pk_bf16_f32 v62, v66, v67
	v_add_co_u32_e32 v66, vcc, s67, v6
	v_cvt_pk_bf16_f32 v63, v68, v69
	v_cvt_pk_bf16_f32 v64, v64, v65
	v_cvt_pk_bf16_f32 v65, v70, v71
	v_pk_mul_f32 v[28:29], v[28:29], s[6:7] op_sel_hi:[1,0]
	s_nop 0
	v_addc_co_u32_e32 v67, vcc, 0, v7, vcc
	global_store_dwordx4 v[66:67], v[62:65], off
	v_pk_mul_f32 v[26:27], v[26:27], s[6:7] op_sel_hi:[1,0]
	s_mov_b32 s73, s71
	v_pk_mul_f32 v[62:63], v[52:53], s[6:7] op_sel_hi:[1,0]
	v_pk_mul_f32 v[52:53], v[50:51], s[6:7] op_sel_hi:[1,0]
	v_cvt_pk_bf16_f32 v50, v58, v59
	v_cvt_pk_bf16_f32 v51, v60, v61
	s_mov_b32 s74, s72
	v_cvt_pk_bf16_f32 v52, v52, v53
	v_cvt_pk_bf16_f32 v53, v62, v63
	global_store_dwordx4 v[8:9], v[50:53], off offset:256
	v_lshl_add_u64 v[8:9], v[6:7], 0, s[10:11]
	s_mov_b64 s[24:25], s[20:21]
	v_pk_mul_f32 v[50:51], v[56:57], s[6:7] op_sel_hi:[1,0]
	v_pk_mul_f32 v[52:53], v[54:55], s[6:7] op_sel_hi:[1,0]
	v_pk_mul_f32 v[54:55], v[48:49], s[6:7] op_sel_hi:[1,0]
	v_pk_mul_f32 v[48:49], v[46:47], s[6:7] op_sel_hi:[1,0]
	v_cvt_pk_bf16_f32 v46, v52, v53
	v_cvt_pk_bf16_f32 v47, v50, v51
	v_add_co_u32_e32 v50, vcc, s68, v6
	v_cvt_pk_bf16_f32 v48, v48, v49
	v_cvt_pk_bf16_f32 v49, v54, v55
	s_mov_b64 s[22:23], s[18:19]
	s_nop 0
	v_addc_co_u32_e32 v51, vcc, 0, v7, vcc
	global_store_dwordx4 v[50:51], v[46:49], off
	v_readlane_b32 s79, v241, 49
	v_pk_mul_f32 v[10:11], v[10:11], s[6:7] op_sel_hi:[1,0]
	v_pk_mul_f32 v[46:47], v[36:37], s[6:7] op_sel_hi:[1,0]
	v_pk_mul_f32 v[36:37], v[34:35], s[6:7] op_sel_hi:[1,0]
	v_cvt_pk_bf16_f32 v34, v42, v43
	v_cvt_pk_bf16_f32 v35, v44, v45
	s_nop 0
	v_cvt_pk_bf16_f32 v36, v36, v37
	v_cvt_pk_bf16_f32 v37, v46, v47
	global_store_dwordx4 v[8:9], v[34:37], off offset:256
	v_lshl_add_u64 v[8:9], v[6:7], 0, s[12:13]
	s_nop 0
	v_pk_mul_f32 v[34:35], v[40:41], s[6:7] op_sel_hi:[1,0]
	v_pk_mul_f32 v[36:37], v[38:39], s[6:7] op_sel_hi:[1,0]
	v_pk_mul_f32 v[38:39], v[32:33], s[6:7] op_sel_hi:[1,0]
	v_pk_mul_f32 v[32:33], v[30:31], s[6:7] op_sel_hi:[1,0]
	v_cvt_pk_bf16_f32 v30, v36, v37
	v_cvt_pk_bf16_f32 v31, v34, v35
	v_add_co_u32_e32 v34, vcc, s69, v6
	v_cvt_pk_bf16_f32 v32, v32, v33
	v_cvt_pk_bf16_f32 v33, v38, v39
	s_nop 1
	v_addc_co_u32_e32 v35, vcc, 0, v7, vcc
	global_store_dwordx4 v[34:35], v[30:33], off
	s_nop 1
	v_pk_mul_f32 v[30:31], v[20:21], s[6:7] op_sel_hi:[1,0]
	v_pk_mul_f32 v[20:21], v[18:19], s[6:7] op_sel_hi:[1,0]
	v_cvt_pk_bf16_f32 v18, v26, v27
	v_cvt_pk_bf16_f32 v19, v28, v29
	s_nop 0
	v_cvt_pk_bf16_f32 v20, v20, v21
	v_cvt_pk_bf16_f32 v21, v30, v31
	global_store_dwordx4 v[8:9], v[18:21], off offset:256
	v_lshl_add_u64 v[8:9], v[6:7], 0, s[14:15]
	v_add_co_u32_e32 v6, vcc, s70, v6
	v_pk_mul_f32 v[20:21], v[22:23], s[6:7] op_sel_hi:[1,0]
	v_pk_mul_f32 v[22:23], v[16:17], s[6:7] op_sel_hi:[1,0]
	v_pk_mul_f32 v[16:17], v[14:15], s[6:7] op_sel_hi:[1,0]
	v_addc_co_u32_e32 v7, vcc, 0, v7, vcc
	v_pk_mul_f32 v[18:19], v[24:25], s[6:7] op_sel_hi:[1,0]
	v_cvt_pk_bf16_f32 v14, v20, v21
	s_and_b64 vcc, exec, s[16:17]
	v_cvt_pk_bf16_f32 v15, v18, v19
	v_cvt_pk_bf16_f32 v16, v16, v17
	v_cvt_pk_bf16_f32 v17, v22, v23
	global_store_dwordx4 v[6:7], v[14:17], off
	v_pk_mul_f32 v[6:7], v[12:13], s[6:7] op_sel_hi:[1,0]
	v_pk_mul_f32 v[12:13], v[4:5], s[6:7] op_sel_hi:[1,0]
	v_pk_mul_f32 v[4:5], v[2:3], s[6:7] op_sel_hi:[1,0]
	v_cvt_pk_bf16_f32 v2, v10, v11
	v_cvt_pk_bf16_f32 v3, v6, v7
	s_nop 0
	v_cvt_pk_bf16_f32 v4, v4, v5
	v_cvt_pk_bf16_f32 v5, v12, v13
	global_store_dwordx4 v[8:9], v[2:5], off offset:256
	s_cbranch_vccz .LBB0_2848
	s_waitcnt vmcnt(0)
	s_cmpk_gt_u32 s7, 0xff
	s_cbranch_scc1 .LBB0_2855
	s_barrier

;     __device__ __forceinline__ bool next(int i, Unit& u) const { if (!order_tile(i, G, c, nM, nN, u.pm, u.pn)) return false; u.A = A0 + (size_t)u.pm * tstep; u.B = B0 + (size_t)u.pn * tstep; return true; }
;     __device__ __forceinline__ bool next(int i, Unit& u) const { if (!order_tile(i, G, c, nM, nN, u.pm, u.pn)) return false; u.A = A0 + (size_t)(u.pn >> 1) * groupA + (size_t)u.pm * tstep; u.B = B0 + (size_t)u.pn * tstep; return true; }
; #define PG8_STAGE(bufoff, gbase, voff) do { _Pragma("unroll") for (int _i = 0; _i < 2; ++_i) glds16_s((const void*)((const char*)(gbase) + _i * r64), (voff), ldsb + (unsigned)(bufoff) + ldsw + _i * 8192u); } while (0)
; #define PG8_WAIT_V(n) asm volatile("s_waitcnt vmcnt(" #n ")" ::: "memory")
; #define PG8_BAR __builtin_amdgcn_s_barrier()
; template <class Epi, class Sched, bool FP8 = false>
; __device__ __forceinline__ void gemm_phase(LAS unsigned char* lds, const int Kb, const int nt  , const Sched& S, const Epi& E) {
;     ...
;         const bool has_next = S.next(ui + 1, nxt);
;         const char* nA = has_next ? nxt.A : cA; const char* nB = has_next ? nxt.B : cB;
;         for (int t = 0; t < nt; t += 2) {
;             const bool last = (t == nt - 2);
;             const char* a1 = cA + (size_t)(t + 1) * kstep;
;             const char* a2 = last ? nA : cA + (size_t)(t + 2) * kstep; const char* b2 = last ? nB : cB + (size_t)(t + 2) * kstep;
;             const char* a3 = a2 + kstep; const char* b3 = b2 + kstep;
;             PG8_LDB(B0, B08, 0, 0); PG8_SCHED; PG8_LDA(0, 0); PG8_STAGE(PG8_SA(1, 1), a1 + hstep, voffA);
;             PG8_WAIT_L(8); PG8_BAR; PG8_HI; PG8_WAIT_L(0); PG8_MMA(0, 0, B0, B08); PG8_BAR; PG8_LO; PG8_SCHED;
;             PG8_LDB(B1, B18, 0, 1); PG8_STAGE(PG8_SB(0, 0), b2, voffB);
;             PG8_BAR; PG8_HI; PG8_WAIT_L(0); PG8_MMA(0, 1, B1, B18); PG8_BAR; PG8_LO;
;             PG8_LDA(0, 1); PG8_STAGE(PG8_SA(0, 0), a2, voffA);
;             PG8_BAR; PG8_HI; PG8_WAIT_L(0); PG8_MMA(1, 0, B0, B08); PG8_BAR; PG8_LO; PG8_SCHED;
;             PG8_STAGE(PG8_SB(0, 1), b2 + hstep, voffB);
;             PG8_WAIT_V(6); PG8_BAR; PG8_HI; PG8_MMA(1, 1, B1, B18); PG8_BAR; PG8_LO;
;             PG8_LDB(B0, B08, 1, 0); PG8_SCHED; PG8_LDA(1, 0); PG8_STAGE(PG8_SA(0, 1), a2 + hstep, voffA);
;             PG8_WAIT_L(8); PG8_BAR; PG8_HI; PG8_WAIT_L(0); PG8_MMA(0, 0, B0, B08); PG8_BAR; PG8_LO; PG8_SCHED;
.LBB0_2865:
	ds_read_b128 v[156:159], v136
	ds_read_b128 v[160:163], v137
	ds_read_b128 v[164:167], v139
	ds_read_b128 v[168:171], v140
	s_add_u32 s24, s22, 0x100
	s_addc_u32 s25, s23, 0
	s_cmp_eq_u32 s73, 10
	s_cselect_b32 s28, s18, s24
	s_cselect_b32 s29, s19, s25
	s_cselect_b32 s26, s20, s71
	s_cselect_b32 s27, s21, s72
	s_add_u32 s30, s28, 0x80
	s_addc_u32 s31, s29, 0
	ds_read_b128 v[172:175], v153
	ds_read_b128 v[176:179], v153 offset:1024
	ds_read_b128 v[180:183], v153 offset:2048
	ds_read_b128 v[184:187], v153 offset:3072
	ds_read_b128 v[192:195], v153 offset:4096
	ds_read_b128 v[196:199], v153 offset:5120
	ds_read_b128 v[200:203], v153 offset:6144
	ds_read_b128 v[204:207], v153 offset:7168
	s_add_u32 s74, s22, 0xe0080
	s_mov_b32 m0, s61
	s_addc_u32 s75, s23, 0
	global_load_lds_dwordx4 v138, s[74:75]
	s_add_u32 s22, s22, 0x150080
	s_mov_b32 m0, s62
	s_addc_u32 s23, s23, 0
	global_load_lds_dwordx4 v138, s[22:23]
	s_waitcnt lgkmcnt(8)
	s_barrier
	s_waitcnt lgkmcnt(0)
	s_setprio 1
	v_mfma_f32_16x16x128_f8f6f4 v[128:131], v[156:163], v[172:179], v[128:131]
	v_mfma_f32_16x16x128_f8f6f4 v[124:127], v[164:171], v[172:179], v[124:127]
	v_mfma_f32_16x16x128_f8f6f4 v[116:119], v[156:163], v[180:187], v[116:119]
	v_mfma_f32_16x16x128_f8f6f4 v[108:111], v[164:171], v[180:187], v[108:111]
	v_mfma_f32_16x16x128_f8f6f4 v[100:103], v[156:163], v[192:199], v[100:103]
	v_mfma_f32_16x16x128_f8f6f4 v[92:95], v[164:171], v[192:199], v[92:95]
	v_mfma_f32_16x16x128_f8f6f4 v[84:87], v[156:163], v[200:207], v[84:87]
	v_mfma_f32_16x16x128_f8f6f4 v[76:79], v[164:171], v[200:207], v[76:79]
	s_setprio 0
	s_barrier
	ds_read_b128 v[208:211], v141
	ds_read_b128 v[212:215], v142
	ds_read_b128 v[216:219], v143
	s_mov_b32 m0, s46
	ds_read_b128 v[220:223], v144
	global_load_lds_dwordx4 v138, s[26:27]
	s_add_u32 s22, s26, 0x70000
	s_mov_b32 m0, s47
	s_addc_u32 s23, s27, 0
	global_load_lds_dwordx4 v138, s[22:23]
	s_barrier
	s_waitcnt lgkmcnt(0)
	s_setprio 1
	v_mfma_f32_16x16x128_f8f6f4 v[120:123], v[208:215], v[172:179], v[120:123]
	v_mfma_f32_16x16x128_f8f6f4 v[112:115], v[216:223], v[172:179], v[112:115]
	v_mfma_f32_16x16x128_f8f6f4 v[104:107], v[208:215], v[180:187], v[104:107]
	v_mfma_f32_16x16x128_f8f6f4 v[96:99], v[216:223], v[180:187], v[96:99]
	v_mfma_f32_16x16x128_f8f6f4 v[88:91], v[208:215], v[192:199], v[88:91]
	v_mfma_f32_16x16x128_f8f6f4 v[80:83], v[216:223], v[192:199], v[80:83]
	v_mfma_f32_16x16x128_f8f6f4 v[72:75], v[208:215], v[200:207], v[72:75]
	v_mfma_f32_16x16x128_f8f6f4 v[68:71], v[216:223], v[200:207], v[68:71]
	s_setprio 0
	s_barrier
	ds_read_b128 v[172:175], v153 offset:16384
	ds_read_b128 v[176:179], v153 offset:17408
	ds_read_b128 v[180:183], v153 offset:18432
	ds_read_b128 v[184:187], v153 offset:19456
	ds_read_b128 v[192:195], v153 offset:20480
	ds_read_b128 v[196:199], v153 offset:21504
	ds_read_b128 v[200:203], v153 offset:22528
	s_mov_b32 m0, s45
	ds_read_b128 v[204:207], v153 offset:23552
	global_load_lds_dwordx4 v138, s[28:29]
	s_add_u32 s22, s28, 0x70000
	s_mov_b32 m0, s48
	s_addc_u32 s23, s29, 0
	global_load_lds_dwordx4 v138, s[22:23]
	s_barrier
	s_waitcnt lgkmcnt(0)
	s_setprio 1
	v_mfma_f32_16x16x128_f8f6f4 v[64:67], v[156:163], v[172:179], v[64:67]
	v_mfma_f32_16x16x128_f8f6f4 v[60:63], v[164:171], v[172:179], v[60:63]
	v_mfma_f32_16x16x128_f8f6f4 v[56:59], v[156:163], v[180:187], v[56:59]
	v_mfma_f32_16x16x128_f8f6f4 v[48:51], v[164:171], v[180:187], v[48:51]
	v_mfma_f32_16x16x128_f8f6f4 v[40:43], v[156:163], v[192:199], v[40:43]
	v_mfma_f32_16x16x128_f8f6f4 v[32:35], v[164:171], v[192:199], v[32:35]
	v_mfma_f32_16x16x128_f8f6f4 v[24:27], v[156:163], v[200:207], v[24:27]
	v_mfma_f32_16x16x128_f8f6f4 v[12:15], v[164:171], v[200:207], v[12:15]
	s_setprio 0
	s_barrier
	s_add_u32 s22, s26, 0xe0000
	s_mov_b32 m0, s49
	s_addc_u32 s23, s27, 0
	global_load_lds_dwordx4 v138, s[22:23]
	s_add_u32 s22, s26, 0x150000
	s_mov_b32 m0, s50
	s_addc_u32 s23, s27, 0
	global_load_lds_dwordx4 v138, s[22:23]
	s_waitcnt vmcnt(6)
	s_barrier
	s_setprio 1
	v_mfma_f32_16x16x128_f8f6f4 v[52:55], v[208:215], v[172:179], v[52:55]
	v_mfma_f32_16x16x128_f8f6f4 v[44:47], v[216:223], v[172:179], v[44:47]
	v_mfma_f32_16x16x128_f8f6f4 v[36:39], v[208:215], v[180:187], v[36:39]
	v_mfma_f32_16x16x128_f8f6f4 v[28:31], v[216:223], v[180:187], v[28:31]
	v_mfma_f32_16x16x128_f8f6f4 v[20:23], v[208:215], v[192:199], v[20:23]
	v_mfma_f32_16x16x128_f8f6f4 v[16:19], v[216:223], v[192:199], v[16:19]
	v_mfma_f32_16x16x128_f8f6f4 v[8:11], v[208:215], v[200:207], v[8:11]
	v_mfma_f32_16x16x128_f8f6f4 v[0:3], v[216:223], v[200:207], v[0:3]
	s_setprio 0
	s_barrier
	ds_read_b128 v[156:159], v145
	ds_read_b128 v[160:163], v146
	ds_read_b128 v[164:167], v147
	ds_read_b128 v[168:171], v148
	ds_read_b128 v[172:175], v153 offset:32768
	ds_read_b128 v[176:179], v153 offset:33792
	ds_read_b128 v[180:183], v153 offset:34816
	ds_read_b128 v[184:187], v153 offset:35840
	ds_read_b128 v[192:195], v153 offset:36864
	ds_read_b128 v[196:199], v153 offset:37888
	ds_read_b128 v[200:203], v153 offset:38912
	ds_read_b128 v[204:207], v153 offset:39936
	s_add_u32 s22, s28, 0xe0000
	s_mov_b32 m0, s51
	s_addc_u32 s23, s29, 0
	global_load_lds_dwordx4 v138, s[22:23]
	s_add_u32 s22, s28, 0x150000
	s_mov_b32 m0, s52
	s_addc_u32 s23, s29, 0
	global_load_lds_dwordx4 v138, s[22:23]
	s_waitcnt lgkmcnt(8)
	s_barrier
; #define PG8_STAGE(bufoff, gbase, voff) do { _Pragma("unroll") for (int _i = 0; _i < 2; ++_i) glds16_s((const void*)((const char*)(gbase) + _i * r64), (voff), ldsb + (unsigned)(bufoff) + ldsw + _i * 8192u); } while (0)
; #define PG8_LDA(b, h) do { _Pragma("unroll") for (int m = 0; m < 4; ++m) { const int o_ = PG8_SA(b, h) + aoff + m * 2048; \
;         if constexpr (FP8) A8[m] = PG8_CAT8(o_); else { At[m][0] = PG8_LD16(o_); At[m][1] = PG8_LD16(o_ + 1024); } } } while (0)
; #define PG8_WAIT_V(n) asm volatile("s_waitcnt vmcnt(" #n ")" ::: "memory")
; #define PG8_BAR __builtin_amdgcn_s_barrier()
;     __device__ __forceinline__ void operator()(const f32x4 (&acc)[2][2][4][2], const Unit& u, int wr, int wc, int fr, int fq) const {
;         const int row0 = u.pm * BM + wr * 64 + fr, col0 = u.pn * BM + wc * 32 + 4 * fq;
;         f32x4 cs[2][2];
; #pragma unroll
;         for (int bj = 0; bj < 2; ++bj)
; #pragma unroll
;             for (int n = 0; n < 2; ++n) cs[bj][n] = (cscale ? *(const f32x4*)(cscale + col0 + bj * HALF + n * 16) : (f32x4){1.f, 1.f, 1.f, 1.f}) * ascale;
; #pragma unroll
;         for (int ai = 0; ai < 2; ++ai)
; #pragma unroll
;             for (int m = 0; m < 4; ++m) { const size_t off = (size_t)(row0 + ai * HALF + m * 16) * ldc + col0;
; #pragma unroll
;                 for (int bj = 0; bj < 2; ++bj)
; #pragma unroll
;                     for (int n = 0; n < 2; ++n) { f32x4 v = acc[ai][bj][m][n] * cs[bj][n];
;                         if (res) v += *(const f32x4*)(res + off + bj * HALF + n * 16);
;                         *(f32x4*)(out + off + bj * HALF + n * 16) = v; }
; template <class Epi, class Sched, bool FP8 = false>
; __device__ __forceinline__ void gemm_phase(LAS unsigned char* lds, const int Kb, const int nt  , const Sched& S, const Epi& E) {
;     ...
;             PG8_WAIT_L(8); PG8_BAR; PG8_HI; PG8_WAIT_L(0); PG8_MMA(0, 0, B0, B08); PG8_BAR; PG8_LO; PG8_SCHED;
;             PG8_LDB(B1, B18, 1, 1); PG8_STAGE(PG8_SB(1, 0), b3, voffB);
;             PG8_BAR; PG8_HI; PG8_WAIT_L(0); PG8_MMA(0, 1, B1, B18); PG8_BAR; PG8_LO;
;             PG8_LDA(1, 1); PG8_STAGE(PG8_SA(1, 0), a3, voffA);
;             PG8_BAR; PG8_HI; PG8_WAIT_L(0); PG8_MMA(1, 0, B0, B08); PG8_BAR; PG8_LO; PG8_SCHED;
;             PG8_STAGE(PG8_SB(1, 1), b3 + hstep, voffB);
;             PG8_WAIT_V(6); PG8_BAR; PG8_HI; PG8_MMA(1, 1, B1, B18); PG8_BAR; PG8_LO;
	s_waitcnt lgkmcnt(0)
	s_setprio 1
	v_mfma_f32_16x16x128_f8f6f4 v[128:131], v[156:163], v[172:179], v[128:131]
	v_mfma_f32_16x16x128_f8f6f4 v[124:127], v[164:171], v[172:179], v[124:127]
	v_mfma_f32_16x16x128_f8f6f4 v[116:119], v[156:163], v[180:187], v[116:119]
	v_mfma_f32_16x16x128_f8f6f4 v[108:111], v[164:171], v[180:187], v[108:111]
	v_mfma_f32_16x16x128_f8f6f4 v[100:103], v[156:163], v[192:199], v[100:103]
	v_mfma_f32_16x16x128_f8f6f4 v[92:95], v[164:171], v[192:199], v[92:95]
	v_mfma_f32_16x16x128_f8f6f4 v[84:87], v[156:163], v[200:207], v[84:87]
	v_mfma_f32_16x16x128_f8f6f4 v[76:79], v[164:171], v[200:207], v[76:79]
	s_setprio 0
	s_barrier
	ds_read_b128 v[208:211], v149
	ds_read_b128 v[212:215], v150
	s_add_u32 s22, s26, 0x80
	s_addc_u32 s23, s27, 0
	ds_read_b128 v[216:219], v151
	s_mov_b32 m0, s55
	ds_read_b128 v[220:223], v152
	global_load_lds_dwordx4 v138, s[22:23]
	s_add_u32 s22, s26, 0x70080
	s_mov_b32 m0, s56
	s_addc_u32 s23, s27, 0
	global_load_lds_dwordx4 v138, s[22:23]
	s_barrier
	s_waitcnt lgkmcnt(0)
	s_setprio 1
	v_mfma_f32_16x16x128_f8f6f4 v[120:123], v[208:215], v[172:179], v[120:123]
	v_mfma_f32_16x16x128_f8f6f4 v[112:115], v[216:223], v[172:179], v[112:115]
	v_mfma_f32_16x16x128_f8f6f4 v[104:107], v[208:215], v[180:187], v[104:107]
	v_mfma_f32_16x16x128_f8f6f4 v[96:99], v[216:223], v[180:187], v[96:99]
	v_mfma_f32_16x16x128_f8f6f4 v[88:91], v[208:215], v[192:199], v[88:91]
	v_mfma_f32_16x16x128_f8f6f4 v[80:83], v[216:223], v[192:199], v[80:83]
	v_mfma_f32_16x16x128_f8f6f4 v[72:75], v[208:215], v[200:207], v[72:75]
	v_mfma_f32_16x16x128_f8f6f4 v[68:71], v[216:223], v[200:207], v[68:71]
	s_setprio 0
	s_barrier
	ds_read_b128 v[172:175], v153 offset:49152
	ds_read_b128 v[176:179], v153 offset:50176
	ds_read_b128 v[180:183], v153 offset:51200
	ds_read_b128 v[184:187], v153 offset:52224
	ds_read_b128 v[192:195], v153 offset:53248
	ds_read_b128 v[196:199], v153 offset:54272
	ds_read_b128 v[200:203], v153 offset:55296
	s_mov_b32 m0, s57
	ds_read_b128 v[204:207], v153 offset:56320
	global_load_lds_dwordx4 v138, s[30:31]
	s_add_u32 s22, s28, 0x70080
	s_mov_b32 m0, s58
	s_addc_u32 s23, s29, 0
	global_load_lds_dwordx4 v138, s[22:23]
	s_barrier
	s_waitcnt lgkmcnt(0)
	s_setprio 1
	v_mfma_f32_16x16x128_f8f6f4 v[64:67], v[156:163], v[172:179], v[64:67]
	v_mfma_f32_16x16x128_f8f6f4 v[60:63], v[164:171], v[172:179], v[60:63]
	v_mfma_f32_16x16x128_f8f6f4 v[56:59], v[156:163], v[180:187], v[56:59]
	v_mfma_f32_16x16x128_f8f6f4 v[48:51], v[164:171], v[180:187], v[48:51]
	v_mfma_f32_16x16x128_f8f6f4 v[40:43], v[156:163], v[192:199], v[40:43]
	v_mfma_f32_16x16x128_f8f6f4 v[32:35], v[164:171], v[192:199], v[32:35]
	v_mfma_f32_16x16x128_f8f6f4 v[24:27], v[156:163], v[200:207], v[24:27]
	v_mfma_f32_16x16x128_f8f6f4 v[12:15], v[164:171], v[200:207], v[12:15]
	s_setprio 0
	s_barrier
	s_add_u32 s22, s26, 0xe0080
	s_mov_b32 m0, s59
	s_addc_u32 s23, s27, 0
	global_load_lds_dwordx4 v138, s[22:23]
	s_add_u32 s22, s26, 0x150080
	s_mov_b32 m0, s60
	s_addc_u32 s23, s27, 0
	global_load_lds_dwordx4 v138, s[22:23]
	s_add_i32 s73, s73, 2
	s_add_u32 s71, s71, 0x100
	s_addc_u32 s72, s72, 0
	s_cmp_gt_u32 s73, 11
	s_mov_b64 s[22:23], s[24:25]
	s_waitcnt vmcnt(6)
	s_barrier
	s_setprio 1
	v_mfma_f32_16x16x128_f8f6f4 v[52:55], v[208:215], v[172:179], v[52:55]
	v_mfma_f32_16x16x128_f8f6f4 v[44:47], v[216:223], v[172:179], v[44:47]
	v_mfma_f32_16x16x128_f8f6f4 v[36:39], v[208:215], v[180:187], v[36:39]
	v_mfma_f32_16x16x128_f8f6f4 v[28:31], v[216:223], v[180:187], v[28:31]
	v_mfma_f32_16x16x128_f8f6f4 v[20:23], v[208:215], v[192:199], v[20:23]
	v_mfma_f32_16x16x128_f8f6f4 v[16:19], v[216:223], v[192:199], v[16:19]
	v_mfma_f32_16x16x128_f8f6f4 v[8:11], v[208:215], v[200:207], v[8:11]
	v_mfma_f32_16x16x128_f8f6f4 v[0:3], v[216:223], v[200:207], v[0:3]
	s_setprio 0
	s_barrier
	s_cbranch_scc0 .LBB0_2865
	s_lshl_b32 s22, s70, 8
	v_mbcnt_lo_u32_b32 v6, -1, 0
	v_mbcnt_hi_u32_b32 v6, -1, v6
	s_add_i32 s22, s22, s53
	s_lshl_b32 s23, s69, 8
	v_ashrrev_i32_e32 v4, 2, v6
	s_or_b32 s23, s23, s54
	v_and_b32_e32 v4, -4, v4
	v_and_or_b32 v6, v6, 15, s22
	v_add_u32_e32 v4, s23, v4
	v_ashrrev_i32_e32 v7, 31, v6
	v_ashrrev_i32_e32 v5, 31, v4
	v_lshlrev_b64 v[132:133], 13, v[6:7]
	v_lshl_add_u64 v[132:133], s[4:5], 0, v[132:133]
	v_lshlrev_b64 v[134:135], 2, v[4:5]
	v_lshl_add_u64 v[4:5], v[132:133], 0, v[134:135]
	v_pk_mul_f32 v[122:123], v[122:123], s[6:7] op_sel_hi:[1,0]
	v_pk_mul_f32 v[120:121], v[120:121], s[6:7] op_sel_hi:[1,0]
	global_store_dwordx4 v[4:5], v[120:123], off offset:512
	v_pk_mul_f32 v[114:115], v[114:115], s[6:7] op_sel_hi:[1,0]
	v_pk_mul_f32 v[112:113], v[112:113], s[6:7] op_sel_hi:[1,0]
	v_or_b32_e32 v120, 16, v6
	v_ashrrev_i32_e32 v121, 31, v120
	global_store_dwordx4 v[4:5], v[112:115], off offset:576
	v_pk_mul_f32 v[130:131], v[130:131], s[6:7] op_sel_hi:[1,0]
	v_pk_mul_f32 v[128:129], v[128:129], s[6:7] op_sel_hi:[1,0]
	v_pk_mul_f32 v[112:113], v[116:117], s[6:7] op_sel_hi:[1,0]
	v_lshlrev_b64 v[116:117], 13, v[120:121]
	v_pk_mul_f32 v[126:127], v[126:127], s[6:7] op_sel_hi:[1,0]
	v_pk_mul_f32 v[124:125], v[124:125], s[6:7] op_sel_hi:[1,0]
	v_lshl_add_u64 v[116:117], s[4:5], 0, v[116:117]
	global_store_dwordx4 v[4:5], v[128:131], off
	global_store_dwordx4 v[4:5], v[124:127], off offset:64
	v_lshl_add_u64 v[116:117], v[116:117], 0, v[134:135]
	v_pk_mul_f32 v[106:107], v[106:107], s[6:7] op_sel_hi:[1,0]
	v_pk_mul_f32 v[104:105], v[104:105], s[6:7] op_sel_hi:[1,0]
	global_store_dwordx4 v[116:117], v[104:107], off offset:512
	v_pk_mul_f32 v[98:99], v[98:99], s[6:7] op_sel_hi:[1,0]
; #define PG8_WAIT_V(n) asm volatile("s_waitcnt vmcnt(" #n ")" ::: "memory")
; #define PG8_BAR __builtin_amdgcn_s_barrier()
;     __device__ __forceinline__ void operator()(const f32x4 (&acc)[2][2][4][2], const Unit& u, int wr, int wc, int fr, int fq) const {
;     ...
;             for (int m = 0; m < 4; ++m) { const size_t off = (size_t)(row0 + ai * HALF + m * 16) * ldc + col0;
; #pragma unroll
;                 for (int bj = 0; bj < 2; ++bj)
; #pragma unroll
;                     for (int n = 0; n < 2; ++n) { f32x4 v = acc[ai][bj][m][n] * cs[bj][n];
;                         if (res) v += *(const f32x4*)(res + off + bj * HALF + n * 16);
;                         *(f32x4*)(out + off + bj * HALF + n * 16) = v; }
;                 asm volatile("" ::: "memory"); }
; template <class Epi, class Sched, bool FP8 = false>
; __device__ __forceinline__ void gemm_phase(LAS unsigned char* lds, const int Kb, const int nt  , const Sched& S, const Epi& E) {
;     ...
;         if (!has_next) break;
; #pragma unroll
;         for (int a = 0; a < 2; ++a)
; #pragma unroll
;             for (int b = 0; b < 2; ++b)
; #pragma unroll
;                 for (int m = 0; m < 4; ++m)
; #pragma unroll
;                     for (int n = 0; n < 2; ++n) acc[a][b][m][n] = (f32x4){0.f, 0.f, 0.f, 0.f};
;         cur = nxt; cA = nA; cB = nB; ++ui;
;     }
;     PG8_WAIT_V(0);
;     if (wr == 0) PG8_BAR;
;     PG8_BAR;
	v_pk_mul_f32 v[96:97], v[96:97], s[6:7] op_sel_hi:[1,0]
	v_or_b32_e32 v104, 32, v6
	v_ashrrev_i32_e32 v105, 31, v104
	v_or_b32_e32 v6, 48, v6
	global_store_dwordx4 v[116:117], v[96:99], off offset:576
	v_ashrrev_i32_e32 v7, 31, v6
	v_pk_mul_f32 v[114:115], v[118:119], s[6:7] op_sel_hi:[1,0]
	v_pk_mul_f32 v[96:97], v[100:101], s[6:7] op_sel_hi:[1,0]
	v_lshlrev_b64 v[100:101], 13, v[104:105]
	v_pk_mul_f32 v[110:111], v[110:111], s[6:7] op_sel_hi:[1,0]
	v_pk_mul_f32 v[108:109], v[108:109], s[6:7] op_sel_hi:[1,0]
	v_lshl_add_u64 v[100:101], s[4:5], 0, v[100:101]
	v_lshlrev_b64 v[6:7], 13, v[6:7]
	global_store_dwordx4 v[116:117], v[112:115], off
	global_store_dwordx4 v[116:117], v[108:111], off offset:64
	v_pk_mul_f32 v[98:99], v[102:103], s[6:7] op_sel_hi:[1,0]
	v_lshl_add_u64 v[100:101], v[100:101], 0, v[134:135]
	v_pk_mul_f32 v[94:95], v[94:95], s[6:7] op_sel_hi:[1,0]
	v_pk_mul_f32 v[92:93], v[92:93], s[6:7] op_sel_hi:[1,0]
	v_pk_mul_f32 v[90:91], v[90:91], s[6:7] op_sel_hi:[1,0]
	v_pk_mul_f32 v[88:89], v[88:89], s[6:7] op_sel_hi:[1,0]
	v_pk_mul_f32 v[82:83], v[82:83], s[6:7] op_sel_hi:[1,0]
	v_pk_mul_f32 v[80:81], v[80:81], s[6:7] op_sel_hi:[1,0]
	v_lshl_add_u64 v[6:7], s[4:5], 0, v[6:7]
	global_store_dwordx4 v[100:101], v[96:99], off
	global_store_dwordx4 v[100:101], v[92:95], off offset:64
	global_store_dwordx4 v[100:101], v[88:91], off offset:512
	global_store_dwordx4 v[100:101], v[80:83], off offset:576
	v_lshl_add_u64 v[6:7], v[6:7], 0, v[134:135]
	v_pk_mul_f32 v[70:71], v[70:71], s[6:7] op_sel_hi:[1,0]
	v_pk_mul_f32 v[68:69], v[68:69], s[6:7] op_sel_hi:[1,0]
	v_pk_mul_f32 v[82:83], v[86:87], s[6:7] op_sel_hi:[1,0]
	v_pk_mul_f32 v[80:81], v[84:85], s[6:7] op_sel_hi:[1,0]
	v_pk_mul_f32 v[78:79], v[78:79], s[6:7] op_sel_hi:[1,0]
	v_pk_mul_f32 v[76:77], v[76:77], s[6:7] op_sel_hi:[1,0]
	v_pk_mul_f32 v[74:75], v[74:75], s[6:7] op_sel_hi:[1,0]
	v_pk_mul_f32 v[72:73], v[72:73], s[6:7] op_sel_hi:[1,0]
	global_store_dwordx4 v[6:7], v[68:71], off offset:576
	global_store_dwordx4 v[6:7], v[80:83], off
	global_store_dwordx4 v[6:7], v[76:79], off offset:64
	v_add_co_u32_e32 v68, vcc, s63, v4
	global_store_dwordx4 v[6:7], v[72:75], off offset:512
	v_lshl_add_u64 v[6:7], v[4:5], 0, s[8:9]
	v_addc_co_u32_e32 v69, vcc, 0, v5, vcc
	v_pk_mul_f32 v[54:55], v[54:55], s[6:7] op_sel_hi:[1,0]
	v_pk_mul_f32 v[52:53], v[52:53], s[6:7] op_sel_hi:[1,0]
	v_pk_mul_f32 v[66:67], v[66:67], s[6:7] op_sel_hi:[1,0]
	v_pk_mul_f32 v[64:65], v[64:65], s[6:7] op_sel_hi:[1,0]
	v_pk_mul_f32 v[62:63], v[62:63], s[6:7] op_sel_hi:[1,0]
	v_pk_mul_f32 v[60:61], v[60:61], s[6:7] op_sel_hi:[1,0]
	global_store_dwordx4 v[6:7], v[52:55], off offset:512
	v_pk_mul_f32 v[46:47], v[46:47], s[6:7] op_sel_hi:[1,0]
	v_pk_mul_f32 v[44:45], v[44:45], s[6:7] op_sel_hi:[1,0]
	v_add_co_u32_e32 v52, vcc, s64, v4
	global_store_dwordx4 v[68:69], v[64:67], off
	global_store_dwordx4 v[6:7], v[60:63], off offset:64
	global_store_dwordx4 v[6:7], v[44:47], off offset:576
	v_lshl_add_u64 v[6:7], v[4:5], 0, s[10:11]
	v_addc_co_u32_e32 v53, vcc, 0, v5, vcc
	v_pk_mul_f32 v[46:47], v[58:59], s[6:7] op_sel_hi:[1,0]
	v_pk_mul_f32 v[44:45], v[56:57], s[6:7] op_sel_hi:[1,0]
	v_pk_mul_f32 v[38:39], v[38:39], s[6:7] op_sel_hi:[1,0]
	v_pk_mul_f32 v[36:37], v[36:37], s[6:7] op_sel_hi:[1,0]
	global_store_dwordx4 v[52:53], v[44:47], off
	global_store_dwordx4 v[6:7], v[36:39], off offset:512
	v_pk_mul_f32 v[30:31], v[30:31], s[6:7] op_sel_hi:[1,0]
	v_pk_mul_f32 v[46:47], v[50:51], s[6:7] op_sel_hi:[1,0]
	v_pk_mul_f32 v[44:45], v[48:49], s[6:7] op_sel_hi:[1,0]
	v_pk_mul_f32 v[28:29], v[28:29], s[6:7] op_sel_hi:[1,0]
	v_add_co_u32_e32 v36, vcc, s65, v4
	global_store_dwordx4 v[6:7], v[44:47], off offset:64
	global_store_dwordx4 v[6:7], v[28:31], off offset:576
	v_lshl_add_u64 v[6:7], v[4:5], 0, s[12:13]
	v_addc_co_u32_e32 v37, vcc, 0, v5, vcc
	v_pk_mul_f32 v[30:31], v[42:43], s[6:7] op_sel_hi:[1,0]
	v_pk_mul_f32 v[28:29], v[40:41], s[6:7] op_sel_hi:[1,0]
	v_pk_mul_f32 v[22:23], v[22:23], s[6:7] op_sel_hi:[1,0]
	v_pk_mul_f32 v[20:21], v[20:21], s[6:7] op_sel_hi:[1,0]
	global_store_dwordx4 v[36:37], v[28:31], off
	global_store_dwordx4 v[6:7], v[20:23], off offset:512
	v_pk_mul_f32 v[18:19], v[18:19], s[6:7] op_sel_hi:[1,0]
	v_pk_mul_f32 v[30:31], v[34:35], s[6:7] op_sel_hi:[1,0]
	v_pk_mul_f32 v[28:29], v[32:33], s[6:7] op_sel_hi:[1,0]
	v_pk_mul_f32 v[16:17], v[16:17], s[6:7] op_sel_hi:[1,0]
	v_lshl_add_u64 v[20:21], v[4:5], 0, s[14:15]
	v_add_co_u32_e32 v4, vcc, s66, v4
	global_store_dwordx4 v[6:7], v[28:31], off offset:64
	global_store_dwordx4 v[6:7], v[16:19], off offset:576
	v_addc_co_u32_e32 v5, vcc, 0, v5, vcc
	s_nop 0
	v_pk_mul_f32 v[18:19], v[26:27], s[6:7] op_sel_hi:[1,0]
	v_pk_mul_f32 v[16:17], v[24:25], s[6:7] op_sel_hi:[1,0]
	global_store_dwordx4 v[4:5], v[16:19], off
	v_pk_mul_f32 v[6:7], v[14:15], s[6:7] op_sel_hi:[1,0]
	v_pk_mul_f32 v[4:5], v[12:13], s[6:7] op_sel_hi:[1,0]
	global_store_dwordx4 v[20:21], v[4:7], off offset:64
	v_pk_mul_f32 v[2:3], v[2:3], s[6:7] op_sel_hi:[1,0]
	v_pk_mul_f32 v[0:1], v[0:1], s[6:7] op_sel_hi:[1,0]
	v_pk_mul_f32 v[6:7], v[10:11], s[6:7] op_sel_hi:[1,0]
	v_pk_mul_f32 v[4:5], v[8:9], s[6:7] op_sel_hi:[1,0]
	global_store_dwordx4 v[20:21], v[4:7], off offset:512
	global_store_dwordx4 v[20:21], v[0:3], off offset:576
	s_and_b64 vcc, exec, s[16:17]
	s_mov_b32 s69, s67
	s_mov_b32 s70, s68
	s_mov_b64 s[24:25], s[20:21]
	s_mov_b64 s[22:23], s[18:19]
	s_cbranch_vccz .LBB0_2862
	s_waitcnt vmcnt(0)
	s_cmpk_gt_u32 s7, 0xff
	s_cbranch_scc1 .LBB0_2869
	s_barrier
